# v053 + GEMM-phase LDS-DMA loads in saddr form where statically safe (63 sites): 64-bit vector address adds dropped
# speedup vs baseline: 1.0063x; 1.0063x over previous
; #define PG8_STAGE(bufoff, gbase, voff) do { _Pragma("unroll") for (int _i = 0; _i < 2; ++_i) \
;         __builtin_amdgcn_global_load_lds((const unsigned*)((const char*)(gbase) + (voff)[_i]), (LAS unsigned*)(lds + (bufoff) + ldsw + _i * 8192), 16, 0, 0); } while (0)
; #define PG8_WAIT_V(n) asm volatile("s_waitcnt vmcnt(" #n ")" ::: "memory")
; #define PG8_BAR __builtin_amdgcn_s_barrier()
; #define PG8_STAGE_A(bufoff, ptr_dense, half, ktoff, goffs) do { if constexpr (GATHER) { PG8_STAGE(bufoff, (const char*)A + (ktoff), goffs); } \
;         else { PG8_STAGE(bufoff, (ptr_dense) + (half) * hstepA, voffA); } } while (0)
; template <class Epi, class Sched, bool GATHER>
; __device__ __forceinline__ void gemm_phase(LAS unsigned char* lds, const int wid, const bf16_t* A, int lda, const bf16_t* Bt, int ldb, size_t b_estride, int K, const Sched& S, const Epi& E) {
;     ...
;     PG8_STAGE(PG8_SB(0, 0), cB, voffB); PG8_STAGE(PG8_SB(0, 1), cB + hstepB, voffB); PG8_STAGE_A(PG8_SA(0, 0), cA, 0, 0, gc0); PG8_STAGE_A(PG8_SA(0, 1), cA, 1, 0, gc1);
;     if (wr == 1) PG8_BAR;
;     PG8_WAIT_V(2); PG8_BAR;
;     PG8_STAGE(PG8_SB(1, 0), cB + kstep, voffB); PG8_STAGE_A(PG8_SA(1, 0), cA + kstep, 0, kstep, gc0); PG8_STAGE(PG8_SB(1, 1), cB + hstepB + kstep, voffB); PG8_STAGE_A(PG8_SA(1, 1), cA + kstep, 1, kstep, gc1);
;     PG8_WAIT_V(8); PG8_BAR;
.LBB0_262:
	v_readlane_b32 s8, v248, 9
	s_bfe_u32 s11, s8, 0x20006
	s_add_u32 s22, s12, 0x2c000000
	s_addc_u32 s23, s13, 0
	s_add_u32 s24, s12, 0x1a000000
	s_addc_u32 s25, s13, 0
	s_add_u32 s26, s12, 0x400000
	s_addc_u32 s27, s13, 0
	s_lshl_b32 s78, s11, 4
	s_lshl_b32 s77, s11, 5
	s_and_b32 s79, s78, 16
	s_cmp_lt_u32 s11, 2
	v_readlane_b32 s9, v248, 10
	s_cselect_b64 s[28:29], -1, 0
	s_and_b64 s[8:9], s[28:29], exec
	s_mov_b64 s[30:31], 0x80
	s_cselect_b32 s80, 32, 0
	v_lshl_add_u64 v[6:7], v[6:7], 0, s[30:31]
	s_add_i32 m0, s15, 0x18000
	s_waitcnt vmcnt(2)
	s_barrier
	global_load_lds_dwordx4 v[6:7], off
	v_lshl_add_u64 v[4:5], v[4:5], 0, s[30:31]
	s_add_i32 m0, s15, 0x1a000
	s_add_i32 s81, s15, 0x8000
	s_add_i32 s82, s15, 0xa000
	global_load_lds_dwordx4 v[4:5], off
	v_lshl_add_u64 v[2:3], v[2:3], 0, s[30:31]
	s_mov_b32 m0, s81
	s_add_u32 s8, s60, 0x40080
	global_load_lds_dwordx4 v[2:3], off
	v_lshl_add_u64 v[0:1], v[0:1], 0, s[30:31]
	s_mov_b32 m0, s82
	s_addc_u32 s9, s61, 0
	global_load_lds_dwordx4 v[0:1], off
	s_add_i32 m0, s15, 0x1c000
	v_and_b32_e32 v3, 48, v8
	global_load_lds_dwordx4 v154, s[8:9]
	s_add_i32 m0, s15, 0x1e000
	v_lshl_add_u64 v[0:1], s[8:9], 0, v[158:159]
	s_add_u32 s8, s70, 0x40080
	s_addc_u32 s9, s71, 0
	s_add_i32 s83, s15, 0xc000
	global_load_lds_dwordx4 v[0:1], off
	s_mov_b32 m0, s83
	s_add_i32 s84, s15, 0xe000
	global_load_lds_dwordx4 v152, s[8:9]
	v_lshl_add_u64 v[0:1], s[8:9], 0, v[156:157]
	s_mov_b32 m0, s84
	s_movk_i32 s8, 0x3c0
	global_load_lds_dwordx4 v[0:1], off
	v_and_b32_e32 v0, 15, v8
	v_or_b32_e32 v1, s1, v0
	v_lshlrev_b32_e32 v2, 6, v1
	v_and_or_b32 v2, v2, s8, v3
	v_and_b32_e32 v4, 0xfffffc00, v9
	v_readlane_b32 s8, v248, 14
	v_lshlrev_b32_e32 v1, 2, v1
	v_and_b32_e32 v1, 32, v1
	v_add_u32_e32 v5, s8, v4
	v_lshl_or_b32 v0, v0, 6, v3
	v_lshlrev_b32_e32 v3, 2, v8
	s_lshl_b32 s8, s11, 2
	v_bitop3_b32 v1, v2, v5, v1 bitop3:0xde
	v_lshl_add_u32 v2, s11, 12, v4
	v_and_b32_e32 v3, 32, v3
	s_waitcnt vmcnt(8)
	s_add_u32 s85, s12, s8
	v_bitop3_b32 v174, v0, v2, v3 bitop3:0xde
	s_addc_u32 s86, s13, 0
	s_add_i32 s87, 0, 0x10000
	s_add_i32 s88, 0, 0x14000
	v_mov_b64_e32 v[162:163], 0x900
	v_mov_b64_e32 v[164:165], 0x8ff
	v_add_u32_e32 v175, s87, v174
	v_add_u32_e32 v176, s88, v174
	v_add_u32_e32 v177, 0, v1
	s_movk_i32 s89, 0x1000
	s_movk_i32 s90, 0x600
	s_mov_b64 s[34:35], 0x20000
	s_mov_b64 s[36:37], 0x24000
	s_mov_b64 s[38:39], 0x28000
	s_mov_b64 s[42:43], 0x2c000
	v_mov_b32_e32 v178, 0x1000
	v_mov_b32_e32 v179, 0x3e38aa3b
	v_mbcnt_hi_u32_b32 v180, -1, v199
	s_mov_b32 s68, 0
	s_mov_b32 s66, 0
	s_barrier
	s_branch .LBB0_265

; #define PG8_STAGE(bufoff, gbase, voff) do { _Pragma("unroll") for (int _i = 0; _i < 2; ++_i) \
;         __builtin_amdgcn_global_load_lds((const unsigned*)((const char*)(gbase) + (voff)[_i]), (LAS unsigned*)(lds + (bufoff) + ldsw + _i * 8192), 16, 0, 0); } while (0)
; #define PG8_LDA(dst, b, h) do { _Pragma("unroll") for (int m = 0; m < 4; ++m) _Pragma("unroll") for (int k = 0; k < 2; ++k) dst[m][k] = *(const LAS bf16x8*)(lds + PG8_SA(b, h) + aoff + m * 2048 + k * 1024); } while (0)
; #define PG8_LDB(dst, b, h) do { _Pragma("unroll") for (int n = 0; n < 2; ++n) _Pragma("unroll") for (int k = 0; k < 2; ++k) dst[n][k] = *(const LAS bf16x8*)(lds + PG8_SB(b, h) + boff + n * 2048 + k * 1024); } while (0)
; #define PG8_MMA(ai, bj, At, Bt_) do { __builtin_amdgcn_s_setprio(1); _Pragma("unroll") for (int m = 0; m < 4; ++m) _Pragma("unroll") for (int n = 0; n < 2; ++n) _Pragma("unroll") for (int k = 0; k < 2; ++k) \
;         acc[ai][bj][m][n] = __builtin_amdgcn_mfma_f32_16x16x32_bf16(Bt_[n][k], At[m][k], acc[ai][bj][m][n], 0, 0, 0); __builtin_amdgcn_s_setprio(0); } while (0)
; #define PG8_BAR __builtin_amdgcn_s_barrier()
; template <class Epi, class Sched, bool GATHER>
; __device__ __forceinline__ void gemm_phase(LAS unsigned char* lds, const int wid, const bf16_t* A, int lda, const bf16_t* Bt, int ldb, size_t b_estride, int K, const Sched& S, const Epi& E) {
;     ...
;             PG8_LDB(B0, 0, 0); PG8_LDB(B1, 0, 1); PG8_SCHED; PG8_LDA(At, 0, 0);
;             PG8_WAIT_VR(rl); PG8_WAIT_L(0); PG8_BAR; PG8_MMA(0, 0, At, B0); PG8_MMA(0, 1, At, B1); PG8_BAR; PG8_SCHED;
;             PG8_LDA(At, 0, 1); PG8_STAGE(PG8_SB(0, 0), b2, voffB); PG8_STAGE(PG8_SB(0, 1), b2 + hstepB, voffB); PG8_STAGE_A(PG8_SA(0, 0), a2, 0, k2, g20);
;             PG8_WAIT_VR(rl); PG8_WAIT_L(0); PG8_BAR; PG8_MMA(1, 0, At, B0); PG8_MMA(1, 1, At, B1); PG8_BAR; PG8_SCHED;
;             PG8_LDB(B0, 1, 0); PG8_LDB(B1, 1, 1); PG8_SCHED; PG8_LDA(At, 1, 0); PG8_STAGE_A(PG8_SA(0, 1), a2, 1, k2, g21);
;             PG8_WAIT_VR(rl); PG8_WAIT_L(0); PG8_BAR; PG8_MMA(0, 0, At, B0); PG8_MMA(0, 1, At, B1); PG8_BAR; PG8_SCHED;
;             PG8_LDA(At, 1, 1); PG8_STAGE(PG8_SB(1, 0), b3, voffB); PG8_STAGE(PG8_SB(1, 1), b3 + hstepB, voffB); PG8_STAGE_A(PG8_SA(1, 0), a3, 0, k3, g20);
;             PG8_WAIT_V(8); PG8_WAIT_L(0); PG8_BAR; PG8_MMA(1, 0, At, B0); PG8_MMA(1, 1, At, B1); PG8_BAR; PG8_SCHED;
.Lwvr0:
	s_waitcnt vmcnt(24)
	s_waitcnt lgkmcnt(0)
	s_barrier
	s_setprio 1
	s_waitcnt lgkmcnt(0)
	v_mfma_f32_16x16x32_bf16 v[124:127], v[128:131], v[182:185], v[124:127]
	v_mfma_f32_16x16x32_bf16 v[120:123], v[136:139], v[182:185], v[120:123]
	v_mfma_f32_16x16x32_bf16 v[108:111], v[128:131], v[190:193], v[108:111]
	v_mfma_f32_16x16x32_bf16 v[104:107], v[136:139], v[190:193], v[104:107]
	v_mfma_f32_16x16x32_bf16 v[92:95], v[128:131], v[200:203], v[92:95]
	v_mfma_f32_16x16x32_bf16 v[88:91], v[136:139], v[200:203], v[88:91]
	v_mfma_f32_16x16x32_bf16 v[76:79], v[128:131], v[208:211], v[76:79]
	v_mfma_f32_16x16x32_bf16 v[72:75], v[136:139], v[208:211], v[72:75]
	v_mfma_f32_16x16x32_bf16 v[124:127], v[132:135], v[186:189], v[124:127]
	v_mfma_f32_16x16x32_bf16 v[120:123], v[140:143], v[186:189], v[120:123]
	v_mfma_f32_16x16x32_bf16 v[108:111], v[132:135], v[194:197], v[108:111]
	v_mfma_f32_16x16x32_bf16 v[104:107], v[140:143], v[194:197], v[104:107]
	v_mfma_f32_16x16x32_bf16 v[92:95], v[132:135], v[204:207], v[92:95]
	v_mfma_f32_16x16x32_bf16 v[88:91], v[140:143], v[204:207], v[88:91]
	v_mfma_f32_16x16x32_bf16 v[76:79], v[132:135], v[212:215], v[76:79]
	v_mfma_f32_16x16x32_bf16 v[72:75], v[140:143], v[212:215], v[72:75]
	s_setprio 0
	s_setprio 1
	v_mfma_f32_16x16x32_bf16 v[116:119], v[144:147], v[182:185], v[116:119]
	v_mfma_f32_16x16x32_bf16 v[112:115], v[166:169], v[182:185], v[112:115]
	v_mfma_f32_16x16x32_bf16 v[100:103], v[144:147], v[190:193], v[100:103]
	v_mfma_f32_16x16x32_bf16 v[96:99], v[166:169], v[190:193], v[96:99]
	v_mfma_f32_16x16x32_bf16 v[84:87], v[144:147], v[200:203], v[84:87]
	v_mfma_f32_16x16x32_bf16 v[80:83], v[166:169], v[200:203], v[80:83]
	v_mfma_f32_16x16x32_bf16 v[68:71], v[144:147], v[208:211], v[68:71]
	v_mfma_f32_16x16x32_bf16 v[64:67], v[166:169], v[208:211], v[64:67]
	v_mfma_f32_16x16x32_bf16 v[116:119], v[148:151], v[186:189], v[116:119]
	v_mfma_f32_16x16x32_bf16 v[112:115], v[170:173], v[186:189], v[112:115]
	v_mfma_f32_16x16x32_bf16 v[100:103], v[148:151], v[194:197], v[100:103]
	v_mfma_f32_16x16x32_bf16 v[96:99], v[170:173], v[194:197], v[96:99]
	v_mfma_f32_16x16x32_bf16 v[84:87], v[148:151], v[204:207], v[84:87]
	v_mfma_f32_16x16x32_bf16 v[80:83], v[170:173], v[204:207], v[80:83]
	v_mfma_f32_16x16x32_bf16 v[68:71], v[148:151], v[212:215], v[68:71]
	v_mfma_f32_16x16x32_bf16 v[64:67], v[170:173], v[212:215], v[64:67]
	s_setprio 0
	s_barrier
	s_add_i32 s96, s87, s33
	v_lshl_add_u64 v[216:217], s[70:71], 0, v[154:155]
	s_mov_b32 m0, s96
	ds_read_b128 v[182:185], v177 offset:16384
	ds_read_b128 v[186:189], v177 offset:17408
	ds_read_b128 v[190:193], v177 offset:18432
	ds_read_b128 v[194:197], v177 offset:19456
	ds_read_b128 v[200:203], v177 offset:20480
	ds_read_b128 v[204:207], v177 offset:21504
	ds_read_b128 v[208:211], v177 offset:22528
	ds_read_b128 v[212:215], v177 offset:23552
	global_load_lds_dwordx4 v[216:217], off
	s_add_i32 m0, s96, 0x2000
	s_add_u32 s96, s70, 0x40000
	v_lshl_add_u64 v[218:219], s[70:71], 0, v[158:159]
	s_addc_u32 s97, s71, 0
	s_add_i32 vcc_lo, s88, s33
	global_load_lds_dwordx4 v[218:219], off
	s_mov_b32 m0, vcc_lo
	v_lshl_add_u64 v[222:223], s[60:61], 0, v[156:157]
	global_load_lds_dwordx4 v154, s[96:97]
	s_add_i32 m0, vcc_lo, 0x2000
	s_nop 0
	global_load_lds_dwordx4 v158, s[96:97]
	v_lshl_add_u64 v[220:221], s[60:61], 0, v[152:153]
	s_mov_b32 m0, s15
	s_nop 0
	global_load_lds_dwordx4 v[220:221], off
	s_mov_b32 m0, s74
	s_nop 0
	global_load_lds_dwordx4 v[222:223], off
	s_cmp_lg_u32 s95, 0
	s_cbranch_scc1 .Lwvr1
	s_waitcnt vmcnt(8)
.Lwvr1:
	s_waitcnt vmcnt(24)
	s_waitcnt lgkmcnt(0)
	s_barrier
	s_setprio 1
	s_waitcnt lgkmcnt(0)
	v_mfma_f32_16x16x32_bf16 v[60:63], v[128:131], v[182:185], v[60:63]
	v_mfma_f32_16x16x32_bf16 v[56:59], v[136:139], v[182:185], v[56:59]
	v_mfma_f32_16x16x32_bf16 v[44:47], v[128:131], v[190:193], v[44:47]
	v_mfma_f32_16x16x32_bf16 v[40:43], v[136:139], v[190:193], v[40:43]
	v_mfma_f32_16x16x32_bf16 v[28:31], v[128:131], v[200:203], v[28:31]
	v_mfma_f32_16x16x32_bf16 v[24:27], v[136:139], v[200:203], v[24:27]
	v_mfma_f32_16x16x32_bf16 v[12:15], v[128:131], v[208:211], v[12:15]
	v_mfma_f32_16x16x32_bf16 v[8:11], v[136:139], v[208:211], v[8:11]
	v_mfma_f32_16x16x32_bf16 v[60:63], v[132:135], v[186:189], v[60:63]
	v_mfma_f32_16x16x32_bf16 v[56:59], v[140:143], v[186:189], v[56:59]
	v_mfma_f32_16x16x32_bf16 v[44:47], v[132:135], v[194:197], v[44:47]
	v_mfma_f32_16x16x32_bf16 v[40:43], v[140:143], v[194:197], v[40:43]
	v_mfma_f32_16x16x32_bf16 v[28:31], v[132:135], v[204:207], v[28:31]
	v_mfma_f32_16x16x32_bf16 v[24:27], v[140:143], v[204:207], v[24:27]
	v_mfma_f32_16x16x32_bf16 v[12:15], v[132:135], v[212:215], v[12:15]
	v_mfma_f32_16x16x32_bf16 v[8:11], v[140:143], v[212:215], v[8:11]
	s_setprio 0
	s_setprio 1
	v_mfma_f32_16x16x32_bf16 v[52:55], v[144:147], v[182:185], v[52:55]
	v_mfma_f32_16x16x32_bf16 v[48:51], v[166:169], v[182:185], v[48:51]
	v_mfma_f32_16x16x32_bf16 v[36:39], v[144:147], v[190:193], v[36:39]
	v_mfma_f32_16x16x32_bf16 v[32:35], v[166:169], v[190:193], v[32:35]
	v_mfma_f32_16x16x32_bf16 v[20:23], v[144:147], v[200:203], v[20:23]
	v_mfma_f32_16x16x32_bf16 v[16:19], v[166:169], v[200:203], v[16:19]
	v_mfma_f32_16x16x32_bf16 v[4:7], v[144:147], v[208:211], v[4:7]
	v_mfma_f32_16x16x32_bf16 v[0:3], v[166:169], v[208:211], v[0:3]
	v_mfma_f32_16x16x32_bf16 v[52:55], v[148:151], v[186:189], v[52:55]
	v_mfma_f32_16x16x32_bf16 v[48:51], v[170:173], v[186:189], v[48:51]
	v_mfma_f32_16x16x32_bf16 v[36:39], v[148:151], v[194:197], v[36:39]
	v_mfma_f32_16x16x32_bf16 v[32:35], v[170:173], v[194:197], v[32:35]
	v_mfma_f32_16x16x32_bf16 v[20:23], v[148:151], v[204:207], v[20:23]
	v_mfma_f32_16x16x32_bf16 v[16:19], v[170:173], v[204:207], v[16:19]
	v_mfma_f32_16x16x32_bf16 v[4:7], v[148:151], v[212:215], v[4:7]
	v_mfma_f32_16x16x32_bf16 v[0:3], v[170:173], v[212:215], v[0:3]
	s_setprio 0
	s_barrier
	s_add_i32 vcc_lo, 0, 0x18000
	s_add_i32 vcc_hi, 0, 0x1c000
	v_add_u32_e32 v140, vcc_lo, v174
	v_add_u32_e32 v160, vcc_hi, v174
	ds_read_b128 v[128:131], v140
	ds_read_b128 v[132:135], v140 offset:1024
	ds_read_b128 v[136:139], v140 offset:2048
	ds_read_b128 v[140:143], v140 offset:3072
	ds_read_b128 v[144:147], v160
	ds_read_b128 v[148:151], v160 offset:1024
	ds_read_b128 v[166:169], v160 offset:2048
	ds_read_b128 v[170:173], v160 offset:3072
	s_add_u32 s96, s60, 0x40000
	s_addc_u32 s97, s61, 0
	s_mov_b32 m0, s75
	ds_read_b128 v[182:185], v177 offset:32768
	ds_read_b128 v[186:189], v177 offset:33792
	ds_read_b128 v[190:193], v177 offset:34816
	ds_read_b128 v[194:197], v177 offset:35840
	ds_read_b128 v[200:203], v177 offset:36864
	ds_read_b128 v[204:207], v177 offset:37888
	ds_read_b128 v[208:211], v177 offset:38912
	ds_read_b128 v[212:215], v177 offset:39936
	global_load_lds_dwordx4 v152, s[96:97]
	v_lshl_add_u64 v[224:225], s[96:97], 0, v[156:157]
	s_mov_b32 m0, s76
	s_nop 0
	global_load_lds_dwordx4 v[224:225], off
	s_cmp_lg_u32 s95, 0
	s_cbranch_scc1 .Lwvr2
	s_waitcnt vmcnt(8)
; #define PG8_STAGE(bufoff, gbase, voff) do { _Pragma("unroll") for (int _i = 0; _i < 2; ++_i) \
;         __builtin_amdgcn_global_load_lds((const unsigned*)((const char*)(gbase) + (voff)[_i]), (LAS unsigned*)(lds + (bufoff) + ldsw + _i * 8192), 16, 0, 0); } while (0)
; #define PG8_LDA(dst, b, h) do { _Pragma("unroll") for (int m = 0; m < 4; ++m) _Pragma("unroll") for (int k = 0; k < 2; ++k) dst[m][k] = *(const LAS bf16x8*)(lds + PG8_SA(b, h) + aoff + m * 2048 + k * 1024); } while (0)
; #define PG8_LDB(dst, b, h) do { _Pragma("unroll") for (int n = 0; n < 2; ++n) _Pragma("unroll") for (int k = 0; k < 2; ++k) dst[n][k] = *(const LAS bf16x8*)(lds + PG8_SB(b, h) + boff + n * 2048 + k * 1024); } while (0)
; #define PG8_MMA(ai, bj, At, Bt_) do { __builtin_amdgcn_s_setprio(1); _Pragma("unroll") for (int m = 0; m < 4; ++m) _Pragma("unroll") for (int n = 0; n < 2; ++n) _Pragma("unroll") for (int k = 0; k < 2; ++k) \
;         acc[ai][bj][m][n] = __builtin_amdgcn_mfma_f32_16x16x32_bf16(Bt_[n][k], At[m][k], acc[ai][bj][m][n], 0, 0, 0); __builtin_amdgcn_s_setprio(0); } while (0)
; #define PG8_WAIT_V(n) asm volatile("s_waitcnt vmcnt(" #n ")" ::: "memory")
; #define PG8_WAIT_L(n) asm volatile("s_waitcnt lgkmcnt(" #n ")" ::: "memory")
; #define PG8_WAIT_VR(rl) asm volatile("s_cmp_lg_u32 %0, 0\n\ts_cbranch_scc1 .Lwvr%=\n\ts_waitcnt vmcnt(8)\n.Lwvr%=:\n\ts_waitcnt vmcnt(24)" :: "s"(rl) : "scc", "memory")
; template <class Epi, class Sched, bool GATHER>
; __device__ __forceinline__ void gemm_phase(LAS unsigned char* lds, const int wid, const bf16_t* A, int lda, const bf16_t* Bt, int ldb, size_t b_estride, int K, const Sched& S, const Epi& E) {
;     ...
;             PG8_WAIT_VR(rl); PG8_WAIT_L(0); PG8_BAR; PG8_MMA(1, 0, At, B0); PG8_MMA(1, 1, At, B1); PG8_BAR; PG8_SCHED;
;             PG8_LDB(B0, 1, 0); PG8_LDB(B1, 1, 1); PG8_SCHED; PG8_LDA(At, 1, 0); PG8_STAGE_A(PG8_SA(0, 1), a2, 1, k2, g21);
;             PG8_WAIT_VR(rl); PG8_WAIT_L(0); PG8_BAR; PG8_MMA(0, 0, At, B0); PG8_MMA(0, 1, At, B1); PG8_BAR; PG8_SCHED;
;             PG8_LDA(At, 1, 1); PG8_STAGE(PG8_SB(1, 0), b3, voffB); PG8_STAGE(PG8_SB(1, 1), b3 + hstepB, voffB); PG8_STAGE_A(PG8_SA(1, 0), a3, 0, k3, g20);
;             PG8_WAIT_V(8); PG8_WAIT_L(0); PG8_BAR; PG8_MMA(1, 0, At, B0); PG8_MMA(1, 1, At, B1); PG8_BAR; PG8_SCHED;
;             PG8_STAGE_A(PG8_SA(1, 1), a3, 1, k3, g21);
;         }
.Lwvr2:
	s_waitcnt vmcnt(24)
	s_waitcnt lgkmcnt(0)
	s_barrier
	s_setprio 1
	s_waitcnt lgkmcnt(0)
	v_mfma_f32_16x16x32_bf16 v[124:127], v[128:131], v[182:185], v[124:127]
	v_mfma_f32_16x16x32_bf16 v[120:123], v[136:139], v[182:185], v[120:123]
	v_mfma_f32_16x16x32_bf16 v[108:111], v[128:131], v[190:193], v[108:111]
	v_mfma_f32_16x16x32_bf16 v[104:107], v[136:139], v[190:193], v[104:107]
	v_mfma_f32_16x16x32_bf16 v[92:95], v[128:131], v[200:203], v[92:95]
	v_mfma_f32_16x16x32_bf16 v[88:91], v[136:139], v[200:203], v[88:91]
	v_mfma_f32_16x16x32_bf16 v[76:79], v[128:131], v[208:211], v[76:79]
	v_mfma_f32_16x16x32_bf16 v[72:75], v[136:139], v[208:211], v[72:75]
	v_mfma_f32_16x16x32_bf16 v[124:127], v[132:135], v[186:189], v[124:127]
	v_mfma_f32_16x16x32_bf16 v[120:123], v[140:143], v[186:189], v[120:123]
	v_mfma_f32_16x16x32_bf16 v[108:111], v[132:135], v[194:197], v[108:111]
	v_mfma_f32_16x16x32_bf16 v[104:107], v[140:143], v[194:197], v[104:107]
	v_mfma_f32_16x16x32_bf16 v[92:95], v[132:135], v[204:207], v[92:95]
	v_mfma_f32_16x16x32_bf16 v[88:91], v[140:143], v[204:207], v[88:91]
	v_mfma_f32_16x16x32_bf16 v[76:79], v[132:135], v[212:215], v[76:79]
	v_mfma_f32_16x16x32_bf16 v[72:75], v[140:143], v[212:215], v[72:75]
	s_setprio 0
	s_setprio 1
	v_mfma_f32_16x16x32_bf16 v[116:119], v[144:147], v[182:185], v[116:119]
	v_mfma_f32_16x16x32_bf16 v[112:115], v[166:169], v[182:185], v[112:115]
	v_mfma_f32_16x16x32_bf16 v[100:103], v[144:147], v[190:193], v[100:103]
	v_mfma_f32_16x16x32_bf16 v[96:99], v[166:169], v[190:193], v[96:99]
	v_mfma_f32_16x16x32_bf16 v[84:87], v[144:147], v[200:203], v[84:87]
	v_mfma_f32_16x16x32_bf16 v[80:83], v[166:169], v[200:203], v[80:83]
	v_mfma_f32_16x16x32_bf16 v[68:71], v[144:147], v[208:211], v[68:71]
	v_mfma_f32_16x16x32_bf16 v[64:67], v[166:169], v[208:211], v[64:67]
	v_mfma_f32_16x16x32_bf16 v[116:119], v[148:151], v[186:189], v[116:119]
	v_mfma_f32_16x16x32_bf16 v[112:115], v[170:173], v[186:189], v[112:115]
	v_mfma_f32_16x16x32_bf16 v[100:103], v[148:151], v[194:197], v[100:103]
	v_mfma_f32_16x16x32_bf16 v[96:99], v[170:173], v[194:197], v[96:99]
	v_mfma_f32_16x16x32_bf16 v[84:87], v[148:151], v[204:207], v[84:87]
	v_mfma_f32_16x16x32_bf16 v[80:83], v[170:173], v[204:207], v[80:83]
	v_mfma_f32_16x16x32_bf16 v[68:71], v[148:151], v[212:215], v[68:71]
	v_mfma_f32_16x16x32_bf16 v[64:67], v[170:173], v[212:215], v[64:67]
	s_setprio 0
	s_barrier
	s_add_i32 s95, vcc_lo, s33
	v_lshl_add_u64 v[216:217], v[216:217], 0, s[30:31]
	s_mov_b32 m0, s95
	ds_read_b128 v[182:185], v177 offset:49152
	ds_read_b128 v[186:189], v177 offset:50176
	ds_read_b128 v[190:193], v177 offset:51200
	ds_read_b128 v[194:197], v177 offset:52224
	ds_read_b128 v[200:203], v177 offset:53248
	ds_read_b128 v[204:207], v177 offset:54272
	ds_read_b128 v[208:211], v177 offset:55296
	ds_read_b128 v[212:215], v177 offset:56320
	global_load_lds_dwordx4 v[216:217], off
	s_add_i32 m0, s95, 0x2000
	s_add_u32 s70, s70, 0x40080
	v_lshl_add_u64 v[216:217], v[218:219], 0, s[30:31]
	s_addc_u32 s71, s71, 0
	s_add_i32 s95, vcc_hi, s33
	global_load_lds_dwordx4 v[216:217], off
	s_mov_b32 m0, s95
	s_nop 0
	global_load_lds_dwordx4 v154, s[70:71]
	s_add_i32 m0, s95, 0x2000
	s_nop 0
	global_load_lds_dwordx4 v158, s[70:71]
	v_lshl_add_u64 v[216:217], v[220:221], 0, s[30:31]
	s_mov_b32 m0, s81
	s_nop 0
	global_load_lds_dwordx4 v[216:217], off
	v_lshl_add_u64 v[216:217], v[222:223], 0, s[30:31]
	s_mov_b32 m0, s82
	s_nop 0
	global_load_lds_dwordx4 v[216:217], off
	s_waitcnt vmcnt(8)
	s_waitcnt lgkmcnt(0)
	s_barrier
	s_setprio 1
	s_waitcnt lgkmcnt(0)
	v_mfma_f32_16x16x32_bf16 v[60:63], v[128:131], v[182:185], v[60:63]
	v_mfma_f32_16x16x32_bf16 v[56:59], v[136:139], v[182:185], v[56:59]
	v_mfma_f32_16x16x32_bf16 v[44:47], v[128:131], v[190:193], v[44:47]
	v_mfma_f32_16x16x32_bf16 v[40:43], v[136:139], v[190:193], v[40:43]
	v_mfma_f32_16x16x32_bf16 v[28:31], v[128:131], v[200:203], v[28:31]
	v_mfma_f32_16x16x32_bf16 v[24:27], v[136:139], v[200:203], v[24:27]
	v_mfma_f32_16x16x32_bf16 v[12:15], v[128:131], v[208:211], v[12:15]
	v_mfma_f32_16x16x32_bf16 v[8:11], v[136:139], v[208:211], v[8:11]
	v_mfma_f32_16x16x32_bf16 v[60:63], v[132:135], v[186:189], v[60:63]
	v_mfma_f32_16x16x32_bf16 v[56:59], v[140:143], v[186:189], v[56:59]
	v_mfma_f32_16x16x32_bf16 v[44:47], v[132:135], v[194:197], v[44:47]
	v_mfma_f32_16x16x32_bf16 v[40:43], v[140:143], v[194:197], v[40:43]
	v_mfma_f32_16x16x32_bf16 v[28:31], v[132:135], v[204:207], v[28:31]
	v_mfma_f32_16x16x32_bf16 v[24:27], v[140:143], v[204:207], v[24:27]
	v_mfma_f32_16x16x32_bf16 v[12:15], v[132:135], v[212:215], v[12:15]
	v_mfma_f32_16x16x32_bf16 v[8:11], v[140:143], v[212:215], v[8:11]
	s_setprio 0
	s_setprio 1
	v_mfma_f32_16x16x32_bf16 v[52:55], v[144:147], v[182:185], v[52:55]
	v_mfma_f32_16x16x32_bf16 v[48:51], v[166:169], v[182:185], v[48:51]
	v_mfma_f32_16x16x32_bf16 v[36:39], v[144:147], v[190:193], v[36:39]
	v_mfma_f32_16x16x32_bf16 v[32:35], v[166:169], v[190:193], v[32:35]
	v_mfma_f32_16x16x32_bf16 v[20:23], v[144:147], v[200:203], v[20:23]
	v_mfma_f32_16x16x32_bf16 v[16:19], v[166:169], v[200:203], v[16:19]
	v_mfma_f32_16x16x32_bf16 v[4:7], v[144:147], v[208:211], v[4:7]
	v_mfma_f32_16x16x32_bf16 v[0:3], v[166:169], v[208:211], v[0:3]
	v_mfma_f32_16x16x32_bf16 v[52:55], v[148:151], v[186:189], v[52:55]
	v_mfma_f32_16x16x32_bf16 v[48:51], v[170:173], v[186:189], v[48:51]
	v_mfma_f32_16x16x32_bf16 v[36:39], v[148:151], v[194:197], v[36:39]
	v_mfma_f32_16x16x32_bf16 v[32:35], v[170:173], v[194:197], v[32:35]
	v_mfma_f32_16x16x32_bf16 v[20:23], v[148:151], v[204:207], v[20:23]
	v_mfma_f32_16x16x32_bf16 v[16:19], v[170:173], v[204:207], v[16:19]
	v_mfma_f32_16x16x32_bf16 v[4:7], v[148:151], v[212:215], v[4:7]
	v_mfma_f32_16x16x32_bf16 v[0:3], v[170:173], v[212:215], v[0:3]
	s_setprio 0
	s_barrier
	s_add_u32 s60, s60, 0x40080
	s_addc_u32 s61, s61, 0
	s_mov_b32 m0, s83
	s_nop 0
	global_load_lds_dwordx4 v152, s[60:61]
	s_mov_b32 m0, s84
	s_add_i32 s94, s94, 2
	global_load_lds_dwordx4 v156, s[60:61]
	s_add_u32 s52, s52, 0x100
	s_addc_u32 s53, s53, 0
	s_add_u32 s92, s92, 0x100
	s_addc_u32 s93, s93, 0
	s_cmp_gt_u32 s94, 13
	s_cbranch_scc0 .LBB0_268
	s_and_b64 vcc, exec, s[40:41]
	s_cbranch_vccz .LBB0_271
	s_barrier

; #define PG8_STAGE(bufoff, gbase, voff) do { _Pragma("unroll") for (int _i = 0; _i < 2; ++_i) \
;         __builtin_amdgcn_global_load_lds((const unsigned*)((const char*)(gbase) + (voff)[_i]), (LAS unsigned*)(lds + (bufoff) + ldsw + _i * 8192), 16, 0, 0); } while (0)
; #define PG8_WAIT_V(n) asm volatile("s_waitcnt vmcnt(" #n ")" ::: "memory")
; #define PG8_BAR __builtin_amdgcn_s_barrier()
; #define PG8_STAGE_A(bufoff, ptr_dense, half, ktoff, goffs) do { if constexpr (GATHER) { PG8_STAGE(bufoff, (const char*)A + (ktoff), goffs); } \
;         else { PG8_STAGE(bufoff, (ptr_dense) + (half) * hstepA, voffA); } } while (0)
; template <class Epi, class Sched, bool GATHER>
; __device__ __forceinline__ void gemm_phase(LAS unsigned char* lds, const int wid, const bf16_t* A, int lda, const bf16_t* Bt, int ldb, size_t b_estride, int K, const Sched& S, const Epi& E) {
;     ...
;     PG8_STAGE(PG8_SB(0, 0), cB, voffB); PG8_STAGE(PG8_SB(0, 1), cB + hstepB, voffB); PG8_STAGE_A(PG8_SA(0, 0), cA, 0, 0, gc0); PG8_STAGE_A(PG8_SA(0, 1), cA, 1, 0, gc1);
;     if (wr == 1) PG8_BAR;
;     PG8_WAIT_V(2); PG8_BAR;
;     PG8_STAGE(PG8_SB(1, 0), cB + kstep, voffB); PG8_STAGE_A(PG8_SA(1, 0), cA + kstep, 0, kstep, gc0); PG8_STAGE(PG8_SB(1, 1), cB + hstepB + kstep, voffB); PG8_STAGE_A(PG8_SA(1, 1), cA + kstep, 1, kstep, gc1);
;     PG8_WAIT_V(8); PG8_BAR;
.LBB0_425:
	s_add_u32 s24, s20, 0x14000000
	s_addc_u32 s25, s21, 0
	s_add_u32 s26, s20, 0x400000
	s_addc_u32 s27, s21, 0
	s_lshl_b32 s8, s1, 2
	s_mov_b64 s[28:29], 0x80
	s_add_i32 s65, s8, 0
	v_lshl_add_u64 v[6:7], v[6:7], 0, s[28:29]
	s_add_i32 m0, s60, 0x18000
	s_add_i32 s65, s65, 0x20000
	s_waitcnt vmcnt(2)
	s_barrier
	global_load_lds_dwordx4 v[6:7], off
	v_lshl_add_u64 v[4:5], v[4:5], 0, s[28:29]
	s_add_i32 m0, s60, 0x1a000
	s_add_i32 s66, s60, 0x8000
	s_add_i32 s67, s60, 0xa000
	global_load_lds_dwordx4 v[4:5], off
	v_lshl_add_u64 v[2:3], v[2:3], 0, s[28:29]
	s_mov_b32 m0, s66
	s_add_u32 s8, s44, 0x10080
	global_load_lds_dwordx4 v[2:3], off
	v_lshl_add_u64 v[0:1], v[0:1], 0, s[28:29]
	s_mov_b32 m0, s67
	s_addc_u32 s9, s45, 0
	global_load_lds_dwordx4 v[0:1], off
	s_add_i32 m0, s60, 0x1c000
	v_and_b32_e32 v4, 48, v8
	global_load_lds_dwordx4 v162, s[8:9]
	s_add_i32 m0, s60, 0x1e000
	v_lshl_add_u64 v[0:1], s[8:9], 0, v[166:167]
	s_add_u32 s8, s46, 0x10080
	s_addc_u32 s9, s47, 0
	s_add_i32 s68, s60, 0xc000
	global_load_lds_dwordx4 v[0:1], off
	s_mov_b32 m0, s68
	s_add_i32 s69, s60, 0xe000
	global_load_lds_dwordx4 v160, s[8:9]
	v_lshl_add_u64 v[0:1], s[8:9], 0, v[164:165]
	s_mov_b32 m0, s69
	s_movk_i32 s8, 0x3c0
	global_load_lds_dwordx4 v[0:1], off
	v_and_b32_e32 v0, 15, v8
	v_or_b32_e32 v1, s1, v0
	v_lshlrev_b32_e32 v3, 6, v1
	v_ashrrev_i32_e32 v2, 6, v8
	v_and_or_b32 v3, v3, s8, v4
	v_readlane_b32 s8, v248, 14
	v_lshlrev_b32_e32 v1, 2, v1
	v_and_b32_e32 v1, 32, v1
	v_lshl_add_u32 v5, v2, 10, s8
	v_bitop3_b32 v1, v3, v5, v1 bitop3:0xde
	v_readlane_b32 s8, v248, 15
	v_lshlrev_b32_e32 v3, 2, v8
	s_cmp_gt_i32 s5, 63
	v_lshl_or_b32 v0, v0, 6, v4
	v_add_lshl_u32 v2, v2, s8, 10
	v_and_b32_e32 v3, 32, v3
	s_waitcnt vmcnt(8)
	s_cselect_b64 s[8:9], -1, 0
	v_bitop3_b32 v198, v0, v2, v3 bitop3:0xde
	v_cndmask_b32_e64 v0, 0, 1, s[8:9]
	s_add_i32 s74, 0, 0x10000
	s_add_i32 s75, 0, 0x14000
	s_add_i32 s73, s4, -2
	v_mov_b64_e32 v[170:171], 0x300
	v_mov_b64_e32 v[172:173], 0x2ff
	v_add_u32_e32 v200, s74, v198
	v_add_u32_e32 v201, s75, v198
	v_add_u32_e32 v202, 0, v1
	s_movk_i32 s76, 0x600
	v_cmp_ne_u32_e64 s[8:9], 1, v0
	s_mov_b32 s15, 0
	s_mov_b32 s42, 0
	s_barrier
	s_branch .LBB0_428

; #define PG8_STAGE(bufoff, gbase, voff) do { _Pragma("unroll") for (int _i = 0; _i < 2; ++_i) \
;         __builtin_amdgcn_global_load_lds((const unsigned*)((const char*)(gbase) + (voff)[_i]), (LAS unsigned*)(lds + (bufoff) + ldsw + _i * 8192), 16, 0, 0); } while (0)
; #define PG8_LDA(dst, b, h) do { _Pragma("unroll") for (int m = 0; m < 4; ++m) _Pragma("unroll") for (int k = 0; k < 2; ++k) dst[m][k] = *(const LAS bf16x8*)(lds + PG8_SA(b, h) + aoff + m * 2048 + k * 1024); } while (0)
; #define PG8_LDB(dst, b, h) do { _Pragma("unroll") for (int n = 0; n < 2; ++n) _Pragma("unroll") for (int k = 0; k < 2; ++k) dst[n][k] = *(const LAS bf16x8*)(lds + PG8_SB(b, h) + boff + n * 2048 + k * 1024); } while (0)
; #define PG8_MMA(ai, bj, At, Bt_) do { __builtin_amdgcn_s_setprio(1); _Pragma("unroll") for (int m = 0; m < 4; ++m) _Pragma("unroll") for (int n = 0; n < 2; ++n) _Pragma("unroll") for (int k = 0; k < 2; ++k) \
;         acc[ai][bj][m][n] = __builtin_amdgcn_mfma_f32_16x16x32_bf16(Bt_[n][k], At[m][k], acc[ai][bj][m][n], 0, 0, 0); __builtin_amdgcn_s_setprio(0); } while (0)
; #define PG8_BAR __builtin_amdgcn_s_barrier()
; template <class Epi, class Sched, bool GATHER>
; __device__ __forceinline__ void gemm_phase(LAS unsigned char* lds, const int wid, const bf16_t* A, int lda, const bf16_t* Bt, int ldb, size_t b_estride, int K, const Sched& S, const Epi& E) {
;     ...
;             PG8_LDB(B0, 0, 0); PG8_LDB(B1, 0, 1); PG8_SCHED; PG8_LDA(At, 0, 0);
;             PG8_WAIT_VR(rl); PG8_WAIT_L(0); PG8_BAR; PG8_MMA(0, 0, At, B0); PG8_MMA(0, 1, At, B1); PG8_BAR; PG8_SCHED;
;             PG8_LDA(At, 0, 1); PG8_STAGE(PG8_SB(0, 0), b2, voffB); PG8_STAGE(PG8_SB(0, 1), b2 + hstepB, voffB); PG8_STAGE_A(PG8_SA(0, 0), a2, 0, k2, g20);
;             PG8_WAIT_VR(rl); PG8_WAIT_L(0); PG8_BAR; PG8_MMA(1, 0, At, B0); PG8_MMA(1, 1, At, B1); PG8_BAR; PG8_SCHED;
;             PG8_LDB(B0, 1, 0); PG8_LDB(B1, 1, 1); PG8_SCHED; PG8_LDA(At, 1, 0); PG8_STAGE_A(PG8_SA(0, 1), a2, 1, k2, g21);
;             PG8_WAIT_VR(rl); PG8_WAIT_L(0); PG8_BAR; PG8_MMA(0, 0, At, B0); PG8_MMA(0, 1, At, B1); PG8_BAR; PG8_SCHED;
;             PG8_LDA(At, 1, 1); PG8_STAGE(PG8_SB(1, 0), b3, voffB); PG8_STAGE(PG8_SB(1, 1), b3 + hstepB, voffB); PG8_STAGE_A(PG8_SA(1, 0), a3, 0, k3, g20);
;             PG8_WAIT_V(8); PG8_WAIT_L(0); PG8_BAR; PG8_MMA(1, 0, At, B0); PG8_MMA(1, 1, At, B1); PG8_BAR; PG8_SCHED;
.Lwvr3:
	s_waitcnt vmcnt(24)
	s_waitcnt lgkmcnt(0)
	s_barrier
	s_setprio 1
	s_waitcnt lgkmcnt(0)
	v_mfma_f32_16x16x32_bf16 v[132:135], v[104:107], v[174:177], v[132:135]
	v_mfma_f32_16x16x32_bf16 v[128:131], v[136:139], v[174:177], v[128:131]
	v_mfma_f32_16x16x32_bf16 v[112:115], v[104:107], v[182:185], v[112:115]
	v_mfma_f32_16x16x32_bf16 v[108:111], v[136:139], v[182:185], v[108:111]
	v_mfma_f32_16x16x32_bf16 v[92:95], v[104:107], v[190:193], v[92:95]
	v_mfma_f32_16x16x32_bf16 v[88:91], v[136:139], v[190:193], v[88:91]
	v_mfma_f32_16x16x32_bf16 v[76:79], v[104:107], v[204:207], v[76:79]
	v_mfma_f32_16x16x32_bf16 v[72:75], v[136:139], v[204:207], v[72:75]
	v_mfma_f32_16x16x32_bf16 v[132:135], v[124:127], v[178:181], v[132:135]
	v_mfma_f32_16x16x32_bf16 v[128:131], v[140:143], v[178:181], v[128:131]
	v_mfma_f32_16x16x32_bf16 v[112:115], v[124:127], v[186:189], v[112:115]
	v_mfma_f32_16x16x32_bf16 v[108:111], v[140:143], v[186:189], v[108:111]
	v_mfma_f32_16x16x32_bf16 v[92:95], v[124:127], v[194:197], v[92:95]
	v_mfma_f32_16x16x32_bf16 v[88:91], v[140:143], v[194:197], v[88:91]
	v_mfma_f32_16x16x32_bf16 v[76:79], v[124:127], v[208:211], v[76:79]
	v_mfma_f32_16x16x32_bf16 v[72:75], v[140:143], v[208:211], v[72:75]
	s_setprio 0
	s_setprio 1
	v_mfma_f32_16x16x32_bf16 v[120:123], v[144:147], v[174:177], v[120:123]
	v_mfma_f32_16x16x32_bf16 v[116:119], v[152:155], v[174:177], v[116:119]
	v_mfma_f32_16x16x32_bf16 v[100:103], v[144:147], v[182:185], v[100:103]
	v_mfma_f32_16x16x32_bf16 v[96:99], v[152:155], v[182:185], v[96:99]
	v_mfma_f32_16x16x32_bf16 v[84:87], v[144:147], v[190:193], v[84:87]
	v_mfma_f32_16x16x32_bf16 v[80:83], v[152:155], v[190:193], v[80:83]
	v_mfma_f32_16x16x32_bf16 v[68:71], v[144:147], v[204:207], v[68:71]
	v_mfma_f32_16x16x32_bf16 v[64:67], v[152:155], v[204:207], v[64:67]
	v_mfma_f32_16x16x32_bf16 v[120:123], v[148:151], v[178:181], v[120:123]
	v_mfma_f32_16x16x32_bf16 v[116:119], v[156:159], v[178:181], v[116:119]
	v_mfma_f32_16x16x32_bf16 v[100:103], v[148:151], v[186:189], v[100:103]
	v_mfma_f32_16x16x32_bf16 v[96:99], v[156:159], v[186:189], v[96:99]
	v_mfma_f32_16x16x32_bf16 v[84:87], v[148:151], v[194:197], v[84:87]
	v_mfma_f32_16x16x32_bf16 v[80:83], v[156:159], v[194:197], v[80:83]
	v_mfma_f32_16x16x32_bf16 v[68:71], v[148:151], v[208:211], v[68:71]
	v_mfma_f32_16x16x32_bf16 v[64:67], v[156:159], v[208:211], v[64:67]
	s_setprio 0
	s_barrier
	s_add_i32 s87, s74, s33
	v_lshl_add_u64 v[212:213], s[46:47], 0, v[162:163]
	s_mov_b32 m0, s87
	ds_read_b128 v[174:177], v202 offset:16384
	ds_read_b128 v[178:181], v202 offset:17408
	ds_read_b128 v[182:185], v202 offset:18432
	ds_read_b128 v[186:189], v202 offset:19456
	ds_read_b128 v[190:193], v202 offset:20480
	ds_read_b128 v[194:197], v202 offset:21504
	ds_read_b128 v[204:207], v202 offset:22528
	ds_read_b128 v[208:211], v202 offset:23552
	global_load_lds_dwordx4 v[212:213], off
	s_add_i32 m0, s87, 0x2000
	s_add_u32 s88, s46, 0x10000
	v_lshl_add_u64 v[214:215], s[46:47], 0, v[166:167]
	s_addc_u32 s89, s47, 0
	s_add_i32 s87, s75, s33
	global_load_lds_dwordx4 v[214:215], off
	s_mov_b32 m0, s87
	v_lshl_add_u64 v[218:219], s[44:45], 0, v[164:165]
	global_load_lds_dwordx4 v162, s[88:89]
	s_add_i32 m0, s87, 0x2000
	s_nop 0
	global_load_lds_dwordx4 v166, s[88:89]
	v_lshl_add_u64 v[216:217], s[44:45], 0, v[160:161]
	s_mov_b32 m0, s60
	s_nop 0
	global_load_lds_dwordx4 v[216:217], off
	s_mov_b32 m0, s61
	s_nop 0
	global_load_lds_dwordx4 v[218:219], off
	s_cmp_lg_u32 s85, 0
	s_cbranch_scc1 .Lwvr4
	s_waitcnt vmcnt(8)
.Lwvr4:
	s_waitcnt vmcnt(24)
	s_waitcnt lgkmcnt(0)
	s_barrier
	s_setprio 1
	s_waitcnt lgkmcnt(0)
	v_mfma_f32_16x16x32_bf16 v[60:63], v[104:107], v[174:177], v[60:63]
	v_mfma_f32_16x16x32_bf16 v[56:59], v[136:139], v[174:177], v[56:59]
	v_mfma_f32_16x16x32_bf16 v[44:47], v[104:107], v[182:185], v[44:47]
	v_mfma_f32_16x16x32_bf16 v[40:43], v[136:139], v[182:185], v[40:43]
	v_mfma_f32_16x16x32_bf16 v[28:31], v[104:107], v[190:193], v[28:31]
	v_mfma_f32_16x16x32_bf16 v[24:27], v[136:139], v[190:193], v[24:27]
	v_mfma_f32_16x16x32_bf16 v[12:15], v[104:107], v[204:207], v[12:15]
	v_mfma_f32_16x16x32_bf16 v[8:11], v[136:139], v[204:207], v[8:11]
	v_mfma_f32_16x16x32_bf16 v[60:63], v[124:127], v[178:181], v[60:63]
	v_mfma_f32_16x16x32_bf16 v[56:59], v[140:143], v[178:181], v[56:59]
	v_mfma_f32_16x16x32_bf16 v[44:47], v[124:127], v[186:189], v[44:47]
	v_mfma_f32_16x16x32_bf16 v[40:43], v[140:143], v[186:189], v[40:43]
	v_mfma_f32_16x16x32_bf16 v[28:31], v[124:127], v[194:197], v[28:31]
	v_mfma_f32_16x16x32_bf16 v[24:27], v[140:143], v[194:197], v[24:27]
	v_mfma_f32_16x16x32_bf16 v[12:15], v[124:127], v[208:211], v[12:15]
	v_mfma_f32_16x16x32_bf16 v[8:11], v[140:143], v[208:211], v[8:11]
	s_setprio 0
	s_setprio 1
	v_mfma_f32_16x16x32_bf16 v[52:55], v[144:147], v[174:177], v[52:55]
	v_mfma_f32_16x16x32_bf16 v[48:51], v[152:155], v[174:177], v[48:51]
	v_mfma_f32_16x16x32_bf16 v[36:39], v[144:147], v[182:185], v[36:39]
	v_mfma_f32_16x16x32_bf16 v[32:35], v[152:155], v[182:185], v[32:35]
	v_mfma_f32_16x16x32_bf16 v[20:23], v[144:147], v[190:193], v[20:23]
	v_mfma_f32_16x16x32_bf16 v[16:19], v[152:155], v[190:193], v[16:19]
	v_mfma_f32_16x16x32_bf16 v[4:7], v[144:147], v[204:207], v[4:7]
	v_mfma_f32_16x16x32_bf16 v[0:3], v[152:155], v[204:207], v[0:3]
	v_mfma_f32_16x16x32_bf16 v[52:55], v[148:151], v[178:181], v[52:55]
	v_mfma_f32_16x16x32_bf16 v[48:51], v[156:159], v[178:181], v[48:51]
	v_mfma_f32_16x16x32_bf16 v[36:39], v[148:151], v[186:189], v[36:39]
	v_mfma_f32_16x16x32_bf16 v[32:35], v[156:159], v[186:189], v[32:35]
	v_mfma_f32_16x16x32_bf16 v[20:23], v[148:151], v[194:197], v[20:23]
	v_mfma_f32_16x16x32_bf16 v[16:19], v[156:159], v[194:197], v[16:19]
	v_mfma_f32_16x16x32_bf16 v[4:7], v[148:151], v[208:211], v[4:7]
	v_mfma_f32_16x16x32_bf16 v[0:3], v[156:159], v[208:211], v[0:3]
	s_setprio 0
	s_barrier
	s_add_i32 s87, 0, 0x18000
	s_add_i32 s90, 0, 0x1c000
	v_add_u32_e32 v140, s87, v198
	v_add_u32_e32 v156, s90, v198
	ds_read_b128 v[104:107], v140
	ds_read_b128 v[124:127], v140 offset:1024
	ds_read_b128 v[136:139], v140 offset:2048
	ds_read_b128 v[140:143], v140 offset:3072
	ds_read_b128 v[144:147], v156
	ds_read_b128 v[148:151], v156 offset:1024
	ds_read_b128 v[152:155], v156 offset:2048
	ds_read_b128 v[156:159], v156 offset:3072
	s_add_u32 s88, s44, 0x10000
	s_addc_u32 s89, s45, 0
	s_mov_b32 m0, s63
	ds_read_b128 v[174:177], v202 offset:32768
	ds_read_b128 v[178:181], v202 offset:33792
	ds_read_b128 v[182:185], v202 offset:34816
	ds_read_b128 v[186:189], v202 offset:35840
	ds_read_b128 v[190:193], v202 offset:36864
	ds_read_b128 v[194:197], v202 offset:37888
	ds_read_b128 v[204:207], v202 offset:38912
	ds_read_b128 v[208:211], v202 offset:39936
	global_load_lds_dwordx4 v160, s[88:89]
	v_lshl_add_u64 v[220:221], s[88:89], 0, v[164:165]
	s_mov_b32 m0, s64
	s_nop 0
	global_load_lds_dwordx4 v[220:221], off
	s_cmp_lg_u32 s85, 0
	s_cbranch_scc1 .Lwvr5
	s_waitcnt vmcnt(8)
; #define PG8_STAGE(bufoff, gbase, voff) do { _Pragma("unroll") for (int _i = 0; _i < 2; ++_i) \
;         __builtin_amdgcn_global_load_lds((const unsigned*)((const char*)(gbase) + (voff)[_i]), (LAS unsigned*)(lds + (bufoff) + ldsw + _i * 8192), 16, 0, 0); } while (0)
; #define PG8_LDA(dst, b, h) do { _Pragma("unroll") for (int m = 0; m < 4; ++m) _Pragma("unroll") for (int k = 0; k < 2; ++k) dst[m][k] = *(const LAS bf16x8*)(lds + PG8_SA(b, h) + aoff + m * 2048 + k * 1024); } while (0)
; #define PG8_LDB(dst, b, h) do { _Pragma("unroll") for (int n = 0; n < 2; ++n) _Pragma("unroll") for (int k = 0; k < 2; ++k) dst[n][k] = *(const LAS bf16x8*)(lds + PG8_SB(b, h) + boff + n * 2048 + k * 1024); } while (0)
; #define PG8_MMA(ai, bj, At, Bt_) do { __builtin_amdgcn_s_setprio(1); _Pragma("unroll") for (int m = 0; m < 4; ++m) _Pragma("unroll") for (int n = 0; n < 2; ++n) _Pragma("unroll") for (int k = 0; k < 2; ++k) \
;         acc[ai][bj][m][n] = __builtin_amdgcn_mfma_f32_16x16x32_bf16(Bt_[n][k], At[m][k], acc[ai][bj][m][n], 0, 0, 0); __builtin_amdgcn_s_setprio(0); } while (0)
; #define PG8_WAIT_V(n) asm volatile("s_waitcnt vmcnt(" #n ")" ::: "memory")
; #define PG8_WAIT_L(n) asm volatile("s_waitcnt lgkmcnt(" #n ")" ::: "memory")
; #define PG8_WAIT_VR(rl) asm volatile("s_cmp_lg_u32 %0, 0\n\ts_cbranch_scc1 .Lwvr%=\n\ts_waitcnt vmcnt(8)\n.Lwvr%=:\n\ts_waitcnt vmcnt(24)" :: "s"(rl) : "scc", "memory")
; template <class Epi, class Sched, bool GATHER>
; __device__ __forceinline__ void gemm_phase(LAS unsigned char* lds, const int wid, const bf16_t* A, int lda, const bf16_t* Bt, int ldb, size_t b_estride, int K, const Sched& S, const Epi& E) {
;     ...
;             PG8_WAIT_VR(rl); PG8_WAIT_L(0); PG8_BAR; PG8_MMA(1, 0, At, B0); PG8_MMA(1, 1, At, B1); PG8_BAR; PG8_SCHED;
;             PG8_LDB(B0, 1, 0); PG8_LDB(B1, 1, 1); PG8_SCHED; PG8_LDA(At, 1, 0); PG8_STAGE_A(PG8_SA(0, 1), a2, 1, k2, g21);
;             PG8_WAIT_VR(rl); PG8_WAIT_L(0); PG8_BAR; PG8_MMA(0, 0, At, B0); PG8_MMA(0, 1, At, B1); PG8_BAR; PG8_SCHED;
;             PG8_LDA(At, 1, 1); PG8_STAGE(PG8_SB(1, 0), b3, voffB); PG8_STAGE(PG8_SB(1, 1), b3 + hstepB, voffB); PG8_STAGE_A(PG8_SA(1, 0), a3, 0, k3, g20);
;             PG8_WAIT_V(8); PG8_WAIT_L(0); PG8_BAR; PG8_MMA(1, 0, At, B0); PG8_MMA(1, 1, At, B1); PG8_BAR; PG8_SCHED;
;             PG8_STAGE_A(PG8_SA(1, 1), a3, 1, k3, g21);
;         }
.Lwvr5:
	s_waitcnt vmcnt(24)
	s_waitcnt lgkmcnt(0)
	s_barrier
	s_setprio 1
	s_waitcnt lgkmcnt(0)
	v_mfma_f32_16x16x32_bf16 v[132:135], v[104:107], v[174:177], v[132:135]
	v_mfma_f32_16x16x32_bf16 v[128:131], v[136:139], v[174:177], v[128:131]
	v_mfma_f32_16x16x32_bf16 v[112:115], v[104:107], v[182:185], v[112:115]
	v_mfma_f32_16x16x32_bf16 v[108:111], v[136:139], v[182:185], v[108:111]
	v_mfma_f32_16x16x32_bf16 v[92:95], v[104:107], v[190:193], v[92:95]
	v_mfma_f32_16x16x32_bf16 v[88:91], v[136:139], v[190:193], v[88:91]
	v_mfma_f32_16x16x32_bf16 v[76:79], v[104:107], v[204:207], v[76:79]
	v_mfma_f32_16x16x32_bf16 v[72:75], v[136:139], v[204:207], v[72:75]
	v_mfma_f32_16x16x32_bf16 v[132:135], v[124:127], v[178:181], v[132:135]
	v_mfma_f32_16x16x32_bf16 v[128:131], v[140:143], v[178:181], v[128:131]
	v_mfma_f32_16x16x32_bf16 v[112:115], v[124:127], v[186:189], v[112:115]
	v_mfma_f32_16x16x32_bf16 v[108:111], v[140:143], v[186:189], v[108:111]
	v_mfma_f32_16x16x32_bf16 v[92:95], v[124:127], v[194:197], v[92:95]
	v_mfma_f32_16x16x32_bf16 v[88:91], v[140:143], v[194:197], v[88:91]
	v_mfma_f32_16x16x32_bf16 v[76:79], v[124:127], v[208:211], v[76:79]
	v_mfma_f32_16x16x32_bf16 v[72:75], v[140:143], v[208:211], v[72:75]
	s_setprio 0
	s_setprio 1
	v_mfma_f32_16x16x32_bf16 v[120:123], v[144:147], v[174:177], v[120:123]
	v_mfma_f32_16x16x32_bf16 v[116:119], v[152:155], v[174:177], v[116:119]
	v_mfma_f32_16x16x32_bf16 v[100:103], v[144:147], v[182:185], v[100:103]
	v_mfma_f32_16x16x32_bf16 v[96:99], v[152:155], v[182:185], v[96:99]
	v_mfma_f32_16x16x32_bf16 v[84:87], v[144:147], v[190:193], v[84:87]
	v_mfma_f32_16x16x32_bf16 v[80:83], v[152:155], v[190:193], v[80:83]
	v_mfma_f32_16x16x32_bf16 v[68:71], v[144:147], v[204:207], v[68:71]
	v_mfma_f32_16x16x32_bf16 v[64:67], v[152:155], v[204:207], v[64:67]
	v_mfma_f32_16x16x32_bf16 v[120:123], v[148:151], v[178:181], v[120:123]
	v_mfma_f32_16x16x32_bf16 v[116:119], v[156:159], v[178:181], v[116:119]
	v_mfma_f32_16x16x32_bf16 v[100:103], v[148:151], v[186:189], v[100:103]
	v_mfma_f32_16x16x32_bf16 v[96:99], v[156:159], v[186:189], v[96:99]
	v_mfma_f32_16x16x32_bf16 v[84:87], v[148:151], v[194:197], v[84:87]
	v_mfma_f32_16x16x32_bf16 v[80:83], v[156:159], v[194:197], v[80:83]
	v_mfma_f32_16x16x32_bf16 v[68:71], v[148:151], v[208:211], v[68:71]
	v_mfma_f32_16x16x32_bf16 v[64:67], v[156:159], v[208:211], v[64:67]
	s_setprio 0
	s_barrier
	s_add_i32 s85, s87, s33
	v_lshl_add_u64 v[212:213], v[212:213], 0, s[28:29]
	s_mov_b32 m0, s85
	ds_read_b128 v[174:177], v202 offset:49152
	ds_read_b128 v[178:181], v202 offset:50176
	ds_read_b128 v[182:185], v202 offset:51200
	ds_read_b128 v[186:189], v202 offset:52224
	ds_read_b128 v[190:193], v202 offset:53248
	ds_read_b128 v[194:197], v202 offset:54272
	ds_read_b128 v[204:207], v202 offset:55296
	ds_read_b128 v[208:211], v202 offset:56320
	global_load_lds_dwordx4 v[212:213], off
	s_add_i32 m0, s85, 0x2000
	s_add_u32 s46, s46, 0x10080
	v_lshl_add_u64 v[212:213], v[214:215], 0, s[28:29]
	s_addc_u32 s47, s47, 0
	s_add_i32 s85, s90, s33
	global_load_lds_dwordx4 v[212:213], off
	s_mov_b32 m0, s85
	s_nop 0
	global_load_lds_dwordx4 v162, s[46:47]
	s_add_i32 m0, s85, 0x2000
	s_nop 0
	global_load_lds_dwordx4 v166, s[46:47]
	v_lshl_add_u64 v[212:213], v[216:217], 0, s[28:29]
	s_mov_b32 m0, s66
	s_nop 0
	global_load_lds_dwordx4 v[212:213], off
	v_lshl_add_u64 v[212:213], v[218:219], 0, s[28:29]
	s_mov_b32 m0, s67
	s_nop 0
	global_load_lds_dwordx4 v[212:213], off
	s_waitcnt vmcnt(8)
	s_waitcnt lgkmcnt(0)
	s_barrier
	s_setprio 1
	s_waitcnt lgkmcnt(0)
	v_mfma_f32_16x16x32_bf16 v[60:63], v[104:107], v[174:177], v[60:63]
	v_mfma_f32_16x16x32_bf16 v[56:59], v[136:139], v[174:177], v[56:59]
	v_mfma_f32_16x16x32_bf16 v[44:47], v[104:107], v[182:185], v[44:47]
	v_mfma_f32_16x16x32_bf16 v[40:43], v[136:139], v[182:185], v[40:43]
	v_mfma_f32_16x16x32_bf16 v[28:31], v[104:107], v[190:193], v[28:31]
	v_mfma_f32_16x16x32_bf16 v[24:27], v[136:139], v[190:193], v[24:27]
	v_mfma_f32_16x16x32_bf16 v[12:15], v[104:107], v[204:207], v[12:15]
	v_mfma_f32_16x16x32_bf16 v[8:11], v[136:139], v[204:207], v[8:11]
	v_mfma_f32_16x16x32_bf16 v[60:63], v[124:127], v[178:181], v[60:63]
	v_mfma_f32_16x16x32_bf16 v[56:59], v[140:143], v[178:181], v[56:59]
	v_mfma_f32_16x16x32_bf16 v[44:47], v[124:127], v[186:189], v[44:47]
	v_mfma_f32_16x16x32_bf16 v[40:43], v[140:143], v[186:189], v[40:43]
	v_mfma_f32_16x16x32_bf16 v[28:31], v[124:127], v[194:197], v[28:31]
	v_mfma_f32_16x16x32_bf16 v[24:27], v[140:143], v[194:197], v[24:27]
	v_mfma_f32_16x16x32_bf16 v[12:15], v[124:127], v[208:211], v[12:15]
	v_mfma_f32_16x16x32_bf16 v[8:11], v[140:143], v[208:211], v[8:11]
	s_setprio 0
	s_setprio 1
	v_mfma_f32_16x16x32_bf16 v[52:55], v[144:147], v[174:177], v[52:55]
	v_mfma_f32_16x16x32_bf16 v[48:51], v[152:155], v[174:177], v[48:51]
	v_mfma_f32_16x16x32_bf16 v[36:39], v[144:147], v[182:185], v[36:39]
	v_mfma_f32_16x16x32_bf16 v[32:35], v[152:155], v[182:185], v[32:35]
	v_mfma_f32_16x16x32_bf16 v[20:23], v[144:147], v[190:193], v[20:23]
	v_mfma_f32_16x16x32_bf16 v[16:19], v[152:155], v[190:193], v[16:19]
	v_mfma_f32_16x16x32_bf16 v[4:7], v[144:147], v[204:207], v[4:7]
	v_mfma_f32_16x16x32_bf16 v[0:3], v[152:155], v[204:207], v[0:3]
	v_mfma_f32_16x16x32_bf16 v[52:55], v[148:151], v[178:181], v[52:55]
	v_mfma_f32_16x16x32_bf16 v[48:51], v[156:159], v[178:181], v[48:51]
	v_mfma_f32_16x16x32_bf16 v[36:39], v[148:151], v[186:189], v[36:39]
	v_mfma_f32_16x16x32_bf16 v[32:35], v[156:159], v[186:189], v[32:35]
	v_mfma_f32_16x16x32_bf16 v[20:23], v[148:151], v[194:197], v[20:23]
	v_mfma_f32_16x16x32_bf16 v[16:19], v[156:159], v[194:197], v[16:19]
	v_mfma_f32_16x16x32_bf16 v[4:7], v[148:151], v[208:211], v[4:7]
	v_mfma_f32_16x16x32_bf16 v[0:3], v[156:159], v[208:211], v[0:3]
	s_setprio 0
	s_barrier
	s_add_u32 s44, s44, 0x10080
	s_addc_u32 s45, s45, 0
	s_mov_b32 m0, s68
	s_nop 0
	global_load_lds_dwordx4 v160, s[44:45]
	s_mov_b32 m0, s69
	s_add_u32 s81, s81, 0x100
	global_load_lds_dwordx4 v164, s[44:45]
	s_addc_u32 s82, s82, 0
	s_add_u32 s83, s83, 0x100
	s_addc_u32 s84, s84, 0
	s_cmp_ge_i32 s86, s4
	s_mov_b32 s85, s86
	s_cbranch_scc0 .LBB0_432

; #define PG8_STAGE(bufoff, gbase, voff) do { _Pragma("unroll") for (int _i = 0; _i < 2; ++_i) \
;         __builtin_amdgcn_global_load_lds((const unsigned*)((const char*)(gbase) + (voff)[_i]), (LAS unsigned*)(lds + (bufoff) + ldsw + _i * 8192), 16, 0, 0); } while (0)
; #define PG8_WAIT_V(n) asm volatile("s_waitcnt vmcnt(" #n ")" ::: "memory")
; #define PG8_BAR __builtin_amdgcn_s_barrier()
; #define PG8_STAGE_A(bufoff, ptr_dense, half, ktoff, goffs) do { if constexpr (GATHER) { PG8_STAGE(bufoff, (const char*)A + (ktoff), goffs); } \
;         else { PG8_STAGE(bufoff, (ptr_dense) + (half) * hstepA, voffA); } } while (0)
; template <class Epi, class Sched, bool GATHER>
; __device__ __forceinline__ void gemm_phase(LAS unsigned char* lds, const int wid, const bf16_t* A, int lda, const bf16_t* Bt, int ldb, size_t b_estride, int K, const Sched& S, const Epi& E) {
;     ...
;     PG8_STAGE(PG8_SB(0, 0), cB, voffB); PG8_STAGE(PG8_SB(0, 1), cB + hstepB, voffB); PG8_STAGE_A(PG8_SA(0, 0), cA, 0, 0, gc0); PG8_STAGE_A(PG8_SA(0, 1), cA, 1, 0, gc1);
;     if (wr == 1) PG8_BAR;
;     PG8_WAIT_V(2); PG8_BAR;
;     PG8_STAGE(PG8_SB(1, 0), cB + kstep, voffB); PG8_STAGE_A(PG8_SA(1, 0), cA + kstep, 0, kstep, gc0); PG8_STAGE(PG8_SB(1, 1), cB + hstepB + kstep, voffB); PG8_STAGE_A(PG8_SA(1, 1), cA + kstep, 1, kstep, gc1);
;     PG8_WAIT_V(8); PG8_BAR;
.LBB0_492:
	s_add_u32 s12, s20, 0x1a000000
	s_addc_u32 s13, s21, 0
	s_add_u32 s14, s20, 0x20000000
	s_addc_u32 s15, s21, 0
	s_lshl_b32 s11, s1, 2
	s_mov_b64 s[20:21], 0x80
	s_add_i32 s60, s11, 0
	v_lshl_add_u64 v[6:7], v[6:7], 0, s[20:21]
	s_add_i32 m0, s52, 0x18000
	s_add_i32 s60, s60, 0x22000
	s_waitcnt vmcnt(2)
	s_barrier
	global_load_lds_dwordx4 v[6:7], off
	v_lshl_add_u64 v[4:5], v[4:5], 0, s[20:21]
	s_add_i32 m0, s52, 0x1a000
	s_add_i32 s61, s52, 0x8000
	s_add_i32 s63, s52, 0xa000
	global_load_lds_dwordx4 v[4:5], off
	v_lshl_add_u64 v[2:3], v[2:3], 0, s[20:21]
	s_mov_b32 m0, s61
	s_add_u32 s22, s38, 0x10080
	global_load_lds_dwordx4 v[2:3], off
	v_lshl_add_u64 v[0:1], v[0:1], 0, s[20:21]
	s_mov_b32 m0, s63
	s_addc_u32 s23, s39, 0
	global_load_lds_dwordx4 v[0:1], off
	s_add_i32 m0, s52, 0x1c000
	s_sext_i32_i8 s74, s10
	global_load_lds_dwordx4 v132, s[22:23]
	s_add_i32 m0, s52, 0x1e000
	v_lshl_add_u64 v[0:1], s[22:23], 0, v[128:129]
	s_add_u32 s22, s42, 0x10080
	s_addc_u32 s23, s43, 0
	s_add_i32 s64, s52, 0xc000
	global_load_lds_dwordx4 v[0:1], off
	s_mov_b32 m0, s64
	s_add_i32 s65, s52, 0xe000
	global_load_lds_dwordx4 v134, s[22:23]
	s_mov_b32 m0, s65
	v_and_b32_e32 v4, 48, v8
	global_load_lds_dwordx4 v130, s[22:23]
	v_and_b32_e32 v0, 15, v8
	v_or_b32_e32 v1, s1, v0
	v_lshlrev_b32_e32 v3, 6, v1
	s_movk_i32 s10, 0x3c0
	v_ashrrev_i32_e32 v2, 6, v8
	v_and_or_b32 v3, v3, s10, v4
	v_readlane_b32 s10, v248, 14
	v_lshlrev_b32_e32 v1, 2, v1
	v_and_b32_e32 v1, 32, v1
	v_lshl_add_u32 v5, v2, 10, s10
	v_bitop3_b32 v1, v3, v5, v1 bitop3:0xde
	v_readlane_b32 s10, v248, 15
	v_lshlrev_b32_e32 v3, 2, v8
	v_lshl_or_b32 v0, v0, 6, v4
	v_add_lshl_u32 v2, v2, s10, 10
	v_and_b32_e32 v3, 32, v3
	s_waitcnt vmcnt(8)
	s_cmp_gt_i32 s5, 63
	v_bitop3_b32 v141, v0, v2, v3 bitop3:0xde
	s_cselect_b64 s[22:23], -1, 0
	s_add_i32 s66, 0, 0x10000
	s_add_i32 s67, 0, 0x14000
	s_add_i32 s5, s4, -2
	v_mov_b64_e32 v[136:137], 0x400
	v_mov_b64_e32 v[138:139], 0x3ff
	v_add_u32_e32 v147, s66, v141
	v_add_u32_e32 v150, s67, v141
	v_add_u32_e32 v151, 0, v1
	s_movk_i32 s68, 0x600
	s_mov_b32 s75, 0
	s_mov_b32 s36, 0
	s_barrier
	s_branch .LBB0_495

; #define PG8_STAGE(bufoff, gbase, voff) do { _Pragma("unroll") for (int _i = 0; _i < 2; ++_i) \
;         __builtin_amdgcn_global_load_lds((const unsigned*)((const char*)(gbase) + (voff)[_i]), (LAS unsigned*)(lds + (bufoff) + ldsw + _i * 8192), 16, 0, 0); } while (0)
; #define PG8_LDA(dst, b, h) do { _Pragma("unroll") for (int m = 0; m < 4; ++m) _Pragma("unroll") for (int k = 0; k < 2; ++k) dst[m][k] = *(const LAS bf16x8*)(lds + PG8_SA(b, h) + aoff + m * 2048 + k * 1024); } while (0)
; #define PG8_LDB(dst, b, h) do { _Pragma("unroll") for (int n = 0; n < 2; ++n) _Pragma("unroll") for (int k = 0; k < 2; ++k) dst[n][k] = *(const LAS bf16x8*)(lds + PG8_SB(b, h) + boff + n * 2048 + k * 1024); } while (0)
; #define PG8_MMA(ai, bj, At, Bt_) do { __builtin_amdgcn_s_setprio(1); _Pragma("unroll") for (int m = 0; m < 4; ++m) _Pragma("unroll") for (int n = 0; n < 2; ++n) _Pragma("unroll") for (int k = 0; k < 2; ++k) \
;         acc[ai][bj][m][n] = __builtin_amdgcn_mfma_f32_16x16x32_bf16(Bt_[n][k], At[m][k], acc[ai][bj][m][n], 0, 0, 0); __builtin_amdgcn_s_setprio(0); } while (0)
; #define PG8_BAR __builtin_amdgcn_s_barrier()
; template <class Epi, class Sched, bool GATHER>
; __device__ __forceinline__ void gemm_phase(LAS unsigned char* lds, const int wid, const bf16_t* A, int lda, const bf16_t* Bt, int ldb, size_t b_estride, int K, const Sched& S, const Epi& E) {
;     ...
;             PG8_LDB(B0, 0, 0); PG8_LDB(B1, 0, 1); PG8_SCHED; PG8_LDA(At, 0, 0);
;             PG8_WAIT_VR(rl); PG8_WAIT_L(0); PG8_BAR; PG8_MMA(0, 0, At, B0); PG8_MMA(0, 1, At, B1); PG8_BAR; PG8_SCHED;
;             PG8_LDA(At, 0, 1); PG8_STAGE(PG8_SB(0, 0), b2, voffB); PG8_STAGE(PG8_SB(0, 1), b2 + hstepB, voffB); PG8_STAGE_A(PG8_SA(0, 0), a2, 0, k2, g20);
;             PG8_WAIT_VR(rl); PG8_WAIT_L(0); PG8_BAR; PG8_MMA(1, 0, At, B0); PG8_MMA(1, 1, At, B1); PG8_BAR; PG8_SCHED;
;             PG8_LDB(B0, 1, 0); PG8_LDB(B1, 1, 1); PG8_SCHED; PG8_LDA(At, 1, 0); PG8_STAGE_A(PG8_SA(0, 1), a2, 1, k2, g21);
;             PG8_WAIT_VR(rl); PG8_WAIT_L(0); PG8_BAR; PG8_MMA(0, 0, At, B0); PG8_MMA(0, 1, At, B1); PG8_BAR; PG8_SCHED;
;             PG8_LDA(At, 1, 1); PG8_STAGE(PG8_SB(1, 0), b3, voffB); PG8_STAGE(PG8_SB(1, 1), b3 + hstepB, voffB); PG8_STAGE_A(PG8_SA(1, 0), a3, 0, k3, g20);
;             PG8_WAIT_V(8); PG8_WAIT_L(0); PG8_BAR; PG8_MMA(1, 0, At, B0); PG8_MMA(1, 1, At, B1); PG8_BAR; PG8_SCHED;
.Lwvr6:
	s_waitcnt vmcnt(24)
	s_waitcnt lgkmcnt(0)
	s_barrier
	s_setprio 1
	s_waitcnt lgkmcnt(0)
	v_mfma_f32_16x16x32_bf16 v[124:127], v[142:145], v[180:183], v[124:127]
	v_mfma_f32_16x16x32_bf16 v[120:123], v[156:159], v[180:183], v[120:123]
	v_mfma_f32_16x16x32_bf16 v[108:111], v[142:145], v[188:191], v[108:111]
	v_mfma_f32_16x16x32_bf16 v[104:107], v[156:159], v[188:191], v[104:107]
	v_mfma_f32_16x16x32_bf16 v[92:95], v[142:145], v[200:203], v[92:95]
	v_mfma_f32_16x16x32_bf16 v[88:91], v[156:159], v[200:203], v[88:91]
	v_mfma_f32_16x16x32_bf16 v[76:79], v[142:145], v[208:211], v[76:79]
	v_mfma_f32_16x16x32_bf16 v[72:75], v[156:159], v[208:211], v[72:75]
	v_mfma_f32_16x16x32_bf16 v[124:127], v[152:155], v[184:187], v[124:127]
	v_mfma_f32_16x16x32_bf16 v[120:123], v[160:163], v[184:187], v[120:123]
	v_mfma_f32_16x16x32_bf16 v[108:111], v[152:155], v[192:195], v[108:111]
	v_mfma_f32_16x16x32_bf16 v[104:107], v[160:163], v[192:195], v[104:107]
	v_mfma_f32_16x16x32_bf16 v[92:95], v[152:155], v[204:207], v[92:95]
	v_mfma_f32_16x16x32_bf16 v[88:91], v[160:163], v[204:207], v[88:91]
	v_mfma_f32_16x16x32_bf16 v[76:79], v[152:155], v[212:215], v[76:79]
	v_mfma_f32_16x16x32_bf16 v[72:75], v[160:163], v[212:215], v[72:75]
	s_setprio 0
	s_setprio 1
	v_mfma_f32_16x16x32_bf16 v[116:119], v[164:167], v[180:183], v[116:119]
	v_mfma_f32_16x16x32_bf16 v[112:115], v[172:175], v[180:183], v[112:115]
	v_mfma_f32_16x16x32_bf16 v[100:103], v[164:167], v[188:191], v[100:103]
	v_mfma_f32_16x16x32_bf16 v[96:99], v[172:175], v[188:191], v[96:99]
	v_mfma_f32_16x16x32_bf16 v[84:87], v[164:167], v[200:203], v[84:87]
	v_mfma_f32_16x16x32_bf16 v[80:83], v[172:175], v[200:203], v[80:83]
	v_mfma_f32_16x16x32_bf16 v[68:71], v[164:167], v[208:211], v[68:71]
	v_mfma_f32_16x16x32_bf16 v[64:67], v[172:175], v[208:211], v[64:67]
	v_mfma_f32_16x16x32_bf16 v[116:119], v[168:171], v[184:187], v[116:119]
	v_mfma_f32_16x16x32_bf16 v[112:115], v[176:179], v[184:187], v[112:115]
	v_mfma_f32_16x16x32_bf16 v[100:103], v[168:171], v[192:195], v[100:103]
	v_mfma_f32_16x16x32_bf16 v[96:99], v[176:179], v[192:195], v[96:99]
	v_mfma_f32_16x16x32_bf16 v[84:87], v[168:171], v[204:207], v[84:87]
	v_mfma_f32_16x16x32_bf16 v[80:83], v[176:179], v[204:207], v[80:83]
	v_mfma_f32_16x16x32_bf16 v[68:71], v[168:171], v[212:215], v[68:71]
	v_mfma_f32_16x16x32_bf16 v[64:67], v[176:179], v[212:215], v[64:67]
	s_setprio 0
	s_barrier
	s_add_i32 s84, s66, s33
	v_lshl_add_u64 v[148:149], s[42:43], 0, v[132:133]
	s_mov_b32 m0, s84
	ds_read_b128 v[180:183], v151 offset:16384
	ds_read_b128 v[184:187], v151 offset:17408
	ds_read_b128 v[188:191], v151 offset:18432
	ds_read_b128 v[192:195], v151 offset:19456
	ds_read_b128 v[200:203], v151 offset:20480
	ds_read_b128 v[204:207], v151 offset:21504
	ds_read_b128 v[208:211], v151 offset:22528
	ds_read_b128 v[212:215], v151 offset:23552
	global_load_lds_dwordx4 v[148:149], off
	s_add_i32 m0, s84, 0x2000
	s_add_u32 s84, s42, 0x10000
	v_lshl_add_u64 v[196:197], s[42:43], 0, v[128:129]
	s_addc_u32 s85, s43, 0
	s_add_i32 s86, s67, s33
	global_load_lds_dwordx4 v[196:197], off
	s_mov_b32 m0, s86
	v_lshl_add_u64 v[218:219], s[38:39], 0, v[130:131]
	global_load_lds_dwordx4 v132, s[84:85]
	s_add_i32 m0, s86, 0x2000
	s_nop 0
	global_load_lds_dwordx4 v128, s[84:85]
	v_lshl_add_u64 v[216:217], s[38:39], 0, v[134:135]
	s_mov_b32 m0, s52
	s_nop 0
	global_load_lds_dwordx4 v[216:217], off
	s_mov_b32 m0, s53
	s_nop 0
	global_load_lds_dwordx4 v[218:219], off
	s_cmp_lg_u32 s82, 0
	s_cbranch_scc1 .Lwvr7
	s_waitcnt vmcnt(8)
.Lwvr7:
	s_waitcnt vmcnt(24)
	s_waitcnt lgkmcnt(0)
	s_barrier
	s_setprio 1
	s_waitcnt lgkmcnt(0)
	v_mfma_f32_16x16x32_bf16 v[60:63], v[142:145], v[180:183], v[60:63]
	v_mfma_f32_16x16x32_bf16 v[56:59], v[156:159], v[180:183], v[56:59]
	v_mfma_f32_16x16x32_bf16 v[44:47], v[142:145], v[188:191], v[44:47]
	v_mfma_f32_16x16x32_bf16 v[40:43], v[156:159], v[188:191], v[40:43]
	v_mfma_f32_16x16x32_bf16 v[28:31], v[142:145], v[200:203], v[28:31]
	v_mfma_f32_16x16x32_bf16 v[24:27], v[156:159], v[200:203], v[24:27]
	v_mfma_f32_16x16x32_bf16 v[12:15], v[142:145], v[208:211], v[12:15]
	v_mfma_f32_16x16x32_bf16 v[8:11], v[156:159], v[208:211], v[8:11]
	v_mfma_f32_16x16x32_bf16 v[60:63], v[152:155], v[184:187], v[60:63]
	v_mfma_f32_16x16x32_bf16 v[56:59], v[160:163], v[184:187], v[56:59]
	v_mfma_f32_16x16x32_bf16 v[44:47], v[152:155], v[192:195], v[44:47]
	v_mfma_f32_16x16x32_bf16 v[40:43], v[160:163], v[192:195], v[40:43]
	v_mfma_f32_16x16x32_bf16 v[28:31], v[152:155], v[204:207], v[28:31]
	v_mfma_f32_16x16x32_bf16 v[24:27], v[160:163], v[204:207], v[24:27]
	v_mfma_f32_16x16x32_bf16 v[12:15], v[152:155], v[212:215], v[12:15]
	v_mfma_f32_16x16x32_bf16 v[8:11], v[160:163], v[212:215], v[8:11]
	s_setprio 0
	s_setprio 1
	v_mfma_f32_16x16x32_bf16 v[52:55], v[164:167], v[180:183], v[52:55]
	v_mfma_f32_16x16x32_bf16 v[48:51], v[172:175], v[180:183], v[48:51]
	v_mfma_f32_16x16x32_bf16 v[36:39], v[164:167], v[188:191], v[36:39]
	v_mfma_f32_16x16x32_bf16 v[32:35], v[172:175], v[188:191], v[32:35]
	v_mfma_f32_16x16x32_bf16 v[20:23], v[164:167], v[200:203], v[20:23]
	v_mfma_f32_16x16x32_bf16 v[16:19], v[172:175], v[200:203], v[16:19]
	v_mfma_f32_16x16x32_bf16 v[4:7], v[164:167], v[208:211], v[4:7]
	v_mfma_f32_16x16x32_bf16 v[0:3], v[172:175], v[208:211], v[0:3]
	v_mfma_f32_16x16x32_bf16 v[52:55], v[168:171], v[184:187], v[52:55]
	v_mfma_f32_16x16x32_bf16 v[48:51], v[176:179], v[184:187], v[48:51]
	v_mfma_f32_16x16x32_bf16 v[36:39], v[168:171], v[192:195], v[36:39]
	v_mfma_f32_16x16x32_bf16 v[32:35], v[176:179], v[192:195], v[32:35]
	v_mfma_f32_16x16x32_bf16 v[20:23], v[168:171], v[204:207], v[20:23]
	v_mfma_f32_16x16x32_bf16 v[16:19], v[176:179], v[204:207], v[16:19]
	v_mfma_f32_16x16x32_bf16 v[4:7], v[168:171], v[212:215], v[4:7]
	v_mfma_f32_16x16x32_bf16 v[0:3], v[176:179], v[212:215], v[0:3]
	s_setprio 0
	s_barrier
	s_add_i32 s86, 0, 0x18000
	v_add_u32_e32 v140, s86, v141
	s_add_i32 s87, 0, 0x1c000
	ds_read_b128 v[142:145], v140
	ds_read_b128 v[152:155], v140 offset:1024
	ds_read_b128 v[156:159], v140 offset:2048
	ds_read_b128 v[160:163], v140 offset:3072
	v_add_u32_e32 v140, s87, v141
	ds_read_b128 v[164:167], v140
	ds_read_b128 v[168:171], v140 offset:1024
	ds_read_b128 v[172:175], v140 offset:2048
	ds_read_b128 v[176:179], v140 offset:3072
	s_add_u32 s84, s38, 0x10000
	s_addc_u32 s85, s39, 0
	s_mov_b32 m0, s58
	ds_read_b128 v[180:183], v151 offset:32768
	ds_read_b128 v[184:187], v151 offset:33792
	ds_read_b128 v[188:191], v151 offset:34816
	ds_read_b128 v[192:195], v151 offset:35840
	ds_read_b128 v[200:203], v151 offset:36864
	ds_read_b128 v[204:207], v151 offset:37888
	ds_read_b128 v[208:211], v151 offset:38912
	ds_read_b128 v[212:215], v151 offset:39936
	global_load_lds_dwordx4 v134, s[84:85]
	v_lshl_add_u64 v[220:221], s[84:85], 0, v[130:131]
	s_mov_b32 m0, s59
	s_nop 0
	global_load_lds_dwordx4 v[220:221], off
	s_cmp_lg_u32 s82, 0
	s_cbranch_scc1 .Lwvr8
	s_waitcnt vmcnt(8)
; #define PG8_STAGE(bufoff, gbase, voff) do { _Pragma("unroll") for (int _i = 0; _i < 2; ++_i) \
;         __builtin_amdgcn_global_load_lds((const unsigned*)((const char*)(gbase) + (voff)[_i]), (LAS unsigned*)(lds + (bufoff) + ldsw + _i * 8192), 16, 0, 0); } while (0)
; #define PG8_LDA(dst, b, h) do { _Pragma("unroll") for (int m = 0; m < 4; ++m) _Pragma("unroll") for (int k = 0; k < 2; ++k) dst[m][k] = *(const LAS bf16x8*)(lds + PG8_SA(b, h) + aoff + m * 2048 + k * 1024); } while (0)
; #define PG8_LDB(dst, b, h) do { _Pragma("unroll") for (int n = 0; n < 2; ++n) _Pragma("unroll") for (int k = 0; k < 2; ++k) dst[n][k] = *(const LAS bf16x8*)(lds + PG8_SB(b, h) + boff + n * 2048 + k * 1024); } while (0)
; #define PG8_MMA(ai, bj, At, Bt_) do { __builtin_amdgcn_s_setprio(1); _Pragma("unroll") for (int m = 0; m < 4; ++m) _Pragma("unroll") for (int n = 0; n < 2; ++n) _Pragma("unroll") for (int k = 0; k < 2; ++k) \
;         acc[ai][bj][m][n] = __builtin_amdgcn_mfma_f32_16x16x32_bf16(Bt_[n][k], At[m][k], acc[ai][bj][m][n], 0, 0, 0); __builtin_amdgcn_s_setprio(0); } while (0)
; #define PG8_WAIT_V(n) asm volatile("s_waitcnt vmcnt(" #n ")" ::: "memory")
; #define PG8_WAIT_L(n) asm volatile("s_waitcnt lgkmcnt(" #n ")" ::: "memory")
; #define PG8_WAIT_VR(rl) asm volatile("s_cmp_lg_u32 %0, 0\n\ts_cbranch_scc1 .Lwvr%=\n\ts_waitcnt vmcnt(8)\n.Lwvr%=:\n\ts_waitcnt vmcnt(24)" :: "s"(rl) : "scc", "memory")
; template <class Epi, class Sched, bool GATHER>
; __device__ __forceinline__ void gemm_phase(LAS unsigned char* lds, const int wid, const bf16_t* A, int lda, const bf16_t* Bt, int ldb, size_t b_estride, int K, const Sched& S, const Epi& E) {
;     ...
;             PG8_WAIT_VR(rl); PG8_WAIT_L(0); PG8_BAR; PG8_MMA(1, 0, At, B0); PG8_MMA(1, 1, At, B1); PG8_BAR; PG8_SCHED;
;             PG8_LDB(B0, 1, 0); PG8_LDB(B1, 1, 1); PG8_SCHED; PG8_LDA(At, 1, 0); PG8_STAGE_A(PG8_SA(0, 1), a2, 1, k2, g21);
;             PG8_WAIT_VR(rl); PG8_WAIT_L(0); PG8_BAR; PG8_MMA(0, 0, At, B0); PG8_MMA(0, 1, At, B1); PG8_BAR; PG8_SCHED;
;             PG8_LDA(At, 1, 1); PG8_STAGE(PG8_SB(1, 0), b3, voffB); PG8_STAGE(PG8_SB(1, 1), b3 + hstepB, voffB); PG8_STAGE_A(PG8_SA(1, 0), a3, 0, k3, g20);
;             PG8_WAIT_V(8); PG8_WAIT_L(0); PG8_BAR; PG8_MMA(1, 0, At, B0); PG8_MMA(1, 1, At, B1); PG8_BAR; PG8_SCHED;
;             PG8_STAGE_A(PG8_SA(1, 1), a3, 1, k3, g21);
;         }
.Lwvr8:
	s_waitcnt vmcnt(24)
	s_waitcnt lgkmcnt(0)
	s_barrier
	s_setprio 1
	s_waitcnt lgkmcnt(0)
	v_mfma_f32_16x16x32_bf16 v[124:127], v[142:145], v[180:183], v[124:127]
	v_mfma_f32_16x16x32_bf16 v[120:123], v[156:159], v[180:183], v[120:123]
	v_mfma_f32_16x16x32_bf16 v[108:111], v[142:145], v[188:191], v[108:111]
	v_mfma_f32_16x16x32_bf16 v[104:107], v[156:159], v[188:191], v[104:107]
	v_mfma_f32_16x16x32_bf16 v[92:95], v[142:145], v[200:203], v[92:95]
	v_mfma_f32_16x16x32_bf16 v[88:91], v[156:159], v[200:203], v[88:91]
	v_mfma_f32_16x16x32_bf16 v[76:79], v[142:145], v[208:211], v[76:79]
	v_mfma_f32_16x16x32_bf16 v[72:75], v[156:159], v[208:211], v[72:75]
	v_mfma_f32_16x16x32_bf16 v[124:127], v[152:155], v[184:187], v[124:127]
	v_mfma_f32_16x16x32_bf16 v[120:123], v[160:163], v[184:187], v[120:123]
	v_mfma_f32_16x16x32_bf16 v[108:111], v[152:155], v[192:195], v[108:111]
	v_mfma_f32_16x16x32_bf16 v[104:107], v[160:163], v[192:195], v[104:107]
	v_mfma_f32_16x16x32_bf16 v[92:95], v[152:155], v[204:207], v[92:95]
	v_mfma_f32_16x16x32_bf16 v[88:91], v[160:163], v[204:207], v[88:91]
	v_mfma_f32_16x16x32_bf16 v[76:79], v[152:155], v[212:215], v[76:79]
	v_mfma_f32_16x16x32_bf16 v[72:75], v[160:163], v[212:215], v[72:75]
	s_setprio 0
	s_setprio 1
	v_mfma_f32_16x16x32_bf16 v[116:119], v[164:167], v[180:183], v[116:119]
	v_mfma_f32_16x16x32_bf16 v[112:115], v[172:175], v[180:183], v[112:115]
	v_mfma_f32_16x16x32_bf16 v[100:103], v[164:167], v[188:191], v[100:103]
	v_mfma_f32_16x16x32_bf16 v[96:99], v[172:175], v[188:191], v[96:99]
	v_mfma_f32_16x16x32_bf16 v[84:87], v[164:167], v[200:203], v[84:87]
	v_mfma_f32_16x16x32_bf16 v[80:83], v[172:175], v[200:203], v[80:83]
	v_mfma_f32_16x16x32_bf16 v[68:71], v[164:167], v[208:211], v[68:71]
	v_mfma_f32_16x16x32_bf16 v[64:67], v[172:175], v[208:211], v[64:67]
	v_mfma_f32_16x16x32_bf16 v[116:119], v[168:171], v[184:187], v[116:119]
	v_mfma_f32_16x16x32_bf16 v[112:115], v[176:179], v[184:187], v[112:115]
	v_mfma_f32_16x16x32_bf16 v[100:103], v[168:171], v[192:195], v[100:103]
	v_mfma_f32_16x16x32_bf16 v[96:99], v[176:179], v[192:195], v[96:99]
	v_mfma_f32_16x16x32_bf16 v[84:87], v[168:171], v[204:207], v[84:87]
	v_mfma_f32_16x16x32_bf16 v[80:83], v[176:179], v[204:207], v[80:83]
	v_mfma_f32_16x16x32_bf16 v[68:71], v[168:171], v[212:215], v[68:71]
	v_mfma_f32_16x16x32_bf16 v[64:67], v[176:179], v[212:215], v[64:67]
	s_setprio 0
	s_barrier
	s_add_i32 s82, s86, s33
	v_lshl_add_u64 v[148:149], v[148:149], 0, s[20:21]
	s_mov_b32 m0, s82
	ds_read_b128 v[180:183], v151 offset:49152
	ds_read_b128 v[184:187], v151 offset:50176
	ds_read_b128 v[188:191], v151 offset:51200
	ds_read_b128 v[192:195], v151 offset:52224
	ds_read_b128 v[200:203], v151 offset:53248
	ds_read_b128 v[204:207], v151 offset:54272
	ds_read_b128 v[208:211], v151 offset:55296
	ds_read_b128 v[212:215], v151 offset:56320
	global_load_lds_dwordx4 v[148:149], off
	s_add_i32 m0, s82, 0x2000
	s_add_u32 s42, s42, 0x10080
	v_lshl_add_u64 v[148:149], v[196:197], 0, s[20:21]
	s_addc_u32 s43, s43, 0
	s_add_i32 s82, s87, s33
	global_load_lds_dwordx4 v[148:149], off
	s_mov_b32 m0, s82
	s_nop 0
	global_load_lds_dwordx4 v132, s[42:43]
	s_add_i32 m0, s82, 0x2000
	s_nop 0
	global_load_lds_dwordx4 v128, s[42:43]
	v_lshl_add_u64 v[148:149], v[216:217], 0, s[20:21]
	s_mov_b32 m0, s61
	s_nop 0
	global_load_lds_dwordx4 v[148:149], off
	v_lshl_add_u64 v[148:149], v[218:219], 0, s[20:21]
	s_mov_b32 m0, s63
	s_nop 0
	global_load_lds_dwordx4 v[148:149], off
	s_waitcnt vmcnt(8)
	s_waitcnt lgkmcnt(0)
	s_barrier
	s_setprio 1
	s_waitcnt lgkmcnt(0)
	v_mfma_f32_16x16x32_bf16 v[60:63], v[142:145], v[180:183], v[60:63]
	v_mfma_f32_16x16x32_bf16 v[56:59], v[156:159], v[180:183], v[56:59]
	v_mfma_f32_16x16x32_bf16 v[44:47], v[142:145], v[188:191], v[44:47]
	v_mfma_f32_16x16x32_bf16 v[40:43], v[156:159], v[188:191], v[40:43]
	v_mfma_f32_16x16x32_bf16 v[28:31], v[142:145], v[200:203], v[28:31]
	v_mfma_f32_16x16x32_bf16 v[24:27], v[156:159], v[200:203], v[24:27]
	v_mfma_f32_16x16x32_bf16 v[12:15], v[142:145], v[208:211], v[12:15]
	v_mfma_f32_16x16x32_bf16 v[8:11], v[156:159], v[208:211], v[8:11]
	v_mfma_f32_16x16x32_bf16 v[60:63], v[152:155], v[184:187], v[60:63]
	v_mfma_f32_16x16x32_bf16 v[56:59], v[160:163], v[184:187], v[56:59]
	v_mfma_f32_16x16x32_bf16 v[44:47], v[152:155], v[192:195], v[44:47]
	v_mfma_f32_16x16x32_bf16 v[40:43], v[160:163], v[192:195], v[40:43]
	v_mfma_f32_16x16x32_bf16 v[28:31], v[152:155], v[204:207], v[28:31]
	v_mfma_f32_16x16x32_bf16 v[24:27], v[160:163], v[204:207], v[24:27]
	v_mfma_f32_16x16x32_bf16 v[12:15], v[152:155], v[212:215], v[12:15]
	v_mfma_f32_16x16x32_bf16 v[8:11], v[160:163], v[212:215], v[8:11]
	s_setprio 0
	s_setprio 1
	v_mfma_f32_16x16x32_bf16 v[52:55], v[164:167], v[180:183], v[52:55]
	v_mfma_f32_16x16x32_bf16 v[48:51], v[172:175], v[180:183], v[48:51]
	v_mfma_f32_16x16x32_bf16 v[36:39], v[164:167], v[188:191], v[36:39]
	v_mfma_f32_16x16x32_bf16 v[32:35], v[172:175], v[188:191], v[32:35]
	v_mfma_f32_16x16x32_bf16 v[20:23], v[164:167], v[200:203], v[20:23]
	v_mfma_f32_16x16x32_bf16 v[16:19], v[172:175], v[200:203], v[16:19]
	v_mfma_f32_16x16x32_bf16 v[4:7], v[164:167], v[208:211], v[4:7]
	v_mfma_f32_16x16x32_bf16 v[0:3], v[172:175], v[208:211], v[0:3]
	v_mfma_f32_16x16x32_bf16 v[52:55], v[168:171], v[184:187], v[52:55]
	v_mfma_f32_16x16x32_bf16 v[48:51], v[176:179], v[184:187], v[48:51]
	v_mfma_f32_16x16x32_bf16 v[36:39], v[168:171], v[192:195], v[36:39]
	v_mfma_f32_16x16x32_bf16 v[32:35], v[176:179], v[192:195], v[32:35]
	v_mfma_f32_16x16x32_bf16 v[20:23], v[168:171], v[204:207], v[20:23]
	v_mfma_f32_16x16x32_bf16 v[16:19], v[176:179], v[204:207], v[16:19]
	v_mfma_f32_16x16x32_bf16 v[4:7], v[168:171], v[212:215], v[4:7]
	v_mfma_f32_16x16x32_bf16 v[0:3], v[176:179], v[212:215], v[0:3]
	s_setprio 0
	s_barrier
	s_add_u32 s38, s38, 0x10080
	s_addc_u32 s39, s39, 0
	s_mov_b32 m0, s64
	s_nop 0
	global_load_lds_dwordx4 v134, s[38:39]
	s_mov_b32 m0, s65
	s_add_u32 s78, s78, 0x100
	global_load_lds_dwordx4 v130, s[38:39]
	s_addc_u32 s79, s79, 0
	s_add_u32 s80, s80, 0x100
	s_addc_u32 s81, s81, 0
	s_cmp_ge_i32 s83, s4
	s_mov_b32 s82, s83
	s_cbranch_scc0 .LBB0_503

; #define DMA_KP(KB, tile, b) do { _Pragma("unroll") for (int _j = 0; _j < NKW; ++_j) glds16((const char*)(KB) + (size_t)(tile) * (KVBLK * LDK * 2) + koff[_j], (LAS unsigned*)(ldsL + (b) * SHM_K + (wid * NKW + _j) * 1024)); } while (0)
; #define DMA_VP(VB, tile, b) do { _Pragma("unroll") for (int _j = 0; _j < 2; ++_j) glds16((const char*)(VB) + (size_t)(tile) * (KVBLK * LDV * 2) + voff[_j], (LAS unsigned*)(ldsL + 3 * SHM_K + (b) * SHM_V + (wid * 2 + _j) * 1024)); } while (0)
;     ...
;     const bool nxt_ = (XP == 0) && (nKh != nullptr);
;     ...
;     if (nxt_ && g == 1) { DMA_KP(nKh, 0, 0); DMA_KP(nKh, 1, 1); DMA_VP(nVh, 0, 0); TOUCH_Q(); }
.LBB0_616:
	s_cmp_lg_u64 s[36:37], 0
	s_cselect_b64 s[44:45], -1, 0
	v_mov_b32_e32 v185, v179
	v_mov_b32_e32 v187, v179
	s_and_b64 s[42:43], s[44:45], s[42:43]
	s_andn2_b64 vcc, exec, s[42:43]
	v_lshl_add_u64 v[120:121], s[36:37], 0, v[178:179]
	v_lshl_add_u64 v[118:119], s[36:37], 0, v[180:181]
	v_lshl_add_u64 v[116:117], s[36:37], 0, v[182:183]
	v_lshl_add_u64 v[114:115], s[38:39], 0, v[184:185]
	v_lshl_add_u64 v[112:113], s[38:39], 0, v[186:187]
	s_cbranch_vccnz .LBB0_623
	s_add_i32 s42, s73, 0
	s_mov_b32 m0, s42
	s_add_i32 s43, s74, 0
	s_add_i32 s46, s75, 0
	global_load_lds_dwordx4 v[120:121], off
	s_mov_b32 m0, s43
	s_add_u32 s38, s36, 0x18000
	global_load_lds_dwordx4 v[118:119], off
	s_mov_b32 m0, s46
	s_addc_u32 s39, s37, 0
	global_load_lds_dwordx4 v[116:117], off
	s_add_i32 m0, s42, 0x6000
	s_nop 0
	global_load_lds_dwordx4 v178, s[38:39]
	s_add_i32 m0, s43, 0x6000
	s_nop 0
	global_load_lds_dwordx4 v180, s[38:39]
	s_add_i32 m0, s46, 0x6000
	s_nop 0
	global_load_lds_dwordx4 v182, s[38:39]
	s_mov_b32 m0, s76
	s_nop 0
	global_load_lds_dwordx4 v[114:115], off
	s_add_i32 m0, s76, 0x400
	s_cmp_lg_u64 s[34:35], 0
	global_load_lds_dwordx4 v[112:113], off
	s_cbranch_scc0 .LBB0_623
	v_cmp_gt_i32_e32 vcc, s86, v200
	s_and_saveexec_b64 s[38:39], vcc
	s_cbranch_execz .LBB0_620
	v_mul_hi_i32 v122, v200, s88
	v_lshrrev_b32_e32 v123, 31, v122
	v_add_u32_e32 v124, v122, v123
	v_add_u32_e32 v125, s57, v124
	v_lshl_add_u32 v124, v124, 1, v124
	v_sub_u32_e32 v124, v200, v124
	v_mov_b64_e32 v[122:123], s[34:35]
	v_lshlrev_b32_e32 v124, 7, v124
	v_mad_i64_i32 v[122:123], s[42:43], v125, s83, v[122:123]
	v_ashrrev_i32_e32 v125, 31, v124
	v_lshl_add_u64 v[122:123], v[122:123], 0, v[124:125]
	s_add_i32 m0, s66, 0x1f000
	s_nop 0
	global_load_lds_dword v[122:123], off

; #define PK4(P, BASE, OUT) do { u32x4 w = {cvtpk(P[BASE + 0], P[BASE + 1]), cvtpk(P[BASE + 2], P[BASE + 3]), cvtpk(P[BASE + 4], P[BASE + 5]), cvtpk(P[BASE + 6], P[BASE + 7])}; \
;     OUT = *reinterpret_cast<bf16x8*>(&w); } while (0)
; #define DMA_KP(KB, tile, b) do { _Pragma("unroll") for (int _j = 0; _j < NKW; ++_j) glds16((const char*)(KB) + (size_t)(tile) * (KVBLK * LDK * 2) + koff[_j], (LAS unsigned*)(ldsL + (b) * SHM_K + (wid * NKW + _j) * 1024)); } while (0)
; #define DMA_VP(VB, tile, b) do { _Pragma("unroll") for (int _j = 0; _j < 2; ++_j) glds16((const char*)(VB) + (size_t)(tile) * (KVBLK * LDV * 2) + voff[_j], (LAS unsigned*)(ldsL + 3 * SHM_K + (b) * SHM_V + (wid * 2 + _j) * 1024)); } while (0)
; __device__ __forceinline__ void smax_tile(f32x16& p0, f32x16& p1, float& mhat, float& l_reg, f32x16 (&o)[4], float* al_l, const bool first, int r32, int hi,
;                                           bf16x8& pa0, bf16x8& pa1, bf16x8& pa2, bf16x8& pa3) {
;     ...
; #pragma unroll
;     for (int r = 0; r < 16; ++r) p0[r] = __builtin_amdgcn_exp2f(p0[r]);
; #pragma unroll
;     for (int r = 0; r < 16; ++r) p1[r] = __builtin_amdgcn_exp2f(p1[r]);
;     float ps = p0[0];
; #pragma unroll
;     for (int r = 1; r < 16; ++r) ps += p0[r];
; #pragma unroll
;     for (int r = 0; r < 16; ++r) ps += p1[r];
;     { auto rr = __builtin_amdgcn_permlane32_swap(__float_as_uint(ps), __float_as_uint(ps), false, false); ps = __uint_as_float(rr[0]) + __uint_as_float(rr[1]); }
;     l_reg += ps;
;     ...
;     PK4(p0, 0, pa0); PK4(p0, 8, pa1); PK4(p1, 0, pa2); PK4(p1, 8, pa3);
;     ...
;     SEG_S(NT - 1);
;     if (nxt_ && g == 0) { DMA_KP(nKh, 0, 0); DMA_KP(nKh, 1, 1); DMA_VP(nVh, 0, 0); TOUCH_Q(); }
.LBB0_624:
	v_exp_f32_e32 v96, v96
	v_exp_f32_e32 v97, v97
	v_exp_f32_e32 v98, v98
	v_exp_f32_e32 v99, v99
	v_exp_f32_e32 v100, v100
	v_exp_f32_e32 v101, v101
	v_exp_f32_e32 v123, v108
	v_add_f32_e32 v108, v97, v96
	v_exp_f32_e32 v102, v102
	v_add_f32_e32 v108, v98, v108
	v_exp_f32_e32 v103, v103
	v_add_f32_e32 v108, v99, v108
	v_exp_f32_e32 v104, v104
	v_add_f32_e32 v108, v100, v108
	v_exp_f32_e32 v105, v105
	v_add_f32_e32 v108, v101, v108
	v_exp_f32_e32 v106, v106
	v_add_f32_e32 v108, v102, v108
	v_exp_f32_e32 v107, v107
	v_add_f32_e32 v108, v103, v108
	v_add_f32_e32 v108, v104, v108
	v_exp_f32_e32 v124, v109
	v_add_f32_e32 v108, v105, v108
	v_exp_f32_e32 v125, v110
	v_add_f32_e32 v108, v106, v108
	v_exp_f32_e32 v126, v111
	v_add_f32_e32 v108, v107, v108
	v_exp_f32_e32 v80, v80
	v_add_f32_e32 v108, v123, v108
	v_exp_f32_e32 v81, v81
	v_add_f32_e32 v108, v124, v108
	v_exp_f32_e32 v82, v82
	v_add_f32_e32 v108, v125, v108
	v_exp_f32_e32 v83, v83
	v_add_f32_e32 v108, v126, v108
	v_exp_f32_e32 v84, v84
	v_add_f32_e32 v108, v80, v108
	v_exp_f32_e32 v85, v85
	v_add_f32_e32 v108, v81, v108
	v_exp_f32_e32 v86, v86
	v_add_f32_e32 v108, v82, v108
	v_exp_f32_e32 v87, v87
	v_add_f32_e32 v108, v83, v108
	v_exp_f32_e32 v88, v88
	v_add_f32_e32 v108, v84, v108
	v_exp_f32_e32 v89, v89
	v_add_f32_e32 v108, v85, v108
	v_exp_f32_e32 v90, v90
	v_add_f32_e32 v108, v86, v108
	v_exp_f32_e32 v91, v91
	v_add_f32_e32 v108, v87, v108
	v_exp_f32_e32 v92, v92
	v_add_f32_e32 v108, v88, v108
	v_exp_f32_e32 v93, v93
	v_add_f32_e32 v108, v89, v108
	v_exp_f32_e32 v94, v94
	v_add_f32_e32 v108, v90, v108
	v_exp_f32_e32 v95, v95
	v_add_f32_e32 v108, v91, v108
	v_add_f32_e32 v108, v92, v108
	v_add_f32_e32 v108, v93, v108
	v_add_f32_e32 v108, v94, v108
	v_add_f32_e32 v108, v95, v108
	v_mov_b32_e32 v109, v108
	s_nop 1
	v_permlane32_swap_b32_e32 v108, v109
	v_add_f32_e32 v108, v108, v109
	v_add_f32_e32 v122, v204, v108
	v_cvt_pk_bf16_f32 v108, v96, v97
	v_cvt_pk_bf16_f32 v109, v98, v99
	v_cvt_pk_bf16_f32 v110, v100, v101
	v_cvt_pk_bf16_f32 v111, v102, v103
	v_cvt_pk_bf16_f32 v104, v104, v105
	v_cvt_pk_bf16_f32 v105, v106, v107
	v_cvt_pk_bf16_f32 v106, v123, v124
	v_cvt_pk_bf16_f32 v107, v125, v126
	v_cvt_pk_bf16_f32 v100, v80, v81
	v_cvt_pk_bf16_f32 v101, v82, v83
	v_cvt_pk_bf16_f32 v102, v84, v85
	v_cvt_pk_bf16_f32 v103, v86, v87
	v_cvt_pk_bf16_f32 v96, v88, v89
	v_cvt_pk_bf16_f32 v97, v90, v91
	v_cvt_pk_bf16_f32 v98, v92, v93
	v_cvt_pk_bf16_f32 v99, v94, v95
	s_cmp_eq_u32 s92, 0
	s_cselect_b64 s[38:39], -1, 0
	s_waitcnt lgkmcnt(0)
	s_barrier
	s_and_b64 s[42:43], s[44:45], s[38:39]
	s_andn2_b64 vcc, exec, s[42:43]
	s_cbranch_vccnz .LBB0_631
	s_add_i32 s42, s73, 0
	s_mov_b32 m0, s42
	s_add_i32 s43, s74, 0
	s_add_i32 s44, s75, 0
	global_load_lds_dwordx4 v[120:121], off
	s_mov_b32 m0, s43
	s_add_u32 s36, s36, 0x18000
	global_load_lds_dwordx4 v[118:119], off
	s_mov_b32 m0, s44
	s_addc_u32 s37, s37, 0
	global_load_lds_dwordx4 v[116:117], off
	s_add_i32 m0, s42, 0x6000
	s_nop 0
	global_load_lds_dwordx4 v178, s[36:37]
	s_add_i32 m0, s43, 0x6000
	s_nop 0
	global_load_lds_dwordx4 v180, s[36:37]
	s_add_i32 m0, s44, 0x6000
	s_nop 0
	global_load_lds_dwordx4 v182, s[36:37]
	s_mov_b32 m0, s76
	s_nop 0
	global_load_lds_dwordx4 v[114:115], off
	s_add_i32 m0, s76, 0x400
	s_cmp_eq_u64 s[34:35], 0
	global_load_lds_dwordx4 v[112:113], off
	s_cbranch_scc1 .LBB0_631
	v_cmp_gt_i32_e32 vcc, s86, v200
	s_and_saveexec_b64 s[36:37], vcc
	s_cbranch_execz .LBB0_628
	v_mul_hi_i32 v80, v200, s88
	v_lshrrev_b32_e32 v81, 31, v80
	v_add_u32_e32 v82, v80, v81
	v_add_u32_e32 v83, s57, v82
	v_lshl_add_u32 v82, v82, 1, v82
	v_sub_u32_e32 v82, v200, v82
	v_mov_b64_e32 v[80:81], s[34:35]
	v_lshlrev_b32_e32 v82, 7, v82
	v_mad_i64_i32 v[80:81], s[42:43], v83, s83, v[80:81]
	v_ashrrev_i32_e32 v83, 31, v82
	v_lshl_add_u64 v[80:81], v[80:81], 0, v[82:83]
	s_add_i32 m0, s66, 0x1f000
	s_nop 0
	global_load_lds_dword v[80:81], off

; #define PG8_STAGE(bufoff, gbase, voff) do { _Pragma("unroll") for (int _i = 0; _i < 2; ++_i) \
;         __builtin_amdgcn_global_load_lds((const unsigned*)((const char*)(gbase) + (voff)[_i]), (LAS unsigned*)(lds + (bufoff) + ldsw + _i * 8192), 16, 0, 0); } while (0)
; #define PG8_WAIT_V(n) asm volatile("s_waitcnt vmcnt(" #n ")" ::: "memory")
; #define PG8_BAR __builtin_amdgcn_s_barrier()
; #define PG8_STAGE_A(bufoff, ptr_dense, half, ktoff, goffs) do { if constexpr (GATHER) { PG8_STAGE(bufoff, (const char*)A + (ktoff), goffs); } \
;         else { PG8_STAGE(bufoff, (ptr_dense) + (half) * hstepA, voffA); } } while (0)
; template <class Epi, class Sched, bool GATHER>
; __device__ __forceinline__ void gemm_phase(LAS unsigned char* lds, const int wid, const bf16_t* A, int lda, const bf16_t* Bt, int ldb, size_t b_estride, int K, const Sched& S, const Epi& E) {
;     ...
;     PG8_STAGE(PG8_SB(0, 0), cB, voffB); PG8_STAGE(PG8_SB(0, 1), cB + hstepB, voffB); PG8_STAGE_A(PG8_SA(0, 0), cA, 0, 0, gc0); PG8_STAGE_A(PG8_SA(0, 1), cA, 1, 0, gc1);
;     if (wr == 1) PG8_BAR;
;     PG8_WAIT_V(2); PG8_BAR;
;     PG8_STAGE(PG8_SB(1, 0), cB + kstep, voffB); PG8_STAGE_A(PG8_SA(1, 0), cA + kstep, 0, kstep, gc0); PG8_STAGE(PG8_SB(1, 1), cB + hstepB + kstep, voffB); PG8_STAGE_A(PG8_SA(1, 1), cA + kstep, 1, kstep, gc1);
;     PG8_WAIT_V(8); PG8_BAR;
.LBB0_765:
	s_add_u32 s51, s14, 0x300000
	s_addc_u32 s52, s15, 0
	s_mov_b64 s[14:15], 0x80
	v_lshl_add_u64 v[6:7], v[6:7], 0, s[14:15]
	s_add_i32 m0, s31, 0x18000
	s_waitcnt vmcnt(2)
	s_barrier
	global_load_lds_dwordx4 v[6:7], off
	v_lshl_add_u64 v[4:5], v[4:5], 0, s[14:15]
	s_add_i32 m0, s31, 0x1a000
	s_add_i32 s53, s31, 0x8000
	s_add_i32 s58, s31, 0xa000
	global_load_lds_dwordx4 v[4:5], off
	v_lshl_add_u64 v[2:3], v[2:3], 0, s[14:15]
	s_mov_b32 m0, s53
	s_add_u32 s18, s36, 0x40080
	global_load_lds_dwordx4 v[2:3], off
	v_lshl_add_u64 v[0:1], v[0:1], 0, s[14:15]
	s_mov_b32 m0, s58
	s_addc_u32 s19, s37, 0
	global_load_lds_dwordx4 v[0:1], off
	s_add_i32 m0, s31, 0x1c000
	s_sext_i32_i8 s66, s8
	global_load_lds_dwordx4 v146, s[18:19]
	s_add_i32 m0, s31, 0x1e000
	v_lshl_add_u64 v[0:1], s[18:19], 0, v[144:145]
	s_add_u32 s18, s38, 0x40080
	s_addc_u32 s19, s39, 0
	s_add_i32 s59, s31, 0xc000
	global_load_lds_dwordx4 v[0:1], off
	s_mov_b32 m0, s59
	s_add_i32 s60, s31, 0xe000
	global_load_lds_dwordx4 v146, s[18:19]
	s_mov_b32 m0, s60
	v_and_b32_e32 v4, 48, v8
	global_load_lds_dwordx4 v144, s[18:19]
	v_and_b32_e32 v0, 15, v8
	v_or_b32_e32 v1, s1, v0
	v_lshlrev_b32_e32 v3, 6, v1
	s_movk_i32 s8, 0x3c0
	v_ashrrev_i32_e32 v2, 6, v8
	v_and_or_b32 v3, v3, s8, v4
	v_readlane_b32 s8, v248, 14
	v_lshlrev_b32_e32 v1, 2, v1
	v_and_b32_e32 v1, 32, v1
	v_lshl_add_u32 v5, v2, 10, s8
	v_bitop3_b32 v1, v3, v5, v1 bitop3:0xde
	v_readlane_b32 s8, v248, 15
	v_lshlrev_b32_e32 v3, 2, v8
	v_lshl_or_b32 v0, v0, 6, v4
	v_add_lshl_u32 v2, v2, s8, 10
	v_and_b32_e32 v3, 32, v3
	s_waitcnt vmcnt(8)
	v_bitop3_b32 v160, v0, v2, v3 bitop3:0xde
	s_add_i32 s61, 0, 0x10000
	s_add_i32 s63, 0, 0x14000
	v_mov_b64_e32 v[148:149], 0x400
	v_mov_b64_e32 v[150:151], 0x3ff
	v_add_u32_e32 v161, s61, v160
	v_add_u32_e32 v162, s63, v160
	v_add_u32_e32 v163, 0, v1
	s_mov_b64 s[18:19], 0x2000
	s_mov_b64 s[20:21], 0x80000
	s_mov_b32 s34, 0
	s_barrier
	s_branch .LBB0_768

; #define PG8_STAGE(bufoff, gbase, voff) do { _Pragma("unroll") for (int _i = 0; _i < 2; ++_i) \
;         __builtin_amdgcn_global_load_lds((const unsigned*)((const char*)(gbase) + (voff)[_i]), (LAS unsigned*)(lds + (bufoff) + ldsw + _i * 8192), 16, 0, 0); } while (0)
; #define PG8_LDA(dst, b, h) do { _Pragma("unroll") for (int m = 0; m < 4; ++m) _Pragma("unroll") for (int k = 0; k < 2; ++k) dst[m][k] = *(const LAS bf16x8*)(lds + PG8_SA(b, h) + aoff + m * 2048 + k * 1024); } while (0)
; #define PG8_LDB(dst, b, h) do { _Pragma("unroll") for (int n = 0; n < 2; ++n) _Pragma("unroll") for (int k = 0; k < 2; ++k) dst[n][k] = *(const LAS bf16x8*)(lds + PG8_SB(b, h) + boff + n * 2048 + k * 1024); } while (0)
; #define PG8_MMA(ai, bj, At, Bt_) do { __builtin_amdgcn_s_setprio(1); _Pragma("unroll") for (int m = 0; m < 4; ++m) _Pragma("unroll") for (int n = 0; n < 2; ++n) _Pragma("unroll") for (int k = 0; k < 2; ++k) \
;         acc[ai][bj][m][n] = __builtin_amdgcn_mfma_f32_16x16x32_bf16(Bt_[n][k], At[m][k], acc[ai][bj][m][n], 0, 0, 0); __builtin_amdgcn_s_setprio(0); } while (0)
; #define PG8_BAR __builtin_amdgcn_s_barrier()
; template <class Epi, class Sched, bool GATHER>
; __device__ __forceinline__ void gemm_phase(LAS unsigned char* lds, const int wid, const bf16_t* A, int lda, const bf16_t* Bt, int ldb, size_t b_estride, int K, const Sched& S, const Epi& E) {
;     ...
;             PG8_LDB(B0, 0, 0); PG8_LDB(B1, 0, 1); PG8_SCHED; PG8_LDA(At, 0, 0);
;             PG8_WAIT_VR(rl); PG8_WAIT_L(0); PG8_BAR; PG8_MMA(0, 0, At, B0); PG8_MMA(0, 1, At, B1); PG8_BAR; PG8_SCHED;
;             PG8_LDA(At, 0, 1); PG8_STAGE(PG8_SB(0, 0), b2, voffB); PG8_STAGE(PG8_SB(0, 1), b2 + hstepB, voffB); PG8_STAGE_A(PG8_SA(0, 0), a2, 0, k2, g20);
;             PG8_WAIT_VR(rl); PG8_WAIT_L(0); PG8_BAR; PG8_MMA(1, 0, At, B0); PG8_MMA(1, 1, At, B1); PG8_BAR; PG8_SCHED;
;             PG8_LDB(B0, 1, 0); PG8_LDB(B1, 1, 1); PG8_SCHED; PG8_LDA(At, 1, 0); PG8_STAGE_A(PG8_SA(0, 1), a2, 1, k2, g21);
;             PG8_WAIT_VR(rl); PG8_WAIT_L(0); PG8_BAR; PG8_MMA(0, 0, At, B0); PG8_MMA(0, 1, At, B1); PG8_BAR; PG8_SCHED;
;             PG8_LDA(At, 1, 1); PG8_STAGE(PG8_SB(1, 0), b3, voffB); PG8_STAGE(PG8_SB(1, 1), b3 + hstepB, voffB); PG8_STAGE_A(PG8_SA(1, 0), a3, 0, k3, g20);
;             PG8_WAIT_V(8); PG8_WAIT_L(0); PG8_BAR; PG8_MMA(1, 0, At, B0); PG8_MMA(1, 1, At, B1); PG8_BAR; PG8_SCHED;
.Lwvr9:
	s_waitcnt vmcnt(24)
	s_waitcnt lgkmcnt(0)
	s_barrier
	s_setprio 1
	s_waitcnt lgkmcnt(0)
	v_mfma_f32_16x16x32_bf16 v[124:127], v[128:131], v[172:175], v[124:127]
	v_mfma_f32_16x16x32_bf16 v[120:123], v[136:139], v[172:175], v[120:123]
	v_mfma_f32_16x16x32_bf16 v[116:119], v[128:131], v[180:183], v[116:119]
	v_mfma_f32_16x16x32_bf16 v[112:115], v[136:139], v[180:183], v[112:115]
	v_mfma_f32_16x16x32_bf16 v[92:95], v[128:131], v[188:191], v[92:95]
	v_mfma_f32_16x16x32_bf16 v[88:91], v[136:139], v[188:191], v[88:91]
	v_mfma_f32_16x16x32_bf16 v[84:87], v[128:131], v[200:203], v[84:87]
	v_mfma_f32_16x16x32_bf16 v[80:83], v[136:139], v[200:203], v[80:83]
	v_mfma_f32_16x16x32_bf16 v[124:127], v[132:135], v[176:179], v[124:127]
	v_mfma_f32_16x16x32_bf16 v[120:123], v[140:143], v[176:179], v[120:123]
	v_mfma_f32_16x16x32_bf16 v[116:119], v[132:135], v[184:187], v[116:119]
	v_mfma_f32_16x16x32_bf16 v[112:115], v[140:143], v[184:187], v[112:115]
	v_mfma_f32_16x16x32_bf16 v[92:95], v[132:135], v[192:195], v[92:95]
	v_mfma_f32_16x16x32_bf16 v[88:91], v[140:143], v[192:195], v[88:91]
	v_mfma_f32_16x16x32_bf16 v[84:87], v[132:135], v[204:207], v[84:87]
	v_mfma_f32_16x16x32_bf16 v[80:83], v[140:143], v[204:207], v[80:83]
	s_setprio 0
	s_setprio 1
	v_mfma_f32_16x16x32_bf16 v[108:111], v[152:155], v[172:175], v[108:111]
	v_mfma_f32_16x16x32_bf16 v[104:107], v[164:167], v[172:175], v[104:107]
	v_mfma_f32_16x16x32_bf16 v[100:103], v[152:155], v[180:183], v[100:103]
	v_mfma_f32_16x16x32_bf16 v[96:99], v[164:167], v[180:183], v[96:99]
	v_mfma_f32_16x16x32_bf16 v[76:79], v[152:155], v[188:191], v[76:79]
	v_mfma_f32_16x16x32_bf16 v[72:75], v[164:167], v[188:191], v[72:75]
	v_mfma_f32_16x16x32_bf16 v[68:71], v[152:155], v[200:203], v[68:71]
	v_mfma_f32_16x16x32_bf16 v[64:67], v[164:167], v[200:203], v[64:67]
	v_mfma_f32_16x16x32_bf16 v[108:111], v[156:159], v[176:179], v[108:111]
	v_mfma_f32_16x16x32_bf16 v[104:107], v[168:171], v[176:179], v[104:107]
	v_mfma_f32_16x16x32_bf16 v[100:103], v[156:159], v[184:187], v[100:103]
	v_mfma_f32_16x16x32_bf16 v[96:99], v[168:171], v[184:187], v[96:99]
	v_mfma_f32_16x16x32_bf16 v[76:79], v[156:159], v[192:195], v[76:79]
	v_mfma_f32_16x16x32_bf16 v[72:75], v[168:171], v[192:195], v[72:75]
	v_mfma_f32_16x16x32_bf16 v[68:71], v[156:159], v[204:207], v[68:71]
	v_mfma_f32_16x16x32_bf16 v[64:67], v[168:171], v[204:207], v[64:67]
	s_setprio 0
	s_barrier
	s_add_i32 s74, s61, s33
	v_lshl_add_u64 v[196:197], s[38:39], 0, v[146:147]
	s_mov_b32 m0, s74
	ds_read_b128 v[172:175], v163 offset:16384
	ds_read_b128 v[176:179], v163 offset:17408
	ds_read_b128 v[180:183], v163 offset:18432
	ds_read_b128 v[184:187], v163 offset:19456
	ds_read_b128 v[188:191], v163 offset:20480
	ds_read_b128 v[192:195], v163 offset:21504
	ds_read_b128 v[200:203], v163 offset:22528
	ds_read_b128 v[204:207], v163 offset:23552
	global_load_lds_dwordx4 v[196:197], off
	s_add_i32 m0, s74, 0x2000
	s_add_u32 s74, s38, 0x40000
	v_lshl_add_u64 v[208:209], s[38:39], 0, v[144:145]
	s_addc_u32 s75, s39, 0
	s_add_i32 s77, s63, s33
	global_load_lds_dwordx4 v[208:209], off
	s_mov_b32 m0, s77
	v_lshl_add_u64 v[212:213], s[36:37], 0, v[144:145]
	global_load_lds_dwordx4 v146, s[74:75]
	s_add_i32 m0, s77, 0x2000
	s_nop 0
	global_load_lds_dwordx4 v144, s[74:75]
	v_lshl_add_u64 v[210:211], s[36:37], 0, v[146:147]
	s_mov_b32 m0, s31
	s_nop 0
	global_load_lds_dwordx4 v[210:211], off
	s_mov_b32 m0, s44
	s_nop 0
	global_load_lds_dwordx4 v[212:213], off
	s_cmp_lg_u32 s76, 0
	s_cbranch_scc1 .Lwvr10
	s_waitcnt vmcnt(8)
.Lwvr10:
	s_waitcnt vmcnt(24)
	s_waitcnt lgkmcnt(0)
	s_barrier
	s_setprio 1
	s_waitcnt lgkmcnt(0)
	v_mfma_f32_16x16x32_bf16 v[60:63], v[128:131], v[172:175], v[60:63]
	v_mfma_f32_16x16x32_bf16 v[56:59], v[136:139], v[172:175], v[56:59]
	v_mfma_f32_16x16x32_bf16 v[44:47], v[128:131], v[180:183], v[44:47]
	v_mfma_f32_16x16x32_bf16 v[40:43], v[136:139], v[180:183], v[40:43]
	v_mfma_f32_16x16x32_bf16 v[36:39], v[128:131], v[188:191], v[36:39]
	v_mfma_f32_16x16x32_bf16 v[32:35], v[136:139], v[188:191], v[32:35]
	v_mfma_f32_16x16x32_bf16 v[20:23], v[128:131], v[200:203], v[20:23]
	v_mfma_f32_16x16x32_bf16 v[16:19], v[136:139], v[200:203], v[16:19]
	v_mfma_f32_16x16x32_bf16 v[60:63], v[132:135], v[176:179], v[60:63]
	v_mfma_f32_16x16x32_bf16 v[56:59], v[140:143], v[176:179], v[56:59]
	v_mfma_f32_16x16x32_bf16 v[44:47], v[132:135], v[184:187], v[44:47]
	v_mfma_f32_16x16x32_bf16 v[40:43], v[140:143], v[184:187], v[40:43]
	v_mfma_f32_16x16x32_bf16 v[36:39], v[132:135], v[192:195], v[36:39]
	v_mfma_f32_16x16x32_bf16 v[32:35], v[140:143], v[192:195], v[32:35]
	v_mfma_f32_16x16x32_bf16 v[20:23], v[132:135], v[204:207], v[20:23]
	v_mfma_f32_16x16x32_bf16 v[16:19], v[140:143], v[204:207], v[16:19]
	s_setprio 0
	s_setprio 1
	v_mfma_f32_16x16x32_bf16 v[52:55], v[152:155], v[172:175], v[52:55]
	v_mfma_f32_16x16x32_bf16 v[48:51], v[164:167], v[172:175], v[48:51]
	v_mfma_f32_16x16x32_bf16 v[28:31], v[152:155], v[180:183], v[28:31]
	v_mfma_f32_16x16x32_bf16 v[24:27], v[164:167], v[180:183], v[24:27]
	v_mfma_f32_16x16x32_bf16 v[12:15], v[152:155], v[188:191], v[12:15]
	v_mfma_f32_16x16x32_bf16 v[8:11], v[164:167], v[188:191], v[8:11]
	v_mfma_f32_16x16x32_bf16 v[4:7], v[152:155], v[200:203], v[4:7]
	v_mfma_f32_16x16x32_bf16 v[0:3], v[164:167], v[200:203], v[0:3]
	v_mfma_f32_16x16x32_bf16 v[52:55], v[156:159], v[176:179], v[52:55]
	v_mfma_f32_16x16x32_bf16 v[48:51], v[168:171], v[176:179], v[48:51]
	v_mfma_f32_16x16x32_bf16 v[28:31], v[156:159], v[184:187], v[28:31]
	v_mfma_f32_16x16x32_bf16 v[24:27], v[168:171], v[184:187], v[24:27]
	v_mfma_f32_16x16x32_bf16 v[12:15], v[156:159], v[192:195], v[12:15]
	v_mfma_f32_16x16x32_bf16 v[8:11], v[168:171], v[192:195], v[8:11]
	v_mfma_f32_16x16x32_bf16 v[4:7], v[156:159], v[204:207], v[4:7]
	v_mfma_f32_16x16x32_bf16 v[0:3], v[168:171], v[204:207], v[0:3]
	s_setprio 0
	s_barrier
	s_add_i32 s77, 0, 0x18000
	s_add_i32 s78, 0, 0x1c000
	v_add_u32_e32 v140, s77, v160
	v_add_u32_e32 v168, s78, v160
	ds_read_b128 v[128:131], v140
	ds_read_b128 v[132:135], v140 offset:1024
	ds_read_b128 v[136:139], v140 offset:2048
	ds_read_b128 v[140:143], v140 offset:3072
	ds_read_b128 v[152:155], v168
	ds_read_b128 v[156:159], v168 offset:1024
	ds_read_b128 v[164:167], v168 offset:2048
	ds_read_b128 v[168:171], v168 offset:3072
	s_add_u32 s74, s36, 0x40000
	s_addc_u32 s75, s37, 0
	s_mov_b32 m0, s45
	ds_read_b128 v[172:175], v163 offset:32768
	ds_read_b128 v[176:179], v163 offset:33792
	ds_read_b128 v[180:183], v163 offset:34816
	ds_read_b128 v[184:187], v163 offset:35840
	ds_read_b128 v[188:191], v163 offset:36864
	ds_read_b128 v[192:195], v163 offset:37888
	ds_read_b128 v[200:203], v163 offset:38912
	ds_read_b128 v[204:207], v163 offset:39936
	global_load_lds_dwordx4 v146, s[74:75]
	s_mov_b32 m0, s46
	s_nop 0
	global_load_lds_dwordx4 v144, s[74:75]
	s_cmp_lg_u32 s76, 0
	s_cbranch_scc1 .Lwvr11
	s_waitcnt vmcnt(8)
; #define PG8_STAGE(bufoff, gbase, voff) do { _Pragma("unroll") for (int _i = 0; _i < 2; ++_i) \
;         __builtin_amdgcn_global_load_lds((const unsigned*)((const char*)(gbase) + (voff)[_i]), (LAS unsigned*)(lds + (bufoff) + ldsw + _i * 8192), 16, 0, 0); } while (0)
; #define PG8_LDA(dst, b, h) do { _Pragma("unroll") for (int m = 0; m < 4; ++m) _Pragma("unroll") for (int k = 0; k < 2; ++k) dst[m][k] = *(const LAS bf16x8*)(lds + PG8_SA(b, h) + aoff + m * 2048 + k * 1024); } while (0)
; #define PG8_LDB(dst, b, h) do { _Pragma("unroll") for (int n = 0; n < 2; ++n) _Pragma("unroll") for (int k = 0; k < 2; ++k) dst[n][k] = *(const LAS bf16x8*)(lds + PG8_SB(b, h) + boff + n * 2048 + k * 1024); } while (0)
; #define PG8_MMA(ai, bj, At, Bt_) do { __builtin_amdgcn_s_setprio(1); _Pragma("unroll") for (int m = 0; m < 4; ++m) _Pragma("unroll") for (int n = 0; n < 2; ++n) _Pragma("unroll") for (int k = 0; k < 2; ++k) \
;         acc[ai][bj][m][n] = __builtin_amdgcn_mfma_f32_16x16x32_bf16(Bt_[n][k], At[m][k], acc[ai][bj][m][n], 0, 0, 0); __builtin_amdgcn_s_setprio(0); } while (0)
; #define PG8_WAIT_V(n) asm volatile("s_waitcnt vmcnt(" #n ")" ::: "memory")
; #define PG8_WAIT_L(n) asm volatile("s_waitcnt lgkmcnt(" #n ")" ::: "memory")
; #define PG8_WAIT_VR(rl) asm volatile("s_cmp_lg_u32 %0, 0\n\ts_cbranch_scc1 .Lwvr%=\n\ts_waitcnt vmcnt(8)\n.Lwvr%=:\n\ts_waitcnt vmcnt(24)" :: "s"(rl) : "scc", "memory")
; template <class Epi, class Sched, bool GATHER>
; __device__ __forceinline__ void gemm_phase(LAS unsigned char* lds, const int wid, const bf16_t* A, int lda, const bf16_t* Bt, int ldb, size_t b_estride, int K, const Sched& S, const Epi& E) {
;     ...
;             PG8_WAIT_VR(rl); PG8_WAIT_L(0); PG8_BAR; PG8_MMA(1, 0, At, B0); PG8_MMA(1, 1, At, B1); PG8_BAR; PG8_SCHED;
;             PG8_LDB(B0, 1, 0); PG8_LDB(B1, 1, 1); PG8_SCHED; PG8_LDA(At, 1, 0); PG8_STAGE_A(PG8_SA(0, 1), a2, 1, k2, g21);
;             PG8_WAIT_VR(rl); PG8_WAIT_L(0); PG8_BAR; PG8_MMA(0, 0, At, B0); PG8_MMA(0, 1, At, B1); PG8_BAR; PG8_SCHED;
;             PG8_LDA(At, 1, 1); PG8_STAGE(PG8_SB(1, 0), b3, voffB); PG8_STAGE(PG8_SB(1, 1), b3 + hstepB, voffB); PG8_STAGE_A(PG8_SA(1, 0), a3, 0, k3, g20);
;             PG8_WAIT_V(8); PG8_WAIT_L(0); PG8_BAR; PG8_MMA(1, 0, At, B0); PG8_MMA(1, 1, At, B1); PG8_BAR; PG8_SCHED;
;             PG8_STAGE_A(PG8_SA(1, 1), a3, 1, k3, g21);
;         }
.Lwvr11:
	s_waitcnt vmcnt(24)
	s_waitcnt lgkmcnt(0)
	s_barrier
	s_setprio 1
	s_waitcnt lgkmcnt(0)
	v_mfma_f32_16x16x32_bf16 v[124:127], v[128:131], v[172:175], v[124:127]
	v_mfma_f32_16x16x32_bf16 v[120:123], v[136:139], v[172:175], v[120:123]
	v_mfma_f32_16x16x32_bf16 v[116:119], v[128:131], v[180:183], v[116:119]
	v_mfma_f32_16x16x32_bf16 v[112:115], v[136:139], v[180:183], v[112:115]
	v_mfma_f32_16x16x32_bf16 v[92:95], v[128:131], v[188:191], v[92:95]
	v_mfma_f32_16x16x32_bf16 v[88:91], v[136:139], v[188:191], v[88:91]
	v_mfma_f32_16x16x32_bf16 v[84:87], v[128:131], v[200:203], v[84:87]
	v_mfma_f32_16x16x32_bf16 v[80:83], v[136:139], v[200:203], v[80:83]
	v_mfma_f32_16x16x32_bf16 v[124:127], v[132:135], v[176:179], v[124:127]
	v_mfma_f32_16x16x32_bf16 v[120:123], v[140:143], v[176:179], v[120:123]
	v_mfma_f32_16x16x32_bf16 v[116:119], v[132:135], v[184:187], v[116:119]
	v_mfma_f32_16x16x32_bf16 v[112:115], v[140:143], v[184:187], v[112:115]
	v_mfma_f32_16x16x32_bf16 v[92:95], v[132:135], v[192:195], v[92:95]
	v_mfma_f32_16x16x32_bf16 v[88:91], v[140:143], v[192:195], v[88:91]
	v_mfma_f32_16x16x32_bf16 v[84:87], v[132:135], v[204:207], v[84:87]
	v_mfma_f32_16x16x32_bf16 v[80:83], v[140:143], v[204:207], v[80:83]
	s_setprio 0
	s_setprio 1
	v_mfma_f32_16x16x32_bf16 v[108:111], v[152:155], v[172:175], v[108:111]
	v_mfma_f32_16x16x32_bf16 v[104:107], v[164:167], v[172:175], v[104:107]
	v_mfma_f32_16x16x32_bf16 v[100:103], v[152:155], v[180:183], v[100:103]
	v_mfma_f32_16x16x32_bf16 v[96:99], v[164:167], v[180:183], v[96:99]
	v_mfma_f32_16x16x32_bf16 v[76:79], v[152:155], v[188:191], v[76:79]
	v_mfma_f32_16x16x32_bf16 v[72:75], v[164:167], v[188:191], v[72:75]
	v_mfma_f32_16x16x32_bf16 v[68:71], v[152:155], v[200:203], v[68:71]
	v_mfma_f32_16x16x32_bf16 v[64:67], v[164:167], v[200:203], v[64:67]
	v_mfma_f32_16x16x32_bf16 v[108:111], v[156:159], v[176:179], v[108:111]
	v_mfma_f32_16x16x32_bf16 v[104:107], v[168:171], v[176:179], v[104:107]
	v_mfma_f32_16x16x32_bf16 v[100:103], v[156:159], v[184:187], v[100:103]
	v_mfma_f32_16x16x32_bf16 v[96:99], v[168:171], v[184:187], v[96:99]
	v_mfma_f32_16x16x32_bf16 v[76:79], v[156:159], v[192:195], v[76:79]
	v_mfma_f32_16x16x32_bf16 v[72:75], v[168:171], v[192:195], v[72:75]
	v_mfma_f32_16x16x32_bf16 v[68:71], v[156:159], v[204:207], v[68:71]
	v_mfma_f32_16x16x32_bf16 v[64:67], v[168:171], v[204:207], v[64:67]
	s_setprio 0
	s_barrier
	s_add_i32 s74, s77, s33
	v_lshl_add_u64 v[196:197], v[196:197], 0, s[14:15]
	s_mov_b32 m0, s74
	ds_read_b128 v[172:175], v163 offset:49152
	ds_read_b128 v[176:179], v163 offset:50176
	ds_read_b128 v[180:183], v163 offset:51200
	ds_read_b128 v[184:187], v163 offset:52224
	ds_read_b128 v[188:191], v163 offset:53248
	ds_read_b128 v[192:195], v163 offset:54272
	ds_read_b128 v[200:203], v163 offset:55296
	ds_read_b128 v[204:207], v163 offset:56320
	global_load_lds_dwordx4 v[196:197], off
	s_add_i32 m0, s74, 0x2000
	s_add_u32 s38, s38, 0x40080
	v_lshl_add_u64 v[196:197], v[208:209], 0, s[14:15]
	s_addc_u32 s39, s39, 0
	s_add_i32 s74, s78, s33
	global_load_lds_dwordx4 v[196:197], off
	s_mov_b32 m0, s74
	s_nop 0
	global_load_lds_dwordx4 v146, s[38:39]
	s_add_i32 m0, s74, 0x2000
	s_nop 0
	global_load_lds_dwordx4 v144, s[38:39]
	v_lshl_add_u64 v[196:197], v[210:211], 0, s[14:15]
	s_mov_b32 m0, s53
	s_nop 0
	global_load_lds_dwordx4 v[196:197], off
	v_lshl_add_u64 v[196:197], v[212:213], 0, s[14:15]
	s_mov_b32 m0, s58
	s_nop 0
	global_load_lds_dwordx4 v[196:197], off
	s_waitcnt vmcnt(8)
	s_waitcnt lgkmcnt(0)
	s_barrier
	s_setprio 1
	s_waitcnt lgkmcnt(0)
	v_mfma_f32_16x16x32_bf16 v[60:63], v[128:131], v[172:175], v[60:63]
	v_mfma_f32_16x16x32_bf16 v[56:59], v[136:139], v[172:175], v[56:59]
	v_mfma_f32_16x16x32_bf16 v[44:47], v[128:131], v[180:183], v[44:47]
	v_mfma_f32_16x16x32_bf16 v[40:43], v[136:139], v[180:183], v[40:43]
	v_mfma_f32_16x16x32_bf16 v[36:39], v[128:131], v[188:191], v[36:39]
	v_mfma_f32_16x16x32_bf16 v[32:35], v[136:139], v[188:191], v[32:35]
	v_mfma_f32_16x16x32_bf16 v[20:23], v[128:131], v[200:203], v[20:23]
	v_mfma_f32_16x16x32_bf16 v[16:19], v[136:139], v[200:203], v[16:19]
	v_mfma_f32_16x16x32_bf16 v[60:63], v[132:135], v[176:179], v[60:63]
	v_mfma_f32_16x16x32_bf16 v[56:59], v[140:143], v[176:179], v[56:59]
	v_mfma_f32_16x16x32_bf16 v[44:47], v[132:135], v[184:187], v[44:47]
	v_mfma_f32_16x16x32_bf16 v[40:43], v[140:143], v[184:187], v[40:43]
	v_mfma_f32_16x16x32_bf16 v[36:39], v[132:135], v[192:195], v[36:39]
	v_mfma_f32_16x16x32_bf16 v[32:35], v[140:143], v[192:195], v[32:35]
	v_mfma_f32_16x16x32_bf16 v[20:23], v[132:135], v[204:207], v[20:23]
	v_mfma_f32_16x16x32_bf16 v[16:19], v[140:143], v[204:207], v[16:19]
	s_setprio 0
	s_setprio 1
	v_mfma_f32_16x16x32_bf16 v[52:55], v[152:155], v[172:175], v[52:55]
	v_mfma_f32_16x16x32_bf16 v[48:51], v[164:167], v[172:175], v[48:51]
	v_mfma_f32_16x16x32_bf16 v[28:31], v[152:155], v[180:183], v[28:31]
	v_mfma_f32_16x16x32_bf16 v[24:27], v[164:167], v[180:183], v[24:27]
	v_mfma_f32_16x16x32_bf16 v[12:15], v[152:155], v[188:191], v[12:15]
	v_mfma_f32_16x16x32_bf16 v[8:11], v[164:167], v[188:191], v[8:11]
	v_mfma_f32_16x16x32_bf16 v[4:7], v[152:155], v[200:203], v[4:7]
	v_mfma_f32_16x16x32_bf16 v[0:3], v[164:167], v[200:203], v[0:3]
	v_mfma_f32_16x16x32_bf16 v[52:55], v[156:159], v[176:179], v[52:55]
	v_mfma_f32_16x16x32_bf16 v[48:51], v[168:171], v[176:179], v[48:51]
	v_mfma_f32_16x16x32_bf16 v[28:31], v[156:159], v[184:187], v[28:31]
	v_mfma_f32_16x16x32_bf16 v[24:27], v[168:171], v[184:187], v[24:27]
	v_mfma_f32_16x16x32_bf16 v[12:15], v[156:159], v[192:195], v[12:15]
	v_mfma_f32_16x16x32_bf16 v[8:11], v[168:171], v[192:195], v[8:11]
	v_mfma_f32_16x16x32_bf16 v[4:7], v[156:159], v[204:207], v[4:7]
	v_mfma_f32_16x16x32_bf16 v[0:3], v[168:171], v[204:207], v[0:3]
	s_setprio 0
	s_barrier
	s_add_u32 s36, s36, 0x40080
	s_addc_u32 s37, s37, 0
	s_mov_b32 m0, s59
	s_nop 0
	global_load_lds_dwordx4 v146, s[36:37]
	s_mov_b32 m0, s60
	s_add_i32 s73, s73, 2
	global_load_lds_dwordx4 v144, s[36:37]
	s_add_u32 s69, s69, 0x100
	s_addc_u32 s70, s70, 0
	s_add_u32 s71, s71, 0x100
	s_addc_u32 s72, s72, 0
	s_cmp_gt_u32 s73, 13
	s_cbranch_scc0 .LBB0_775
	s_and_b64 vcc, exec, s[40:41]
	s_cbranch_vccz .LBB0_778
	s_barrier

; #define PG8_STAGE(bufoff, gbase, voff) do { _Pragma("unroll") for (int _i = 0; _i < 2; ++_i) \
;         __builtin_amdgcn_global_load_lds((const unsigned*)((const char*)(gbase) + (voff)[_i]), (LAS unsigned*)(lds + (bufoff) + ldsw + _i * 8192), 16, 0, 0); } while (0)
; #define PG8_WAIT_V(n) asm volatile("s_waitcnt vmcnt(" #n ")" ::: "memory")
; #define PG8_BAR __builtin_amdgcn_s_barrier()
; #define PG8_STAGE_A(bufoff, ptr_dense, half, ktoff, goffs) do { if constexpr (GATHER) { PG8_STAGE(bufoff, (const char*)A + (ktoff), goffs); } \
;         else { PG8_STAGE(bufoff, (ptr_dense) + (half) * hstepA, voffA); } } while (0)
; template <class Epi, class Sched, bool GATHER>
; __device__ __forceinline__ void gemm_phase(LAS unsigned char* lds, const int wid, const bf16_t* A, int lda, const bf16_t* Bt, int ldb, size_t b_estride, int K, const Sched& S, const Epi& E) {
;     ...
;     Unit cur, nxt; int ui = 0, nst = 0;
;     if (!S.next(0, cur)) return;
;     f32x4 acc[2][2][4][2];
; #pragma unroll
;     for (int a = 0; a < 2; ++a)
; #pragma unroll
;         for (int b = 0; b < 2; ++b)
; #pragma unroll
;             for (int m = 0; m < 4; ++m)
; #pragma unroll
;                 for (int n = 0; n < 2; ++n) acc[a][b][m][n] = (f32x4){0.f, 0.f, 0.f, 0.f};
;     bf16x8 At[4][2], B0[2][2], B1[2][2];
;     unsigned gc0[2] = {0u, 0u}, gc1[2] = {0u, 0u}, gn0[2] = {0u, 0u}, gn1[2] = {0u, 0u};
;     if constexpr (GATHER) {
; #pragma unroll
;         for (int i = 0; i < 2; ++i) { gc0[i] = (unsigned)(S.gather(cur, RA[i]) * lda + CA[i]) * 2u; gc1[i] = (unsigned)(S.gather(cur, 128 + RA[i]) * lda + CA[i]) * 2u; }
;     }
;     const char* cA = (const char*)A + (size_t)cur.pm * tstepA; const char* cB = (const char*)Bt + ((size_t)cur.e * b_estride) * 2 + (size_t)cur.pn * tstepB;
;     PG8_STAGE(PG8_SB(0, 0), cB, voffB); PG8_STAGE(PG8_SB(0, 1), cB + hstepB, voffB); PG8_STAGE_A(PG8_SA(0, 0), cA, 0, 0, gc0); PG8_STAGE_A(PG8_SA(0, 1), cA, 1, 0, gc1);
;     if (wr == 1) PG8_BAR;
;     PG8_WAIT_V(2); PG8_BAR;
;     PG8_STAGE(PG8_SB(1, 0), cB + kstep, voffB); PG8_STAGE_A(PG8_SA(1, 0), cA + kstep, 0, kstep, gc0); PG8_STAGE(PG8_SB(1, 1), cB + hstepB + kstep, voffB); PG8_STAGE_A(PG8_SA(1, 1), cA + kstep, 1, kstep, gc1);
;     PG8_WAIT_V(8); PG8_BAR;
.LBB0_1025:
	s_add_u32 s14, s46, 0x10000000
	s_mov_b64 s[16:17], 0x80
	s_addc_u32 s15, s47, 0
	v_lshl_add_u64 v[2:3], v[2:3], 0, s[16:17]
	s_add_i32 m0, s13, 0x18000
	s_waitcnt vmcnt(2)
	s_barrier
	global_load_lds_dwordx4 v[2:3], off
	s_add_i32 m0, s13, 0x1a000
	s_add_u32 s8, s46, 0x8000080
	v_lshl_add_u64 v[0:1], v[0:1], 0, s[16:17]
	s_addc_u32 s9, s47, 0
	s_add_i32 s38, s13, 0x8000
	s_add_i32 s39, s13, 0xa000
	global_load_lds_dwordx4 v[0:1], off
	s_mov_b32 m0, s38
	s_add_u32 s18, s24, 0x40080
	global_load_lds_dwordx4 v132, s[8:9]
	s_mov_b32 m0, s39
	s_addc_u32 s19, s25, 0
	global_load_lds_dwordx4 v134, s[8:9]
	s_add_i32 m0, s13, 0x1c000
	s_add_i32 s43, s13, 0xc000
	global_load_lds_dwordx4 v130, s[18:19]
	s_add_i32 m0, s13, 0x1e000
	s_add_i32 s46, s13, 0xe000
	global_load_lds_dwordx4 v128, s[18:19]
	s_mov_b32 m0, s43
	v_and_b32_e32 v5, 48, v4
	global_load_lds_dwordx4 v136, s[8:9]
	v_lshl_add_u64 v[0:1], s[8:9], 0, v[138:139]
	s_mov_b32 m0, s46
	s_movk_i32 s8, 0x3c0
	global_load_lds_dwordx4 v[0:1], off
	v_and_b32_e32 v0, 15, v4
	v_or_b32_e32 v1, s1, v0
	v_lshlrev_b32_e32 v3, 6, v1
	v_ashrrev_i32_e32 v2, 6, v4
	v_and_or_b32 v3, v3, s8, v5
	v_readlane_b32 s8, v248, 14
	v_lshlrev_b32_e32 v1, 2, v1
	v_and_b32_e32 v1, 32, v1
	v_lshl_add_u32 v6, v2, 10, s8
	v_bitop3_b32 v1, v3, v6, v1 bitop3:0xde
	v_readlane_b32 s8, v248, 15
	v_lshlrev_b32_e32 v3, 2, v4
	v_lshl_or_b32 v0, v0, 6, v5
	v_add_lshl_u32 v2, v2, s8, 10
	v_and_b32_e32 v3, 32, v3
	v_bitop3_b32 v0, v0, v2, v3 bitop3:0xde
	s_waitcnt vmcnt(8)
	s_add_i32 s53, 0, 0x10000
	s_add_i32 s59, 0, 0x14000
	s_add_i32 s61, 0, 0x18000
	v_add_u32_e32 v137, s53, v0
	v_add_u32_e32 v139, s59, v0
	s_add_i32 s53, s53, s33
	s_add_i32 s59, s59, s33
	v_add_u32_e32 v154, s61, v0
	s_add_i32 s63, 0, 0x1c000
	s_add_i32 s61, s61, s33
	v_add_u32_e32 v153, 0, v1
	s_mov_b32 s47, 0x24000
	s_mov_b32 s51, 0x28000
	s_mov_b32 s52, 0
	s_add_i32 s58, s53, 0x2000
	s_add_i32 s60, s59, 0x2000
	v_add_u32_e32 v155, s63, v0
	s_add_i32 s62, s61, 0x2000
	s_add_i32 s63, s63, s33
	v_mov_b32_e32 v135, v132
	s_mov_b32 s64, 0
	s_barrier
	s_branch .LBB0_1028

; #define PG8_STAGE(bufoff, gbase, voff) do { _Pragma("unroll") for (int _i = 0; _i < 2; ++_i) \
;         __builtin_amdgcn_global_load_lds((const unsigned*)((const char*)(gbase) + (voff)[_i]), (LAS unsigned*)(lds + (bufoff) + ldsw + _i * 8192), 16, 0, 0); } while (0)
; #define PG8_LDA(dst, b, h) do { _Pragma("unroll") for (int m = 0; m < 4; ++m) _Pragma("unroll") for (int k = 0; k < 2; ++k) dst[m][k] = *(const LAS bf16x8*)(lds + PG8_SA(b, h) + aoff + m * 2048 + k * 1024); } while (0)
; #define PG8_LDB(dst, b, h) do { _Pragma("unroll") for (int n = 0; n < 2; ++n) _Pragma("unroll") for (int k = 0; k < 2; ++k) dst[n][k] = *(const LAS bf16x8*)(lds + PG8_SB(b, h) + boff + n * 2048 + k * 1024); } while (0)
; #define PG8_MMA(ai, bj, At, Bt_) do { __builtin_amdgcn_s_setprio(1); _Pragma("unroll") for (int m = 0; m < 4; ++m) _Pragma("unroll") for (int n = 0; n < 2; ++n) _Pragma("unroll") for (int k = 0; k < 2; ++k) \
;         acc[ai][bj][m][n] = __builtin_amdgcn_mfma_f32_16x16x32_bf16(Bt_[n][k], At[m][k], acc[ai][bj][m][n], 0, 0, 0); __builtin_amdgcn_s_setprio(0); } while (0)
; #define PG8_WAIT_L(n) asm volatile("s_waitcnt lgkmcnt(" #n ")" ::: "memory")
; #define PG8_WAIT_VR(rl) asm volatile("s_cmp_lg_u32 %0, 0\n\ts_cbranch_scc1 .Lwvr%=\n\ts_waitcnt vmcnt(8)\n.Lwvr%=:\n\ts_waitcnt vmcnt(24)" :: "s"(rl) : "scc", "memory")
; #define PG8_BAR __builtin_amdgcn_s_barrier()
; #define PG8_SCHED __builtin_amdgcn_sched_barrier(0)
; template <class Epi, class Sched, bool GATHER>
; __device__ __forceinline__ void gemm_phase(LAS unsigned char* lds, const int wid, const bf16_t* A, int lda, const bf16_t* Bt, int ldb, size_t b_estride, int K, const Sched& S, const Epi& E) {
;     ...
;             PG8_WAIT_VR(rl); PG8_WAIT_L(0); PG8_BAR; PG8_MMA(0, 0, At, B0); PG8_MMA(0, 1, At, B1); PG8_BAR; PG8_SCHED;
;             PG8_LDA(At, 0, 1); PG8_STAGE(PG8_SB(0, 0), b2, voffB); PG8_STAGE(PG8_SB(0, 1), b2 + hstepB, voffB); PG8_STAGE_A(PG8_SA(0, 0), a2, 0, k2, g20);
;             PG8_WAIT_VR(rl); PG8_WAIT_L(0); PG8_BAR; PG8_MMA(1, 0, At, B0); PG8_MMA(1, 1, At, B1); PG8_BAR; PG8_SCHED;
;             PG8_LDB(B0, 1, 0); PG8_LDB(B1, 1, 1); PG8_SCHED; PG8_LDA(At, 1, 0); PG8_STAGE_A(PG8_SA(0, 1), a2, 1, k2, g21);
.Lwvr12:
	s_waitcnt vmcnt(24)
	s_waitcnt lgkmcnt(0)
	s_barrier
	s_setprio 1
	s_waitcnt lgkmcnt(0)
	v_mfma_f32_16x16x32_bf16 v[124:127], v[160:163], v[192:195], v[124:127]
	v_mfma_f32_16x16x32_bf16 v[120:123], v[168:171], v[192:195], v[120:123]
	v_mfma_f32_16x16x32_bf16 v[108:111], v[160:163], v[200:203], v[108:111]
	v_mfma_f32_16x16x32_bf16 v[104:107], v[168:171], v[200:203], v[104:107]
	v_mfma_f32_16x16x32_bf16 v[92:95], v[160:163], v[208:211], v[92:95]
	v_mfma_f32_16x16x32_bf16 v[88:91], v[168:171], v[208:211], v[88:91]
	v_mfma_f32_16x16x32_bf16 v[76:79], v[160:163], v[216:219], v[76:79]
	v_mfma_f32_16x16x32_bf16 v[72:75], v[168:171], v[216:219], v[72:75]
	v_mfma_f32_16x16x32_bf16 v[124:127], v[164:167], v[196:199], v[124:127]
	v_mfma_f32_16x16x32_bf16 v[120:123], v[172:175], v[196:199], v[120:123]
	v_mfma_f32_16x16x32_bf16 v[108:111], v[164:167], v[204:207], v[108:111]
	v_mfma_f32_16x16x32_bf16 v[104:107], v[172:175], v[204:207], v[104:107]
	v_mfma_f32_16x16x32_bf16 v[92:95], v[164:167], v[212:215], v[92:95]
	v_mfma_f32_16x16x32_bf16 v[88:91], v[172:175], v[212:215], v[88:91]
	v_mfma_f32_16x16x32_bf16 v[76:79], v[164:167], v[220:223], v[76:79]
	v_mfma_f32_16x16x32_bf16 v[72:75], v[172:175], v[220:223], v[72:75]
	s_setprio 0
	s_setprio 1
	v_mfma_f32_16x16x32_bf16 v[116:119], v[176:179], v[192:195], v[116:119]
	v_mfma_f32_16x16x32_bf16 v[112:115], v[184:187], v[192:195], v[112:115]
	v_mfma_f32_16x16x32_bf16 v[100:103], v[176:179], v[200:203], v[100:103]
	v_mfma_f32_16x16x32_bf16 v[96:99], v[184:187], v[200:203], v[96:99]
	v_mfma_f32_16x16x32_bf16 v[84:87], v[176:179], v[208:211], v[84:87]
	v_mfma_f32_16x16x32_bf16 v[80:83], v[184:187], v[208:211], v[80:83]
	v_mfma_f32_16x16x32_bf16 v[68:71], v[176:179], v[216:219], v[68:71]
	v_mfma_f32_16x16x32_bf16 v[64:67], v[184:187], v[216:219], v[64:67]
	v_mfma_f32_16x16x32_bf16 v[116:119], v[180:183], v[196:199], v[116:119]
	v_mfma_f32_16x16x32_bf16 v[112:115], v[188:191], v[196:199], v[112:115]
	v_mfma_f32_16x16x32_bf16 v[100:103], v[180:183], v[204:207], v[100:103]
	v_mfma_f32_16x16x32_bf16 v[96:99], v[188:191], v[204:207], v[96:99]
	v_mfma_f32_16x16x32_bf16 v[84:87], v[180:183], v[212:215], v[84:87]
	v_mfma_f32_16x16x32_bf16 v[80:83], v[188:191], v[212:215], v[80:83]
	v_mfma_f32_16x16x32_bf16 v[68:71], v[180:183], v[220:223], v[68:71]
	v_mfma_f32_16x16x32_bf16 v[64:67], v[188:191], v[220:223], v[64:67]
	s_setprio 0
	s_barrier
	s_mov_b32 m0, s53
	v_lshl_add_u64 v[230:231], s[28:29], 0, v[130:131]
	s_add_u32 s70, s28, 0x40000
	ds_read_b128 v[192:195], v153 offset:16384
	ds_read_b128 v[196:199], v153 offset:17408
	ds_read_b128 v[200:203], v153 offset:18432
	ds_read_b128 v[204:207], v153 offset:19456
	ds_read_b128 v[208:211], v153 offset:20480
	ds_read_b128 v[212:215], v153 offset:21504
	ds_read_b128 v[216:219], v153 offset:22528
	ds_read_b128 v[220:223], v153 offset:23552
	global_load_lds_dwordx4 v[230:231], off
	v_lshl_add_u64 v[232:233], s[28:29], 0, v[128:129]
	s_mov_b32 m0, s58
	s_addc_u32 s71, s29, 0
	global_load_lds_dwordx4 v[232:233], off
	s_mov_b32 m0, s59
	v_mov_b32_e32 v227, v133
	global_load_lds_dwordx4 v130, s[70:71]
	v_lshl_add_u64 v[234:235], s[70:71], 0, v[128:129]
	s_mov_b32 m0, s60
	s_add_u32 s70, s10, s69
	global_load_lds_dwordx4 v[234:235], off
	s_addc_u32 s71, s11, 0
	s_mov_b32 m0, s13
	v_lshl_add_u64 v[234:235], s[70:71], 0, v[132:133]
	global_load_lds_dwordx4 v132, s[70:71]
	s_mov_b32 m0, s34
	s_nop 0
	global_load_lds_dwordx4 v226, s[70:71]
	s_cmp_lg_u32 s52, 0
	s_cbranch_scc1 .Lwvr13
	s_waitcnt vmcnt(8)

; #define PG8_STAGE(bufoff, gbase, voff) do { _Pragma("unroll") for (int _i = 0; _i < 2; ++_i) \
;         __builtin_amdgcn_global_load_lds((const unsigned*)((const char*)(gbase) + (voff)[_i]), (LAS unsigned*)(lds + (bufoff) + ldsw + _i * 8192), 16, 0, 0); } while (0)
; #define PG8_LDA(dst, b, h) do { _Pragma("unroll") for (int m = 0; m < 4; ++m) _Pragma("unroll") for (int k = 0; k < 2; ++k) dst[m][k] = *(const LAS bf16x8*)(lds + PG8_SA(b, h) + aoff + m * 2048 + k * 1024); } while (0)
; #define PG8_MMA(ai, bj, At, Bt_) do { __builtin_amdgcn_s_setprio(1); _Pragma("unroll") for (int m = 0; m < 4; ++m) _Pragma("unroll") for (int n = 0; n < 2; ++n) _Pragma("unroll") for (int k = 0; k < 2; ++k) \
;         acc[ai][bj][m][n] = __builtin_amdgcn_mfma_f32_16x16x32_bf16(Bt_[n][k], At[m][k], acc[ai][bj][m][n], 0, 0, 0); __builtin_amdgcn_s_setprio(0); } while (0)
; #define PG8_WAIT_V(n) asm volatile("s_waitcnt vmcnt(" #n ")" ::: "memory")
; #define PG8_WAIT_L(n) asm volatile("s_waitcnt lgkmcnt(" #n ")" ::: "memory")
; #define PG8_WAIT_VR(rl) asm volatile("s_cmp_lg_u32 %0, 0\n\ts_cbranch_scc1 .Lwvr%=\n\ts_waitcnt vmcnt(8)\n.Lwvr%=:\n\ts_waitcnt vmcnt(24)" :: "s"(rl) : "scc", "memory")
; #define PG8_BAR __builtin_amdgcn_s_barrier()
; #define PG8_SCHED __builtin_amdgcn_sched_barrier(0)
; #define PG8_STAGE_A(bufoff, ptr_dense, half, ktoff, goffs) do { if constexpr (GATHER) { PG8_STAGE(bufoff, (const char*)A + (ktoff), goffs); } \
;         else { PG8_STAGE(bufoff, (ptr_dense) + (half) * hstepA, voffA); } } while (0)
; template <class Epi, class Sched, bool GATHER>
; __device__ __forceinline__ void gemm_phase(LAS unsigned char* lds, const int wid, const bf16_t* A, int lda, const bf16_t* Bt, int ldb, size_t b_estride, int K, const Sched& S, const Epi& E) {
;     ...
;             PG8_WAIT_VR(rl); PG8_WAIT_L(0); PG8_BAR; PG8_MMA(0, 0, At, B0); PG8_MMA(0, 1, At, B1); PG8_BAR; PG8_SCHED;
;             PG8_LDA(At, 1, 1); PG8_STAGE(PG8_SB(1, 0), b3, voffB); PG8_STAGE(PG8_SB(1, 1), b3 + hstepB, voffB); PG8_STAGE_A(PG8_SA(1, 0), a3, 0, k3, g20);
;             PG8_WAIT_V(8); PG8_WAIT_L(0); PG8_BAR; PG8_MMA(1, 0, At, B0); PG8_MMA(1, 1, At, B1); PG8_BAR; PG8_SCHED;
;             PG8_STAGE_A(PG8_SA(1, 1), a3, 1, k3, g21);
;         }
.Lwvr14:
	s_waitcnt vmcnt(24)
	s_waitcnt lgkmcnt(0)
	v_mov_b32_e32 v229, v133
	v_lshl_add_u64 v[224:225], s[70:71], 0, v[224:225]
	v_lshl_add_u64 v[228:229], s[70:71], 0, v[228:229]
	s_barrier
	s_setprio 1
	s_waitcnt lgkmcnt(0)
	v_mfma_f32_16x16x32_bf16 v[124:127], v[160:163], v[192:195], v[124:127]
	v_mfma_f32_16x16x32_bf16 v[120:123], v[168:171], v[192:195], v[120:123]
	v_mfma_f32_16x16x32_bf16 v[108:111], v[160:163], v[200:203], v[108:111]
	v_mfma_f32_16x16x32_bf16 v[104:107], v[168:171], v[200:203], v[104:107]
	v_mfma_f32_16x16x32_bf16 v[92:95], v[160:163], v[208:211], v[92:95]
	v_mfma_f32_16x16x32_bf16 v[88:91], v[168:171], v[208:211], v[88:91]
	v_mfma_f32_16x16x32_bf16 v[76:79], v[160:163], v[216:219], v[76:79]
	v_mfma_f32_16x16x32_bf16 v[72:75], v[168:171], v[216:219], v[72:75]
	v_mfma_f32_16x16x32_bf16 v[124:127], v[164:167], v[196:199], v[124:127]
	v_mfma_f32_16x16x32_bf16 v[120:123], v[172:175], v[196:199], v[120:123]
	v_mfma_f32_16x16x32_bf16 v[108:111], v[164:167], v[204:207], v[108:111]
	v_mfma_f32_16x16x32_bf16 v[104:107], v[172:175], v[204:207], v[104:107]
	v_mfma_f32_16x16x32_bf16 v[92:95], v[164:167], v[212:215], v[92:95]
	v_mfma_f32_16x16x32_bf16 v[88:91], v[172:175], v[212:215], v[88:91]
	v_mfma_f32_16x16x32_bf16 v[76:79], v[164:167], v[220:223], v[76:79]
	v_mfma_f32_16x16x32_bf16 v[72:75], v[172:175], v[220:223], v[72:75]
	s_setprio 0
	s_setprio 1
	v_mfma_f32_16x16x32_bf16 v[116:119], v[176:179], v[192:195], v[116:119]
	v_mfma_f32_16x16x32_bf16 v[112:115], v[184:187], v[192:195], v[112:115]
	v_mfma_f32_16x16x32_bf16 v[100:103], v[176:179], v[200:203], v[100:103]
	v_mfma_f32_16x16x32_bf16 v[96:99], v[184:187], v[200:203], v[96:99]
	v_mfma_f32_16x16x32_bf16 v[84:87], v[176:179], v[208:211], v[84:87]
	v_mfma_f32_16x16x32_bf16 v[80:83], v[184:187], v[208:211], v[80:83]
	v_mfma_f32_16x16x32_bf16 v[68:71], v[176:179], v[216:219], v[68:71]
	v_mfma_f32_16x16x32_bf16 v[64:67], v[184:187], v[216:219], v[64:67]
	v_mfma_f32_16x16x32_bf16 v[116:119], v[180:183], v[196:199], v[116:119]
	v_mfma_f32_16x16x32_bf16 v[112:115], v[188:191], v[196:199], v[112:115]
	v_mfma_f32_16x16x32_bf16 v[100:103], v[180:183], v[204:207], v[100:103]
	v_mfma_f32_16x16x32_bf16 v[96:99], v[188:191], v[204:207], v[96:99]
	v_mfma_f32_16x16x32_bf16 v[84:87], v[180:183], v[212:215], v[84:87]
	v_mfma_f32_16x16x32_bf16 v[80:83], v[188:191], v[212:215], v[80:83]
	v_mfma_f32_16x16x32_bf16 v[68:71], v[180:183], v[220:223], v[68:71]
	v_mfma_f32_16x16x32_bf16 v[64:67], v[188:191], v[220:223], v[64:67]
	s_setprio 0
	s_barrier
	s_mov_b32 m0, s61
	v_lshl_add_u64 v[230:231], v[230:231], 0, s[16:17]
	s_add_u32 s28, s28, 0x40080
	ds_read_b128 v[192:195], v153 offset:49152
	ds_read_b128 v[196:199], v153 offset:50176
	ds_read_b128 v[200:203], v153 offset:51200
	ds_read_b128 v[204:207], v153 offset:52224
	ds_read_b128 v[208:211], v153 offset:53248
	ds_read_b128 v[212:215], v153 offset:54272
	ds_read_b128 v[216:219], v153 offset:55296
	ds_read_b128 v[220:223], v153 offset:56320
	global_load_lds_dwordx4 v[230:231], off
	v_lshl_add_u64 v[230:231], v[232:233], 0, s[16:17]
	s_mov_b32 m0, s62
	s_addc_u32 s29, s29, 0
	global_load_lds_dwordx4 v[230:231], off
	s_mov_b32 m0, s63
	v_lshl_add_u64 v[226:227], v[226:227], 0, s[16:17]
	global_load_lds_dwordx4 v130, s[28:29]
	s_add_i32 m0, s63, 0x2000
	s_nop 0
	global_load_lds_dwordx4 v128, s[28:29]
	v_lshl_add_u64 v[230:231], v[234:235], 0, s[16:17]
	s_mov_b32 m0, s38
	s_nop 0
	global_load_lds_dwordx4 v[230:231], off
	s_mov_b32 m0, s39
	s_nop 0
	global_load_lds_dwordx4 v[226:227], off
	s_waitcnt vmcnt(8)
	s_waitcnt lgkmcnt(0)
	s_barrier
	s_setprio 1
	s_waitcnt lgkmcnt(0)
	v_mfma_f32_16x16x32_bf16 v[60:63], v[160:163], v[192:195], v[60:63]
	v_mfma_f32_16x16x32_bf16 v[56:59], v[168:171], v[192:195], v[56:59]
	v_mfma_f32_16x16x32_bf16 v[44:47], v[160:163], v[200:203], v[44:47]
	v_mfma_f32_16x16x32_bf16 v[32:35], v[168:171], v[200:203], v[32:35]
	v_mfma_f32_16x16x32_bf16 v[12:15], v[160:163], v[208:211], v[12:15]
	v_mfma_f32_16x16x32_bf16 v[8:11], v[168:171], v[208:211], v[8:11]
	v_mfma_f32_16x16x32_bf16 v[4:7], v[160:163], v[216:219], v[4:7]
	v_mfma_f32_16x16x32_bf16 v[0:3], v[168:171], v[216:219], v[0:3]
	v_mfma_f32_16x16x32_bf16 v[60:63], v[164:167], v[196:199], v[60:63]
	v_mfma_f32_16x16x32_bf16 v[56:59], v[172:175], v[196:199], v[56:59]
	v_mfma_f32_16x16x32_bf16 v[44:47], v[164:167], v[204:207], v[44:47]
	v_mfma_f32_16x16x32_bf16 v[32:35], v[172:175], v[204:207], v[32:35]
	v_mfma_f32_16x16x32_bf16 v[12:15], v[164:167], v[212:215], v[12:15]
	v_mfma_f32_16x16x32_bf16 v[8:11], v[172:175], v[212:215], v[8:11]
	v_mfma_f32_16x16x32_bf16 v[4:7], v[164:167], v[220:223], v[4:7]
	v_mfma_f32_16x16x32_bf16 v[0:3], v[172:175], v[220:223], v[0:3]
	s_setprio 0
	s_setprio 1
	v_mfma_f32_16x16x32_bf16 v[52:55], v[176:179], v[192:195], v[52:55]
	v_mfma_f32_16x16x32_bf16 v[48:51], v[184:187], v[192:195], v[48:51]
	v_mfma_f32_16x16x32_bf16 v[28:31], v[176:179], v[200:203], v[28:31]
	v_mfma_f32_16x16x32_bf16 v[24:27], v[184:187], v[200:203], v[24:27]
	v_mfma_f32_16x16x32_bf16 v[36:39], v[176:179], v[208:211], v[36:39]
	v_mfma_f32_16x16x32_bf16 v[40:43], v[184:187], v[208:211], v[40:43]
	v_mfma_f32_16x16x32_bf16 v[16:19], v[176:179], v[216:219], v[16:19]
	v_mfma_f32_16x16x32_bf16 v[20:23], v[184:187], v[216:219], v[20:23]
	v_mfma_f32_16x16x32_bf16 v[52:55], v[180:183], v[196:199], v[52:55]
	v_mfma_f32_16x16x32_bf16 v[48:51], v[188:191], v[196:199], v[48:51]
	v_mfma_f32_16x16x32_bf16 v[28:31], v[180:183], v[204:207], v[28:31]
	v_mfma_f32_16x16x32_bf16 v[24:27], v[188:191], v[204:207], v[24:27]
	v_mfma_f32_16x16x32_bf16 v[36:39], v[180:183], v[212:215], v[36:39]
	v_mfma_f32_16x16x32_bf16 v[40:43], v[188:191], v[212:215], v[40:43]
	v_mfma_f32_16x16x32_bf16 v[16:19], v[180:183], v[220:223], v[16:19]
	v_mfma_f32_16x16x32_bf16 v[20:23], v[188:191], v[220:223], v[20:23]
	s_setprio 0
	s_barrier
	s_mov_b32 m0, s43
	v_lshl_add_u64 v[160:161], v[224:225], 0, s[16:17]
	global_load_lds_dwordx4 v[160:161], off
	v_lshl_add_u64 v[160:161], v[228:229], 0, s[16:17]
	s_mov_b32 m0, s46
	s_add_i32 s68, s68, 2
	global_load_lds_dwordx4 v[160:161], off
	s_add_u32 s26, s26, 0x100
	s_addc_u32 s27, s27, 0
	s_cmp_gt_u32 s68, 13
	s_cbranch_scc0 .LBB0_1033
	s_and_b64 vcc, exec, s[40:41]
	s_cbranch_vccz .LBB0_1036
	s_barrier

; #define PG8_STAGE(bufoff, gbase, voff) do { _Pragma("unroll") for (int _i = 0; _i < 2; ++_i) \
;         __builtin_amdgcn_global_load_lds((const unsigned*)((const char*)(gbase) + (voff)[_i]), (LAS unsigned*)(lds + (bufoff) + ldsw + _i * 8192), 16, 0, 0); } while (0)
; #define PG8_WAIT_V(n) asm volatile("s_waitcnt vmcnt(" #n ")" ::: "memory")
; #define PG8_BAR __builtin_amdgcn_s_barrier()
; #define PG8_STAGE_A(bufoff, ptr_dense, half, ktoff, goffs) do { if constexpr (GATHER) { PG8_STAGE(bufoff, (const char*)A + (ktoff), goffs); } \
;         else { PG8_STAGE(bufoff, (ptr_dense) + (half) * hstepA, voffA); } } while (0)
; template <class Epi, class Sched, bool GATHER>
; __device__ __forceinline__ void gemm_phase(LAS unsigned char* lds, const int wid, const bf16_t* A, int lda, const bf16_t* Bt, int ldb, size_t b_estride, int K, const Sched& S, const Epi& E) {
;     ...
;     for (int i = 0; i < 2; ++i) { int R, C; stage_rc(tid * 16 + i * 8192, R, C); const int Rb = Epi::PERM ? ((R & ~31) + perm32(R & 31)) : R;
;         RA[i] = R; CA[i] = C; voffA[i] = (unsigned)(R * lda + C) * 2u; voffB[i] = (unsigned)(Rb * ldb + C) * 2u; }
;     const size_t kstep = (size_t)(BK * 2);
;     const size_t hstepA = (size_t)HALF * lda * 2, hstepB = (size_t)HALF * ldb * 2;
;     const size_t tstepA = 2 * hstepA, tstepB = 2 * hstepB;
;     const unsigned ldsw = (unsigned)wid * 1024u;
;     const int aoff = lds_byte(wr * 64 + fr, fq * 8), boff = lds_byte(wc * 32 + fr, fq * 8);
;     ...
;     PG8_STAGE(PG8_SB(0, 0), cB, voffB); PG8_STAGE(PG8_SB(0, 1), cB + hstepB, voffB); PG8_STAGE_A(PG8_SA(0, 0), cA, 0, 0, gc0); PG8_STAGE_A(PG8_SA(0, 1), cA, 1, 0, gc1);
;     if (wr == 1) PG8_BAR;
;     PG8_WAIT_V(2); PG8_BAR;
;     PG8_STAGE(PG8_SB(1, 0), cB + kstep, voffB); PG8_STAGE_A(PG8_SA(1, 0), cA + kstep, 0, kstep, gc0); PG8_STAGE(PG8_SB(1, 1), cB + hstepB + kstep, voffB); PG8_STAGE_A(PG8_SA(1, 1), cA + kstep, 1, kstep, gc1);
;     PG8_WAIT_V(8); PG8_BAR;
.LBB0_1194:
	s_add_u32 s2, s38, 0x19000000
	s_mov_b64 s[8:9], 0x80
	s_addc_u32 s3, s39, 0
	v_lshl_add_u64 v[6:7], v[6:7], 0, s[8:9]
	s_add_i32 m0, s43, 0x18000
	s_waitcnt vmcnt(2)
	s_barrier
	global_load_lds_dwordx4 v[6:7], off
	v_lshl_add_u64 v[4:5], v[4:5], 0, s[8:9]
	s_add_i32 m0, s43, 0x1a000
	s_add_i32 s38, s43, 0x8000
	s_add_i32 s39, s43, 0xa000
	global_load_lds_dwordx4 v[4:5], off
	v_lshl_add_u64 v[2:3], v[2:3], 0, s[8:9]
	s_mov_b32 m0, s38
	s_add_u32 s4, s26, 0x20080
	global_load_lds_dwordx4 v[2:3], off
	v_lshl_add_u64 v[0:1], v[0:1], 0, s[8:9]
	s_mov_b32 m0, s39
	s_addc_u32 s5, s27, 0
	global_load_lds_dwordx4 v[0:1], off
	s_add_i32 m0, s43, 0x1c000
	v_and_b32_e32 v4, 48, v8
	global_load_lds_dwordx4 v130, s[4:5]
	s_add_i32 m0, s43, 0x1e000
	v_lshl_add_u64 v[0:1], s[4:5], 0, v[134:135]
	s_add_u32 s4, s28, 0x20080
	s_addc_u32 s5, s29, 0
	s_add_i32 s47, s43, 0xc000
	global_load_lds_dwordx4 v[0:1], off
	s_mov_b32 m0, s47
	s_add_i32 s51, s43, 0xe000
	global_load_lds_dwordx4 v128, s[4:5]
	v_lshl_add_u64 v[0:1], s[4:5], 0, v[132:133]
	s_mov_b32 m0, s51
	s_movk_i32 s4, 0x3c0
	global_load_lds_dwordx4 v[0:1], off
	v_and_b32_e32 v0, 15, v8
	v_or_b32_e32 v1, s1, v0
	v_lshlrev_b32_e32 v3, 6, v1
	v_ashrrev_i32_e32 v2, 6, v8
	v_and_or_b32 v3, v3, s4, v4
	v_readlane_b32 s4, v248, 14
	v_lshlrev_b32_e32 v1, 2, v1
	v_and_b32_e32 v1, 32, v1
	v_lshl_add_u32 v5, v2, 10, s4
	v_bitop3_b32 v1, v3, v5, v1 bitop3:0xde
	v_readlane_b32 s4, v248, 15
	v_lshlrev_b32_e32 v3, 2, v8
	v_lshl_or_b32 v0, v0, 6, v4
	v_add_lshl_u32 v2, v2, s4, 10
	v_and_b32_e32 v3, 32, v3
	s_waitcnt vmcnt(8)
	v_bitop3_b32 v159, v0, v2, v3 bitop3:0xde
	s_add_i32 s52, 0, 0x10000
	s_add_i32 s53, 0, 0x14000
	v_add_u32_e32 v165, s52, v159
	v_add_u32_e32 v170, s53, v159
	v_add_u32_e32 v171, 0, v1
	s_add_i32 s56, 0, 0x20000
	s_add_i32 s58, 0, 0x23c00
	s_mov_b32 s11, 0
	s_mov_b32 s24, 0
	s_mov_b32 s22, 0
	s_barrier
	s_branch .LBB0_1197

; #define PG8_STAGE(bufoff, gbase, voff) do { _Pragma("unroll") for (int _i = 0; _i < 2; ++_i) \
;         __builtin_amdgcn_global_load_lds((const unsigned*)((const char*)(gbase) + (voff)[_i]), (LAS unsigned*)(lds + (bufoff) + ldsw + _i * 8192), 16, 0, 0); } while (0)
; #define PG8_LDA(dst, b, h) do { _Pragma("unroll") for (int m = 0; m < 4; ++m) _Pragma("unroll") for (int k = 0; k < 2; ++k) dst[m][k] = *(const LAS bf16x8*)(lds + PG8_SA(b, h) + aoff + m * 2048 + k * 1024); } while (0)
; #define PG8_LDB(dst, b, h) do { _Pragma("unroll") for (int n = 0; n < 2; ++n) _Pragma("unroll") for (int k = 0; k < 2; ++k) dst[n][k] = *(const LAS bf16x8*)(lds + PG8_SB(b, h) + boff + n * 2048 + k * 1024); } while (0)
; #define PG8_MMA(ai, bj, At, Bt_) do { __builtin_amdgcn_s_setprio(1); _Pragma("unroll") for (int m = 0; m < 4; ++m) _Pragma("unroll") for (int n = 0; n < 2; ++n) _Pragma("unroll") for (int k = 0; k < 2; ++k) \
;         acc[ai][bj][m][n] = __builtin_amdgcn_mfma_f32_16x16x32_bf16(Bt_[n][k], At[m][k], acc[ai][bj][m][n], 0, 0, 0); __builtin_amdgcn_s_setprio(0); } while (0)
; #define PG8_WAIT_L(n) asm volatile("s_waitcnt lgkmcnt(" #n ")" ::: "memory")
; #define PG8_WAIT_VR(rl) asm volatile("s_cmp_lg_u32 %0, 0\n\ts_cbranch_scc1 .Lwvr%=\n\ts_waitcnt vmcnt(8)\n.Lwvr%=:\n\ts_waitcnt vmcnt(24)" :: "s"(rl) : "scc", "memory")
; #define PG8_BAR __builtin_amdgcn_s_barrier()
; #define PG8_SCHED __builtin_amdgcn_sched_barrier(0)
; template <class Epi, class Sched, bool GATHER>
; __device__ __forceinline__ void gemm_phase(LAS unsigned char* lds, const int wid, const bf16_t* A, int lda, const bf16_t* Bt, int ldb, size_t b_estride, int K, const Sched& S, const Epi& E) {
;     ...
;             PG8_WAIT_VR(rl); PG8_WAIT_L(0); PG8_BAR; PG8_MMA(0, 0, At, B0); PG8_MMA(0, 1, At, B1); PG8_BAR; PG8_SCHED;
;             PG8_LDA(At, 0, 1); PG8_STAGE(PG8_SB(0, 0), b2, voffB); PG8_STAGE(PG8_SB(0, 1), b2 + hstepB, voffB); PG8_STAGE_A(PG8_SA(0, 0), a2, 0, k2, g20);
;             PG8_WAIT_VR(rl); PG8_WAIT_L(0); PG8_BAR; PG8_MMA(1, 0, At, B0); PG8_MMA(1, 1, At, B1); PG8_BAR; PG8_SCHED;
;             PG8_LDB(B0, 1, 0); PG8_LDB(B1, 1, 1); PG8_SCHED; PG8_LDA(At, 1, 0); PG8_STAGE_A(PG8_SA(0, 1), a2, 1, k2, g21);
;             PG8_WAIT_VR(rl); PG8_WAIT_L(0); PG8_BAR; PG8_MMA(0, 0, At, B0); PG8_MMA(0, 1, At, B1); PG8_BAR; PG8_SCHED;
.Lwvr15:
	s_waitcnt vmcnt(24)
	s_waitcnt lgkmcnt(0)
	s_barrier
	s_setprio 1
	s_waitcnt lgkmcnt(0)
	v_mfma_f32_16x16x32_bf16 v[124:127], v[144:147], v[192:195], v[124:127]
	v_mfma_f32_16x16x32_bf16 v[120:123], v[166:169], v[192:195], v[120:123]
	v_mfma_f32_16x16x32_bf16 v[108:111], v[144:147], v[200:203], v[108:111]
	v_mfma_f32_16x16x32_bf16 v[104:107], v[166:169], v[200:203], v[104:107]
	v_mfma_f32_16x16x32_bf16 v[92:95], v[144:147], v[208:211], v[92:95]
	v_mfma_f32_16x16x32_bf16 v[88:91], v[166:169], v[208:211], v[88:91]
	v_mfma_f32_16x16x32_bf16 v[76:79], v[144:147], v[216:219], v[76:79]
	v_mfma_f32_16x16x32_bf16 v[72:75], v[166:169], v[216:219], v[72:75]
	v_mfma_f32_16x16x32_bf16 v[124:127], v[160:163], v[196:199], v[124:127]
	v_mfma_f32_16x16x32_bf16 v[120:123], v[172:175], v[196:199], v[120:123]
	v_mfma_f32_16x16x32_bf16 v[108:111], v[160:163], v[204:207], v[108:111]
	v_mfma_f32_16x16x32_bf16 v[104:107], v[172:175], v[204:207], v[104:107]
	v_mfma_f32_16x16x32_bf16 v[92:95], v[160:163], v[212:215], v[92:95]
	v_mfma_f32_16x16x32_bf16 v[88:91], v[172:175], v[212:215], v[88:91]
	v_mfma_f32_16x16x32_bf16 v[76:79], v[160:163], v[220:223], v[76:79]
	v_mfma_f32_16x16x32_bf16 v[72:75], v[172:175], v[220:223], v[72:75]
	s_setprio 0
	s_setprio 1
	v_mfma_f32_16x16x32_bf16 v[116:119], v[176:179], v[192:195], v[116:119]
	v_mfma_f32_16x16x32_bf16 v[112:115], v[184:187], v[192:195], v[112:115]
	v_mfma_f32_16x16x32_bf16 v[100:103], v[176:179], v[200:203], v[100:103]
	v_mfma_f32_16x16x32_bf16 v[96:99], v[184:187], v[200:203], v[96:99]
	v_mfma_f32_16x16x32_bf16 v[84:87], v[176:179], v[208:211], v[84:87]
	v_mfma_f32_16x16x32_bf16 v[80:83], v[184:187], v[208:211], v[80:83]
	v_mfma_f32_16x16x32_bf16 v[68:71], v[176:179], v[216:219], v[68:71]
	v_mfma_f32_16x16x32_bf16 v[64:67], v[184:187], v[216:219], v[64:67]
	v_mfma_f32_16x16x32_bf16 v[116:119], v[180:183], v[196:199], v[116:119]
	v_mfma_f32_16x16x32_bf16 v[112:115], v[188:191], v[196:199], v[112:115]
	v_mfma_f32_16x16x32_bf16 v[100:103], v[180:183], v[204:207], v[100:103]
	v_mfma_f32_16x16x32_bf16 v[96:99], v[188:191], v[204:207], v[96:99]
	v_mfma_f32_16x16x32_bf16 v[84:87], v[180:183], v[212:215], v[84:87]
	v_mfma_f32_16x16x32_bf16 v[80:83], v[188:191], v[212:215], v[80:83]
	v_mfma_f32_16x16x32_bf16 v[68:71], v[180:183], v[220:223], v[68:71]
	v_mfma_f32_16x16x32_bf16 v[64:67], v[188:191], v[220:223], v[64:67]
	s_setprio 0
	s_barrier
	s_add_i32 s72, s52, s33
	v_lshl_add_u64 v[136:137], s[28:29], 0, v[130:131]
	s_mov_b32 m0, s72
	ds_read_b128 v[192:195], v171 offset:16384
	ds_read_b128 v[196:199], v171 offset:17408
	ds_read_b128 v[200:203], v171 offset:18432
	ds_read_b128 v[204:207], v171 offset:19456
	ds_read_b128 v[208:211], v171 offset:20480
	ds_read_b128 v[212:215], v171 offset:21504
	ds_read_b128 v[216:219], v171 offset:22528
	ds_read_b128 v[220:223], v171 offset:23552
	global_load_lds_dwordx4 v[136:137], off
	s_add_i32 m0, s72, 0x2000
	s_add_u32 s72, s28, 0x20000
	v_lshl_add_u64 v[140:141], s[28:29], 0, v[134:135]
	s_addc_u32 s73, s29, 0
	s_add_i32 s74, s53, s33
	global_load_lds_dwordx4 v[140:141], off
	s_mov_b32 m0, s74
	v_lshl_add_u64 v[152:153], s[26:27], 0, v[132:133]
	global_load_lds_dwordx4 v130, s[72:73]
	s_add_i32 m0, s74, 0x2000
	s_nop 0
	global_load_lds_dwordx4 v134, s[72:73]
	v_lshl_add_u64 v[148:149], s[26:27], 0, v[128:129]
	s_mov_b32 m0, s43
	s_nop 0
	global_load_lds_dwordx4 v[148:149], off
	s_mov_b32 m0, s44
	s_nop 0
	global_load_lds_dwordx4 v[152:153], off
	s_cmp_lg_u32 s71, 0
	s_cbranch_scc1 .Lwvr16
	s_waitcnt vmcnt(8)
.Lwvr16:
	s_waitcnt vmcnt(24)
	s_waitcnt lgkmcnt(0)
	s_barrier
	s_setprio 1
	s_waitcnt lgkmcnt(0)
	v_mfma_f32_16x16x32_bf16 v[60:63], v[144:147], v[192:195], v[60:63]
	v_mfma_f32_16x16x32_bf16 v[56:59], v[166:169], v[192:195], v[56:59]
	v_mfma_f32_16x16x32_bf16 v[44:47], v[144:147], v[200:203], v[44:47]
	v_mfma_f32_16x16x32_bf16 v[40:43], v[166:169], v[200:203], v[40:43]
	v_mfma_f32_16x16x32_bf16 v[28:31], v[144:147], v[208:211], v[28:31]
	v_mfma_f32_16x16x32_bf16 v[24:27], v[166:169], v[208:211], v[24:27]
	v_mfma_f32_16x16x32_bf16 v[12:15], v[144:147], v[216:219], v[12:15]
	v_mfma_f32_16x16x32_bf16 v[8:11], v[166:169], v[216:219], v[8:11]
	v_mfma_f32_16x16x32_bf16 v[60:63], v[160:163], v[196:199], v[60:63]
	v_mfma_f32_16x16x32_bf16 v[56:59], v[172:175], v[196:199], v[56:59]
	v_mfma_f32_16x16x32_bf16 v[44:47], v[160:163], v[204:207], v[44:47]
	v_mfma_f32_16x16x32_bf16 v[40:43], v[172:175], v[204:207], v[40:43]
	v_mfma_f32_16x16x32_bf16 v[28:31], v[160:163], v[212:215], v[28:31]
	v_mfma_f32_16x16x32_bf16 v[24:27], v[172:175], v[212:215], v[24:27]
	v_mfma_f32_16x16x32_bf16 v[12:15], v[160:163], v[220:223], v[12:15]
	v_mfma_f32_16x16x32_bf16 v[8:11], v[172:175], v[220:223], v[8:11]
	s_setprio 0
	s_setprio 1
	v_mfma_f32_16x16x32_bf16 v[52:55], v[176:179], v[192:195], v[52:55]
	v_mfma_f32_16x16x32_bf16 v[48:51], v[184:187], v[192:195], v[48:51]
	v_mfma_f32_16x16x32_bf16 v[36:39], v[176:179], v[200:203], v[36:39]
	v_mfma_f32_16x16x32_bf16 v[32:35], v[184:187], v[200:203], v[32:35]
	v_mfma_f32_16x16x32_bf16 v[20:23], v[176:179], v[208:211], v[20:23]
	v_mfma_f32_16x16x32_bf16 v[16:19], v[184:187], v[208:211], v[16:19]
	v_mfma_f32_16x16x32_bf16 v[4:7], v[176:179], v[216:219], v[4:7]
	v_mfma_f32_16x16x32_bf16 v[0:3], v[184:187], v[216:219], v[0:3]
	v_mfma_f32_16x16x32_bf16 v[52:55], v[180:183], v[196:199], v[52:55]
	v_mfma_f32_16x16x32_bf16 v[48:51], v[188:191], v[196:199], v[48:51]
	v_mfma_f32_16x16x32_bf16 v[36:39], v[180:183], v[204:207], v[36:39]
	v_mfma_f32_16x16x32_bf16 v[32:35], v[188:191], v[204:207], v[32:35]
	v_mfma_f32_16x16x32_bf16 v[20:23], v[180:183], v[212:215], v[20:23]
	v_mfma_f32_16x16x32_bf16 v[16:19], v[188:191], v[212:215], v[16:19]
	v_mfma_f32_16x16x32_bf16 v[4:7], v[180:183], v[220:223], v[4:7]
	v_mfma_f32_16x16x32_bf16 v[0:3], v[188:191], v[220:223], v[0:3]
	s_setprio 0
	s_barrier
	s_add_i32 s74, 0, 0x18000
	v_add_u32_e32 v138, s74, v159
	s_add_i32 s75, 0, 0x1c000
	ds_read_b128 v[144:147], v138
	ds_read_b128 v[160:163], v138 offset:1024
	ds_read_b128 v[166:169], v138 offset:2048
	ds_read_b128 v[172:175], v138 offset:3072
	v_add_u32_e32 v138, s75, v159
	ds_read_b128 v[176:179], v138
	ds_read_b128 v[180:183], v138 offset:1024
	ds_read_b128 v[184:187], v138 offset:2048
	ds_read_b128 v[188:191], v138 offset:3072
	s_add_u32 s72, s26, 0x20000
	s_addc_u32 s73, s27, 0
	s_mov_b32 m0, s45
	ds_read_b128 v[192:195], v171 offset:32768
	ds_read_b128 v[196:199], v171 offset:33792
	ds_read_b128 v[200:203], v171 offset:34816
	ds_read_b128 v[204:207], v171 offset:35840
	ds_read_b128 v[208:211], v171 offset:36864
	ds_read_b128 v[212:215], v171 offset:37888
	ds_read_b128 v[216:219], v171 offset:38912
	ds_read_b128 v[220:223], v171 offset:39936
	global_load_lds_dwordx4 v128, s[72:73]
	s_mov_b32 m0, s46
	s_nop 0
	global_load_lds_dwordx4 v132, s[72:73]
	s_cmp_lg_u32 s71, 0
	s_cbranch_scc1 .Lwvr17
	s_waitcnt vmcnt(8)
; #define PG8_STAGE(bufoff, gbase, voff) do { _Pragma("unroll") for (int _i = 0; _i < 2; ++_i) \
;         __builtin_amdgcn_global_load_lds((const unsigned*)((const char*)(gbase) + (voff)[_i]), (LAS unsigned*)(lds + (bufoff) + ldsw + _i * 8192), 16, 0, 0); } while (0)
; #define PG8_LDA(dst, b, h) do { _Pragma("unroll") for (int m = 0; m < 4; ++m) _Pragma("unroll") for (int k = 0; k < 2; ++k) dst[m][k] = *(const LAS bf16x8*)(lds + PG8_SA(b, h) + aoff + m * 2048 + k * 1024); } while (0)
; #define PG8_MMA(ai, bj, At, Bt_) do { __builtin_amdgcn_s_setprio(1); _Pragma("unroll") for (int m = 0; m < 4; ++m) _Pragma("unroll") for (int n = 0; n < 2; ++n) _Pragma("unroll") for (int k = 0; k < 2; ++k) \
;         acc[ai][bj][m][n] = __builtin_amdgcn_mfma_f32_16x16x32_bf16(Bt_[n][k], At[m][k], acc[ai][bj][m][n], 0, 0, 0); __builtin_amdgcn_s_setprio(0); } while (0)
; #define PG8_WAIT_V(n) asm volatile("s_waitcnt vmcnt(" #n ")" ::: "memory")
; #define PG8_WAIT_L(n) asm volatile("s_waitcnt lgkmcnt(" #n ")" ::: "memory")
; #define PG8_WAIT_VR(rl) asm volatile("s_cmp_lg_u32 %0, 0\n\ts_cbranch_scc1 .Lwvr%=\n\ts_waitcnt vmcnt(8)\n.Lwvr%=:\n\ts_waitcnt vmcnt(24)" :: "s"(rl) : "scc", "memory")
; #define PG8_BAR __builtin_amdgcn_s_barrier()
; #define PG8_SCHED __builtin_amdgcn_sched_barrier(0)
; #define PG8_STAGE_A(bufoff, ptr_dense, half, ktoff, goffs) do { if constexpr (GATHER) { PG8_STAGE(bufoff, (const char*)A + (ktoff), goffs); } \
;         else { PG8_STAGE(bufoff, (ptr_dense) + (half) * hstepA, voffA); } } while (0)
; template <class Epi, class Sched, bool GATHER>
; __device__ __forceinline__ void gemm_phase(LAS unsigned char* lds, const int wid, const bf16_t* A, int lda, const bf16_t* Bt, int ldb, size_t b_estride, int K, const Sched& S, const Epi& E) {
;     ...
;             PG8_WAIT_VR(rl); PG8_WAIT_L(0); PG8_BAR; PG8_MMA(0, 0, At, B0); PG8_MMA(0, 1, At, B1); PG8_BAR; PG8_SCHED;
;             PG8_LDA(At, 1, 1); PG8_STAGE(PG8_SB(1, 0), b3, voffB); PG8_STAGE(PG8_SB(1, 1), b3 + hstepB, voffB); PG8_STAGE_A(PG8_SA(1, 0), a3, 0, k3, g20);
;             PG8_WAIT_V(8); PG8_WAIT_L(0); PG8_BAR; PG8_MMA(1, 0, At, B0); PG8_MMA(1, 1, At, B1); PG8_BAR; PG8_SCHED;
;             PG8_STAGE_A(PG8_SA(1, 1), a3, 1, k3, g21);
;         }
.Lwvr17:
	s_waitcnt vmcnt(24)
	s_waitcnt lgkmcnt(0)
	s_barrier
	s_setprio 1
	s_waitcnt lgkmcnt(0)
	v_mfma_f32_16x16x32_bf16 v[124:127], v[144:147], v[192:195], v[124:127]
	v_mfma_f32_16x16x32_bf16 v[120:123], v[166:169], v[192:195], v[120:123]
	v_mfma_f32_16x16x32_bf16 v[108:111], v[144:147], v[200:203], v[108:111]
	v_mfma_f32_16x16x32_bf16 v[104:107], v[166:169], v[200:203], v[104:107]
	v_mfma_f32_16x16x32_bf16 v[92:95], v[144:147], v[208:211], v[92:95]
	v_mfma_f32_16x16x32_bf16 v[88:91], v[166:169], v[208:211], v[88:91]
	v_mfma_f32_16x16x32_bf16 v[76:79], v[144:147], v[216:219], v[76:79]
	v_mfma_f32_16x16x32_bf16 v[72:75], v[166:169], v[216:219], v[72:75]
	v_mfma_f32_16x16x32_bf16 v[124:127], v[160:163], v[196:199], v[124:127]
	v_mfma_f32_16x16x32_bf16 v[120:123], v[172:175], v[196:199], v[120:123]
	v_mfma_f32_16x16x32_bf16 v[108:111], v[160:163], v[204:207], v[108:111]
	v_mfma_f32_16x16x32_bf16 v[104:107], v[172:175], v[204:207], v[104:107]
	v_mfma_f32_16x16x32_bf16 v[92:95], v[160:163], v[212:215], v[92:95]
	v_mfma_f32_16x16x32_bf16 v[88:91], v[172:175], v[212:215], v[88:91]
	v_mfma_f32_16x16x32_bf16 v[76:79], v[160:163], v[220:223], v[76:79]
	v_mfma_f32_16x16x32_bf16 v[72:75], v[172:175], v[220:223], v[72:75]
	s_setprio 0
	s_setprio 1
	v_mfma_f32_16x16x32_bf16 v[116:119], v[176:179], v[192:195], v[116:119]
	v_mfma_f32_16x16x32_bf16 v[112:115], v[184:187], v[192:195], v[112:115]
	v_mfma_f32_16x16x32_bf16 v[100:103], v[176:179], v[200:203], v[100:103]
	v_mfma_f32_16x16x32_bf16 v[96:99], v[184:187], v[200:203], v[96:99]
	v_mfma_f32_16x16x32_bf16 v[84:87], v[176:179], v[208:211], v[84:87]
	v_mfma_f32_16x16x32_bf16 v[80:83], v[184:187], v[208:211], v[80:83]
	v_mfma_f32_16x16x32_bf16 v[68:71], v[176:179], v[216:219], v[68:71]
	v_mfma_f32_16x16x32_bf16 v[64:67], v[184:187], v[216:219], v[64:67]
	v_mfma_f32_16x16x32_bf16 v[116:119], v[180:183], v[196:199], v[116:119]
	v_mfma_f32_16x16x32_bf16 v[112:115], v[188:191], v[196:199], v[112:115]
	v_mfma_f32_16x16x32_bf16 v[100:103], v[180:183], v[204:207], v[100:103]
	v_mfma_f32_16x16x32_bf16 v[96:99], v[188:191], v[204:207], v[96:99]
	v_mfma_f32_16x16x32_bf16 v[84:87], v[180:183], v[212:215], v[84:87]
	v_mfma_f32_16x16x32_bf16 v[80:83], v[188:191], v[212:215], v[80:83]
	v_mfma_f32_16x16x32_bf16 v[68:71], v[180:183], v[220:223], v[68:71]
	v_mfma_f32_16x16x32_bf16 v[64:67], v[188:191], v[220:223], v[64:67]
	s_setprio 0
	s_barrier
	s_add_i32 s71, s74, s33
	v_lshl_add_u64 v[136:137], v[136:137], 0, s[8:9]
	s_mov_b32 m0, s71
	ds_read_b128 v[192:195], v171 offset:49152
	ds_read_b128 v[196:199], v171 offset:50176
	ds_read_b128 v[200:203], v171 offset:51200
	ds_read_b128 v[204:207], v171 offset:52224
	ds_read_b128 v[208:211], v171 offset:53248
	ds_read_b128 v[212:215], v171 offset:54272
	ds_read_b128 v[216:219], v171 offset:55296
	ds_read_b128 v[220:223], v171 offset:56320
	global_load_lds_dwordx4 v[136:137], off
	s_add_i32 m0, s71, 0x2000
	s_add_u32 s28, s28, 0x20080
	v_lshl_add_u64 v[136:137], v[140:141], 0, s[8:9]
	s_addc_u32 s29, s29, 0
	s_add_i32 s71, s75, s33
	global_load_lds_dwordx4 v[136:137], off
	s_mov_b32 m0, s71
	s_nop 0
	global_load_lds_dwordx4 v130, s[28:29]
	s_add_i32 m0, s71, 0x2000
	s_nop 0
	global_load_lds_dwordx4 v134, s[28:29]
	v_lshl_add_u64 v[136:137], v[148:149], 0, s[8:9]
	s_mov_b32 m0, s38
	s_nop 0
	global_load_lds_dwordx4 v[136:137], off
	v_lshl_add_u64 v[136:137], v[152:153], 0, s[8:9]
	s_mov_b32 m0, s39
	s_nop 0
	global_load_lds_dwordx4 v[136:137], off
	s_waitcnt vmcnt(8)
	s_waitcnt lgkmcnt(0)
	s_barrier
	s_setprio 1
	s_waitcnt lgkmcnt(0)
	v_mfma_f32_16x16x32_bf16 v[60:63], v[144:147], v[192:195], v[60:63]
	v_mfma_f32_16x16x32_bf16 v[56:59], v[166:169], v[192:195], v[56:59]
	v_mfma_f32_16x16x32_bf16 v[44:47], v[144:147], v[200:203], v[44:47]
	v_mfma_f32_16x16x32_bf16 v[40:43], v[166:169], v[200:203], v[40:43]
	v_mfma_f32_16x16x32_bf16 v[28:31], v[144:147], v[208:211], v[28:31]
	v_mfma_f32_16x16x32_bf16 v[24:27], v[166:169], v[208:211], v[24:27]
	v_mfma_f32_16x16x32_bf16 v[12:15], v[144:147], v[216:219], v[12:15]
	v_mfma_f32_16x16x32_bf16 v[8:11], v[166:169], v[216:219], v[8:11]
	v_mfma_f32_16x16x32_bf16 v[60:63], v[160:163], v[196:199], v[60:63]
	v_mfma_f32_16x16x32_bf16 v[56:59], v[172:175], v[196:199], v[56:59]
	v_mfma_f32_16x16x32_bf16 v[44:47], v[160:163], v[204:207], v[44:47]
	v_mfma_f32_16x16x32_bf16 v[40:43], v[172:175], v[204:207], v[40:43]
	v_mfma_f32_16x16x32_bf16 v[28:31], v[160:163], v[212:215], v[28:31]
	v_mfma_f32_16x16x32_bf16 v[24:27], v[172:175], v[212:215], v[24:27]
	v_mfma_f32_16x16x32_bf16 v[12:15], v[160:163], v[220:223], v[12:15]
	v_mfma_f32_16x16x32_bf16 v[8:11], v[172:175], v[220:223], v[8:11]
	s_setprio 0
	s_setprio 1
	v_mfma_f32_16x16x32_bf16 v[52:55], v[176:179], v[192:195], v[52:55]
	v_mfma_f32_16x16x32_bf16 v[48:51], v[184:187], v[192:195], v[48:51]
	v_mfma_f32_16x16x32_bf16 v[36:39], v[176:179], v[200:203], v[36:39]
	v_mfma_f32_16x16x32_bf16 v[32:35], v[184:187], v[200:203], v[32:35]
	v_mfma_f32_16x16x32_bf16 v[20:23], v[176:179], v[208:211], v[20:23]
	v_mfma_f32_16x16x32_bf16 v[16:19], v[184:187], v[208:211], v[16:19]
	v_mfma_f32_16x16x32_bf16 v[4:7], v[176:179], v[216:219], v[4:7]
	v_mfma_f32_16x16x32_bf16 v[0:3], v[184:187], v[216:219], v[0:3]
	v_mfma_f32_16x16x32_bf16 v[52:55], v[180:183], v[196:199], v[52:55]
	v_mfma_f32_16x16x32_bf16 v[48:51], v[188:191], v[196:199], v[48:51]
	v_mfma_f32_16x16x32_bf16 v[36:39], v[180:183], v[204:207], v[36:39]
	v_mfma_f32_16x16x32_bf16 v[32:35], v[188:191], v[204:207], v[32:35]
	v_mfma_f32_16x16x32_bf16 v[20:23], v[180:183], v[212:215], v[20:23]
	v_mfma_f32_16x16x32_bf16 v[16:19], v[188:191], v[212:215], v[16:19]
	v_mfma_f32_16x16x32_bf16 v[4:7], v[180:183], v[220:223], v[4:7]
	v_mfma_f32_16x16x32_bf16 v[0:3], v[188:191], v[220:223], v[0:3]
	s_setprio 0
	s_barrier
	s_add_u32 s26, s26, 0x20080
	s_addc_u32 s27, s27, 0
	s_mov_b32 m0, s47
	s_nop 0
	global_load_lds_dwordx4 v128, s[26:27]
	s_mov_b32 m0, s51
	s_add_i32 s70, s70, 2
	global_load_lds_dwordx4 v132, s[26:27]
	s_add_u32 s66, s66, 0x100
	s_addc_u32 s67, s67, 0
	s_add_u32 s68, s68, 0x100
	s_addc_u32 s69, s69, 0
	s_cmp_gt_u32 s70, 5
	s_cbranch_scc0 .LBB0_1202
	s_and_b64 vcc, exec, s[40:41]
	s_cbranch_vccz .LBB0_1205
	s_barrier
